# MFMA issue order inside each independent group of 8 changed to a Gray-code walk (one operand changes per step) in all GEMM main loops
# speedup vs baseline: 1.0161x; 1.0058x over previous
.LBB0_261:
	s_nop 2
	ds_read_b128 v[0:3], v219
	ds_read_b128 v[4:7], v219 offset:1024
	ds_read_b128 v[8:11], v219 offset:2048
	ds_read_b128 v[12:15], v219 offset:3072
	ds_read_b128 v[16:19], v220
	ds_read_b128 v[20:23], v220 offset:1024
	ds_read_b128 v[24:27], v220 offset:2048
	ds_read_b128 v[28:31], v220 offset:3072
	s_add_u32 s8, s46, 0x100
	s_addc_u32 s9, s47, 0
	s_cmp_eq_u32 s76, 12
	s_cselect_b32 s52, s11, s8
	s_cselect_b32 s53, s7, s9
	s_cselect_b32 s48, s41, s77
	s_cselect_b32 s49, s39, s80
	s_add_u32 s12, s52, 0x80
	s_addc_u32 s13, s53, 0
	ds_read_b128 v[32:35], v221
	ds_read_b128 v[36:39], v221 offset:1024
	ds_read_b128 v[40:43], v221 offset:2048
	ds_read_b128 v[44:47], v221 offset:3072
	ds_read_b128 v[48:51], v221 offset:4096
	ds_read_b128 v[52:55], v221 offset:5120
	ds_read_b128 v[56:59], v221 offset:6144
	ds_read_b128 v[60:63], v221 offset:7168
	s_add_u32 s50, s48, 0x80
	s_addc_u32 s51, s49, 0
	s_add_u32 s46, s46, 0x40080
	s_addc_u32 s47, s47, 0
	s_add_i32 m0, s59, 0xc000
	s_nop 0
	global_load_lds_dwordx4 v215, s[46:47]
	s_nop 0
	s_add_i32 m0, s59, 0xe000
	s_nop 0
	global_load_lds_dwordx4 v217, s[46:47]
	s_waitcnt vmcnt(8)
	s_waitcnt lgkmcnt(0)
	s_barrier
	v_mfma_i32_16x16x64_i8 v[172:175], v[0:3], v[48:51], v[172:175]
	v_mfma_i32_16x16x64_i8 v[168:171], v[8:11], v[48:51], v[168:171]
	v_mfma_i32_16x16x64_i8 v[152:155], v[8:11], v[56:59], v[152:155]
	v_mfma_i32_16x16x64_i8 v[156:159], v[0:3], v[56:59], v[156:159]
	v_mfma_i32_16x16x64_i8 v[64:67], v[0:3], v[32:35], v[204:207]
	v_mfma_i32_16x16x64_i8 v[76:79], v[8:11], v[32:35], v[200:203]
	v_mfma_i32_16x16x64_i8 v[92:95], v[8:11], v[40:43], v[184:187]
	v_mfma_i32_16x16x64_i8 v[80:83], v[0:3], v[40:43], v[188:191]
	v_mfma_i32_16x16x64_i8 v[172:175], v[4:7], v[52:55], v[172:175]
	v_mfma_i32_16x16x64_i8 v[168:171], v[12:15], v[52:55], v[168:171]
	v_mfma_i32_16x16x64_i8 v[152:155], v[12:15], v[60:63], v[152:155]
	v_mfma_i32_16x16x64_i8 v[156:159], v[4:7], v[60:63], v[156:159]
	v_mfma_i32_16x16x64_i8 v[64:67], v[4:7], v[36:39], v[64:67]
	v_mfma_i32_16x16x64_i8 v[76:79], v[12:15], v[36:39], v[76:79]
	v_mfma_i32_16x16x64_i8 v[92:95], v[12:15], v[44:47], v[92:95]
	v_mfma_i32_16x16x64_i8 v[80:83], v[4:7], v[44:47], v[80:83]
	v_mfma_i32_16x16x64_i8 v[184:187], v[16:19], v[32:35], v[196:199]
	v_mfma_i32_16x16x64_i8 v[32:35], v[24:27], v[32:35], v[192:195]
	v_mfma_i32_16x16x64_i8 v[196:199], v[20:23], v[36:39], v[184:187]
	v_mfma_i32_16x16x64_i8 v[32:35], v[28:31], v[36:39], v[32:35]
	v_mfma_i32_16x16x64_i8 v[36:39], v[16:19], v[40:43], v[180:183]
	v_mfma_i32_16x16x64_i8 v[40:43], v[24:27], v[40:43], v[176:179]
	v_mfma_i32_16x16x64_i8 v[36:39], v[20:23], v[44:47], v[36:39]
	v_mfma_i32_16x16x64_i8 v[40:43], v[28:31], v[44:47], v[40:43]
	v_mfma_i32_16x16x64_i8 v[44:47], v[16:19], v[48:51], v[164:167]
	v_mfma_i32_16x16x64_i8 v[48:51], v[24:27], v[48:51], v[160:163]
	v_mfma_i32_16x16x64_i8 v[44:47], v[20:23], v[52:55], v[44:47]
	v_mfma_i32_16x16x64_i8 v[48:51], v[28:31], v[52:55], v[48:51]
	v_mfma_i32_16x16x64_i8 v[52:55], v[16:19], v[56:59], v[148:151]
	v_mfma_i32_16x16x64_i8 v[56:59], v[24:27], v[56:59], v[144:147]
	v_mfma_i32_16x16x64_i8 v[52:55], v[20:23], v[60:63], v[52:55]
	v_mfma_i32_16x16x64_i8 v[56:59], v[28:31], v[60:63], v[56:59]
	s_barrier
	ds_read_b128 v[60:63], v221 offset:16384
	ds_read_b128 v[144:147], v221 offset:17408
	ds_read_b128 v[148:151], v221 offset:18432
	ds_read_b128 v[160:163], v221 offset:19456
	ds_read_b128 v[164:167], v221 offset:20480
	ds_read_b128 v[176:179], v221 offset:21504
	ds_read_b128 v[180:183], v221 offset:22528
	ds_read_b128 v[184:187], v221 offset:23552
	s_add_i32 m0, s59, 0x10000
	s_nop 0
	global_load_lds_dwordx4 v216, s[48:49]
	s_nop 0
	s_add_i32 m0, s59, 0x12000
	s_nop 0
	global_load_lds_dwordx4 v218, s[48:49]
	s_add_u32 s46, s48, 0x40000
	s_addc_u32 s47, s49, 0
	s_add_i32 m0, s59, 0x14000
	s_nop 0
	global_load_lds_dwordx4 v216, s[46:47]
	s_nop 0
	s_add_i32 m0, s59, 0x16000
	s_nop 0
	global_load_lds_dwordx4 v218, s[46:47]
	s_nop 0
	s_add_i32 m0, s59, 0
	s_nop 0
	global_load_lds_dwordx4 v215, s[52:53]
	s_nop 0
	s_add_i32 m0, s59, 0x2000
	s_nop 0
	global_load_lds_dwordx4 v217, s[52:53]
	s_waitcnt vmcnt(8)
	s_waitcnt lgkmcnt(0)
	s_barrier
	v_mfma_i32_16x16x64_i8 v[140:143], v[0:3], v[60:63], v[140:143]
	v_mfma_i32_16x16x64_i8 v[124:127], v[0:3], v[148:151], v[124:127]
	v_mfma_i32_16x16x64_i8 v[108:111], v[0:3], v[164:167], v[108:111]
	v_mfma_i32_16x16x64_i8 v[0:3], v[0:3], v[180:183], v[88:91]
	v_mfma_i32_16x16x64_i8 v[136:139], v[8:11], v[60:63], v[136:139]
	v_mfma_i32_16x16x64_i8 v[120:123], v[8:11], v[148:151], v[120:123]
	v_mfma_i32_16x16x64_i8 v[104:107], v[8:11], v[164:167], v[104:107]
	v_mfma_i32_16x16x64_i8 v[88:91], v[4:7], v[184:187], v[0:3]
	v_mfma_i32_16x16x64_i8 v[0:3], v[8:11], v[180:183], v[84:87]
	v_mfma_i32_16x16x64_i8 v[140:143], v[4:7], v[144:147], v[140:143]
	v_mfma_i32_16x16x64_i8 v[136:139], v[12:15], v[144:147], v[136:139]
	v_mfma_i32_16x16x64_i8 v[124:127], v[4:7], v[160:163], v[124:127]
	v_mfma_i32_16x16x64_i8 v[120:123], v[12:15], v[160:163], v[120:123]
	v_mfma_i32_16x16x64_i8 v[108:111], v[4:7], v[176:179], v[108:111]
	v_mfma_i32_16x16x64_i8 v[104:107], v[12:15], v[176:179], v[104:107]
	v_mfma_i32_16x16x64_i8 v[84:87], v[12:15], v[184:187], v[0:3]
	v_mfma_i32_16x16x64_i8 v[0:3], v[16:19], v[60:63], v[132:135]
	v_mfma_i32_16x16x64_i8 v[132:135], v[20:23], v[144:147], v[0:3]
	v_mfma_i32_16x16x64_i8 v[0:3], v[24:27], v[60:63], v[128:131]
	v_mfma_i32_16x16x64_i8 v[128:131], v[28:31], v[144:147], v[0:3]
	v_mfma_i32_16x16x64_i8 v[0:3], v[16:19], v[148:151], v[116:119]
	v_mfma_i32_16x16x64_i8 v[116:119], v[20:23], v[160:163], v[0:3]
	v_mfma_i32_16x16x64_i8 v[0:3], v[24:27], v[148:151], v[112:115]
	v_mfma_i32_16x16x64_i8 v[112:115], v[28:31], v[160:163], v[0:3]
	v_mfma_i32_16x16x64_i8 v[0:3], v[16:19], v[164:167], v[100:103]
	v_mfma_i32_16x16x64_i8 v[100:103], v[20:23], v[176:179], v[0:3]
	v_mfma_i32_16x16x64_i8 v[0:3], v[24:27], v[164:167], v[96:99]
	v_mfma_i32_16x16x64_i8 v[96:99], v[28:31], v[176:179], v[0:3]
	v_mfma_i32_16x16x64_i8 v[0:3], v[16:19], v[180:183], v[72:75]
	v_mfma_i32_16x16x64_i8 v[72:75], v[20:23], v[184:187], v[0:3]
	v_mfma_i32_16x16x64_i8 v[0:3], v[24:27], v[180:183], v[68:71]
	v_mfma_i32_16x16x64_i8 v[68:71], v[28:31], v[184:187], v[0:3]
	s_barrier
	ds_read_b128 v[16:19], v222
	ds_read_b128 v[8:11], v222 offset:1024
	ds_read_b128 v[4:7], v222 offset:2048
	s_nop 1
	ds_read_b128 v[0:3], v222 offset:3072
	ds_read_b128 v[28:31], v223
	ds_read_b128 v[24:27], v223 offset:1024
	ds_read_b128 v[20:23], v223 offset:2048
	ds_read_b128 v[12:15], v223 offset:3072
	ds_read_b128 v[60:63], v221 offset:32768
	ds_read_b128 v[144:147], v221 offset:33792
	ds_read_b128 v[148:151], v221 offset:34816
	ds_read_b128 v[160:163], v221 offset:35840
	ds_read_b128 v[208:211], v221 offset:36864
	ds_read_b128 v[224:227], v221 offset:37888
	ds_read_b128 v[228:231], v221 offset:38912
	ds_read_b128 v[232:235], v221 offset:39936
	s_add_u32 s46, s52, 0x40000
	s_addc_u32 s47, s53, 0
	s_add_i32 m0, s59, 0x4000
	s_nop 0
	global_load_lds_dwordx4 v215, s[46:47]
	s_nop 0
	s_add_i32 m0, s59, 0x6000
	s_nop 0
	global_load_lds_dwordx4 v217, s[46:47]
	s_waitcnt vmcnt(8)
	s_waitcnt lgkmcnt(0)
	s_barrier
	v_mfma_i32_16x16x64_i8 v[64:67], v[16:19], v[60:63], v[64:67]
	v_mfma_i32_16x16x64_i8 v[204:207], v[8:11], v[144:147], v[64:67]
	v_mfma_i32_16x16x64_i8 v[64:67], v[4:7], v[60:63], v[76:79]
	v_mfma_i32_16x16x64_i8 v[200:203], v[0:3], v[144:147], v[64:67]
	v_mfma_i32_16x16x64_i8 v[64:67], v[16:19], v[148:151], v[80:83]
	v_mfma_i32_16x16x64_i8 v[188:191], v[8:11], v[160:163], v[64:67]
	v_mfma_i32_16x16x64_i8 v[64:67], v[4:7], v[148:151], v[92:95]
	v_mfma_i32_16x16x64_i8 v[184:187], v[0:3], v[160:163], v[64:67]
	v_mfma_i32_16x16x64_i8 v[64:67], v[16:19], v[208:211], v[172:175]
	v_mfma_i32_16x16x64_i8 v[172:175], v[8:11], v[224:227], v[64:67]
	v_mfma_i32_16x16x64_i8 v[64:67], v[4:7], v[208:211], v[168:171]
	v_mfma_i32_16x16x64_i8 v[168:171], v[0:3], v[224:227], v[64:67]
	v_mfma_i32_16x16x64_i8 v[64:67], v[16:19], v[228:231], v[156:159]
	v_mfma_i32_16x16x64_i8 v[156:159], v[8:11], v[232:235], v[64:67]
	v_mfma_i32_16x16x64_i8 v[64:67], v[4:7], v[228:231], v[152:155]
	v_mfma_i32_16x16x64_i8 v[152:155], v[0:3], v[232:235], v[64:67]
	v_mfma_i32_16x16x64_i8 v[32:35], v[20:23], v[60:63], v[32:35]
	v_mfma_i32_16x16x64_i8 v[192:195], v[12:15], v[144:147], v[32:35]
	v_mfma_i32_16x16x64_i8 v[32:35], v[28:31], v[148:151], v[36:39]
	v_mfma_i32_16x16x64_i8 v[180:183], v[24:27], v[160:163], v[32:35]
	v_mfma_i32_16x16x64_i8 v[32:35], v[20:23], v[148:151], v[40:43]
	v_mfma_i32_16x16x64_i8 v[176:179], v[12:15], v[160:163], v[32:35]
	v_mfma_i32_16x16x64_i8 v[32:35], v[28:31], v[208:211], v[44:47]
	v_mfma_i32_16x16x64_i8 v[164:167], v[24:27], v[224:227], v[32:35]
	v_mfma_i32_16x16x64_i8 v[32:35], v[20:23], v[208:211], v[48:51]
	v_mfma_i32_16x16x64_i8 v[160:163], v[12:15], v[224:227], v[32:35]
	v_mfma_i32_16x16x64_i8 v[32:35], v[28:31], v[228:231], v[52:55]
	v_mfma_i32_16x16x64_i8 v[64:67], v[28:31], v[60:63], v[196:199]
	v_mfma_i32_16x16x64_i8 v[148:151], v[24:27], v[232:235], v[32:35]
	v_mfma_i32_16x16x64_i8 v[32:35], v[20:23], v[228:231], v[56:59]
	v_mfma_i32_16x16x64_i8 v[196:199], v[24:27], v[144:147], v[64:67]
	v_mfma_i32_16x16x64_i8 v[144:147], v[12:15], v[232:235], v[32:35]
	s_barrier
	ds_read_b128 v[60:63], v221 offset:49152
	ds_read_b128 v[56:59], v221 offset:50176
	ds_read_b128 v[52:55], v221 offset:51200
	ds_read_b128 v[48:51], v221 offset:52224
	ds_read_b128 v[44:47], v221 offset:53248
	ds_read_b128 v[40:43], v221 offset:54272
	ds_read_b128 v[36:39], v221 offset:55296
	ds_read_b128 v[32:35], v221 offset:56320
	s_add_i32 m0, s59, 0x18000
	s_nop 0
	global_load_lds_dwordx4 v216, s[50:51]
	s_nop 0
	s_add_i32 m0, s59, 0x1a000
	s_nop 0
	global_load_lds_dwordx4 v218, s[50:51]
	s_add_u32 s46, s48, 0x40080
	s_addc_u32 s47, s49, 0
	s_add_i32 m0, s59, 0x1c000
	s_nop 0
	global_load_lds_dwordx4 v216, s[46:47]
	s_nop 0
	s_add_i32 m0, s59, 0x1e000
	s_nop 0
	global_load_lds_dwordx4 v218, s[46:47]
	s_nop 0
	s_add_i32 m0, s59, 0x8000
	s_nop 0
	global_load_lds_dwordx4 v215, s[12:13]
	s_nop 0
	s_add_i32 m0, s59, 0xa000
	s_nop 0
	global_load_lds_dwordx4 v217, s[12:13]
	s_waitcnt vmcnt(8)
	s_waitcnt lgkmcnt(0)
	s_barrier
	v_mfma_i32_16x16x64_i8 v[64:67], v[16:19], v[60:63], v[140:143]
	v_mfma_i32_16x16x64_i8 v[140:143], v[8:11], v[56:59], v[64:67]
	v_mfma_i32_16x16x64_i8 v[64:67], v[4:7], v[60:63], v[136:139]
	v_mfma_i32_16x16x64_i8 v[136:139], v[0:3], v[56:59], v[64:67]
	v_mfma_i32_16x16x64_i8 v[64:67], v[16:19], v[52:55], v[124:127]
	v_mfma_i32_16x16x64_i8 v[124:127], v[8:11], v[48:51], v[64:67]
	v_mfma_i32_16x16x64_i8 v[64:67], v[4:7], v[52:55], v[120:123]
	v_mfma_i32_16x16x64_i8 v[120:123], v[0:3], v[48:51], v[64:67]
	v_mfma_i32_16x16x64_i8 v[64:67], v[16:19], v[44:47], v[108:111]
	v_mfma_i32_16x16x64_i8 v[108:111], v[8:11], v[40:43], v[64:67]
	v_mfma_i32_16x16x64_i8 v[64:67], v[4:7], v[44:47], v[104:107]
	v_mfma_i32_16x16x64_i8 v[104:107], v[0:3], v[40:43], v[64:67]
	v_mfma_i32_16x16x64_i8 v[64:67], v[16:19], v[36:39], v[88:91]
	v_mfma_i32_16x16x64_i8 v[88:91], v[8:11], v[32:35], v[64:67]
	v_mfma_i32_16x16x64_i8 v[64:67], v[4:7], v[36:39], v[84:87]
	v_mfma_i32_16x16x64_i8 v[84:87], v[0:3], v[32:35], v[64:67]
	v_mfma_i32_16x16x64_i8 v[64:67], v[28:31], v[60:63], v[132:135]
	v_mfma_i32_16x16x64_i8 v[132:135], v[24:27], v[56:59], v[64:67]
	v_mfma_i32_16x16x64_i8 v[64:67], v[20:23], v[60:63], v[128:131]
	v_mfma_i32_16x16x64_i8 v[128:131], v[12:15], v[56:59], v[64:67]
	v_mfma_i32_16x16x64_i8 v[64:67], v[28:31], v[52:55], v[116:119]
	v_mfma_i32_16x16x64_i8 v[116:119], v[24:27], v[48:51], v[64:67]
	v_mfma_i32_16x16x64_i8 v[64:67], v[20:23], v[52:55], v[112:115]
	v_mfma_i32_16x16x64_i8 v[112:115], v[12:15], v[48:51], v[64:67]
	v_mfma_i32_16x16x64_i8 v[64:67], v[28:31], v[44:47], v[100:103]
	v_mfma_i32_16x16x64_i8 v[100:103], v[24:27], v[40:43], v[64:67]
	v_mfma_i32_16x16x64_i8 v[64:67], v[20:23], v[44:47], v[96:99]
	v_mfma_i32_16x16x64_i8 v[96:99], v[12:15], v[40:43], v[64:67]
	v_mfma_i32_16x16x64_i8 v[64:67], v[28:31], v[36:39], v[72:75]
	v_mfma_i32_16x16x64_i8 v[72:75], v[24:27], v[32:35], v[64:67]
	v_mfma_i32_16x16x64_i8 v[64:67], v[20:23], v[36:39], v[68:71]
	v_mfma_i32_16x16x64_i8 v[68:71], v[12:15], v[32:35], v[64:67]
	s_barrier
	s_add_i32 s76, s76, 2
	s_add_u32 s77, s77, 0x100
	s_addc_u32 s80, s80, 0
	s_cmp_gt_u32 s76, 13
	s_mov_b64 s[46:47], s[8:9]
	s_cbranch_scc0 .LBB0_261
	s_and_b64 vcc, exec, s[28:29]
	s_cbranch_vccz .LBB0_264
	s_barrier

.LBB0_603:
	ds_read_b128 v[100:103], v217
	ds_read_b128 v[108:111], v217 offset:1024
	ds_read_b128 v[116:119], v217 offset:2048
	ds_read_b128 v[124:127], v217 offset:3072
	ds_read_b128 v[132:135], v218
	ds_read_b128 v[140:143], v218 offset:1024
	ds_read_b128 v[148:151], v218 offset:2048
	ds_read_b128 v[156:159], v218 offset:3072
	s_add_u32 s30, s36, 0x100
	s_addc_u32 s31, s37, 0
	s_cmp_eq_u32 s61, 28
	s_cselect_b32 s42, s9, s30
	s_cselect_b32 s43, s7, s31
	s_cselect_b32 s38, s25, s59
	s_cselect_b32 s39, s23, s60
	s_add_u32 s34, s42, 0x80
	s_addc_u32 s35, s43, 0
	ds_read_b128 v[160:163], v219
	ds_read_b128 v[164:167], v219 offset:1024
	ds_read_b128 v[168:171], v219 offset:2048
	ds_read_b128 v[172:175], v219 offset:3072
	ds_read_b128 v[176:179], v219 offset:4096
	ds_read_b128 v[180:183], v219 offset:5120
	ds_read_b128 v[184:187], v219 offset:6144
	ds_read_b128 v[194:197], v219 offset:7168
	s_add_u32 s40, s38, 0x80
	s_addc_u32 s41, s39, 0
	s_add_u32 s36, s36, 0x80080
	s_addc_u32 s37, s37, 0
	s_add_i32 m0, s48, 0xc000
	s_nop 0
	global_load_lds_dwordx4 v213, s[36:37]
	s_nop 0
	s_add_i32 m0, s48, 0xe000
	s_nop 0
	global_load_lds_dwordx4 v214, s[36:37]
	s_waitcnt vmcnt(8)
	s_waitcnt lgkmcnt(0)
	s_barrier
	v_mfma_f32_16x16x32_bf16 v[152:155], v[100:103], v[160:163], v[152:155]
	v_mfma_f32_16x16x32_bf16 v[144:147], v[116:119], v[160:163], v[144:147]
	v_mfma_f32_16x16x32_bf16 v[112:115], v[116:119], v[168:171], v[112:115]
	v_mfma_f32_16x16x32_bf16 v[120:123], v[100:103], v[168:171], v[120:123]
	v_mfma_f32_16x16x32_bf16 v[92:95], v[100:103], v[176:179], v[92:95]
	v_mfma_f32_16x16x32_bf16 v[88:91], v[116:119], v[176:179], v[88:91]
	v_mfma_f32_16x16x32_bf16 v[72:75], v[116:119], v[184:187], v[72:75]
	v_mfma_f32_16x16x32_bf16 v[76:79], v[100:103], v[184:187], v[76:79]
	v_mfma_f32_16x16x32_bf16 v[152:155], v[108:111], v[164:167], v[152:155]
	v_mfma_f32_16x16x32_bf16 v[144:147], v[124:127], v[164:167], v[144:147]
	v_mfma_f32_16x16x32_bf16 v[112:115], v[124:127], v[172:175], v[112:115]
	v_mfma_f32_16x16x32_bf16 v[120:123], v[108:111], v[172:175], v[120:123]
	v_mfma_f32_16x16x32_bf16 v[92:95], v[108:111], v[180:183], v[92:95]
	v_mfma_f32_16x16x32_bf16 v[88:91], v[124:127], v[180:183], v[88:91]
	v_mfma_f32_16x16x32_bf16 v[72:75], v[124:127], v[194:197], v[72:75]
	v_mfma_f32_16x16x32_bf16 v[76:79], v[108:111], v[194:197], v[76:79]
	v_mfma_f32_16x16x32_bf16 v[136:139], v[132:135], v[160:163], v[136:139]
	v_mfma_f32_16x16x32_bf16 v[128:131], v[148:151], v[160:163], v[128:131]
	v_mfma_f32_16x16x32_bf16 v[96:99], v[148:151], v[168:171], v[96:99]
	v_mfma_f32_16x16x32_bf16 v[104:107], v[132:135], v[168:171], v[104:107]
	v_mfma_f32_16x16x32_bf16 v[84:87], v[132:135], v[176:179], v[84:87]
	v_mfma_f32_16x16x32_bf16 v[80:83], v[148:151], v[176:179], v[80:83]
	v_mfma_f32_16x16x32_bf16 v[64:67], v[148:151], v[184:187], v[64:67]
	v_mfma_f32_16x16x32_bf16 v[68:71], v[132:135], v[184:187], v[68:71]
	v_mfma_f32_16x16x32_bf16 v[136:139], v[140:143], v[164:167], v[136:139]
	v_mfma_f32_16x16x32_bf16 v[128:131], v[156:159], v[164:167], v[128:131]
	v_mfma_f32_16x16x32_bf16 v[96:99], v[156:159], v[172:175], v[96:99]
	v_mfma_f32_16x16x32_bf16 v[104:107], v[140:143], v[172:175], v[104:107]
	v_mfma_f32_16x16x32_bf16 v[84:87], v[140:143], v[180:183], v[84:87]
	v_mfma_f32_16x16x32_bf16 v[80:83], v[156:159], v[180:183], v[80:83]
	v_mfma_f32_16x16x32_bf16 v[64:67], v[156:159], v[194:197], v[64:67]
	v_mfma_f32_16x16x32_bf16 v[68:71], v[140:143], v[194:197], v[68:71]
	s_barrier
	ds_read_b128 v[160:163], v219 offset:16384
	ds_read_b128 v[164:167], v219 offset:17408
	ds_read_b128 v[168:171], v219 offset:18432
	ds_read_b128 v[172:175], v219 offset:19456
	ds_read_b128 v[176:179], v219 offset:20480
	ds_read_b128 v[180:183], v219 offset:21504
	ds_read_b128 v[184:187], v219 offset:22528
	ds_read_b128 v[194:197], v219 offset:23552
	s_add_i32 m0, s48, 0x10000
	s_nop 0
	global_load_lds_dwordx4 v213, s[38:39]
	s_nop 0
	s_add_i32 m0, s48, 0x12000
	s_nop 0
	global_load_lds_dwordx4 v214, s[38:39]
	s_add_u32 s36, s38, 0x80000
	s_addc_u32 s37, s39, 0
	s_add_i32 m0, s48, 0x14000
	s_nop 0
	global_load_lds_dwordx4 v213, s[36:37]
	s_nop 0
	s_add_i32 m0, s48, 0x16000
	s_nop 0
	global_load_lds_dwordx4 v214, s[36:37]
	s_nop 0
	s_add_i32 m0, s48, 0
	s_nop 0
	global_load_lds_dwordx4 v213, s[42:43]
	s_nop 0
	s_add_i32 m0, s48, 0x2000
	s_nop 0
	global_load_lds_dwordx4 v214, s[42:43]
	s_waitcnt vmcnt(8)
	s_waitcnt lgkmcnt(0)
	s_barrier
	v_mfma_f32_16x16x32_bf16 v[60:63], v[100:103], v[160:163], v[60:63]
	v_mfma_f32_16x16x32_bf16 v[56:59], v[116:119], v[160:163], v[56:59]
	v_mfma_f32_16x16x32_bf16 v[40:43], v[116:119], v[168:171], v[40:43]
	v_mfma_f32_16x16x32_bf16 v[44:47], v[100:103], v[168:171], v[44:47]
	v_mfma_f32_16x16x32_bf16 v[28:31], v[100:103], v[176:179], v[28:31]
	v_mfma_f32_16x16x32_bf16 v[24:27], v[116:119], v[176:179], v[24:27]
	v_mfma_f32_16x16x32_bf16 v[8:11], v[116:119], v[184:187], v[8:11]
	v_mfma_f32_16x16x32_bf16 v[12:15], v[100:103], v[184:187], v[12:15]
	v_mfma_f32_16x16x32_bf16 v[60:63], v[108:111], v[164:167], v[60:63]
	v_mfma_f32_16x16x32_bf16 v[56:59], v[124:127], v[164:167], v[56:59]
	v_mfma_f32_16x16x32_bf16 v[40:43], v[124:127], v[172:175], v[40:43]
	v_mfma_f32_16x16x32_bf16 v[44:47], v[108:111], v[172:175], v[44:47]
	v_mfma_f32_16x16x32_bf16 v[28:31], v[108:111], v[180:183], v[28:31]
	v_mfma_f32_16x16x32_bf16 v[24:27], v[124:127], v[180:183], v[24:27]
	v_mfma_f32_16x16x32_bf16 v[8:11], v[124:127], v[194:197], v[8:11]
	v_mfma_f32_16x16x32_bf16 v[12:15], v[108:111], v[194:197], v[12:15]
	v_mfma_f32_16x16x32_bf16 v[52:55], v[132:135], v[160:163], v[52:55]
	v_mfma_f32_16x16x32_bf16 v[48:51], v[148:151], v[160:163], v[48:51]
	v_mfma_f32_16x16x32_bf16 v[32:35], v[148:151], v[168:171], v[32:35]
	v_mfma_f32_16x16x32_bf16 v[36:39], v[132:135], v[168:171], v[36:39]
	v_mfma_f32_16x16x32_bf16 v[20:23], v[132:135], v[176:179], v[20:23]
	v_mfma_f32_16x16x32_bf16 v[16:19], v[148:151], v[176:179], v[16:19]
	v_mfma_f32_16x16x32_bf16 v[0:3], v[148:151], v[184:187], v[0:3]
	v_mfma_f32_16x16x32_bf16 v[4:7], v[132:135], v[184:187], v[4:7]
	v_mfma_f32_16x16x32_bf16 v[52:55], v[140:143], v[164:167], v[52:55]
	v_mfma_f32_16x16x32_bf16 v[48:51], v[156:159], v[164:167], v[48:51]
	v_mfma_f32_16x16x32_bf16 v[32:35], v[156:159], v[172:175], v[32:35]
	v_mfma_f32_16x16x32_bf16 v[36:39], v[140:143], v[172:175], v[36:39]
	v_mfma_f32_16x16x32_bf16 v[20:23], v[140:143], v[180:183], v[20:23]
	v_mfma_f32_16x16x32_bf16 v[16:19], v[156:159], v[180:183], v[16:19]
	v_mfma_f32_16x16x32_bf16 v[0:3], v[156:159], v[194:197], v[0:3]
	v_mfma_f32_16x16x32_bf16 v[4:7], v[140:143], v[194:197], v[4:7]
	s_barrier
	ds_read_b128 v[100:103], v220
	ds_read_b128 v[108:111], v220 offset:1024
	ds_read_b128 v[116:119], v220 offset:2048
	ds_read_b128 v[124:127], v220 offset:3072
	ds_read_b128 v[132:135], v221
	ds_read_b128 v[140:143], v221 offset:1024
	ds_read_b128 v[148:151], v221 offset:2048
	ds_read_b128 v[156:159], v221 offset:3072
	ds_read_b128 v[160:163], v219 offset:32768
	ds_read_b128 v[164:167], v219 offset:33792
	ds_read_b128 v[168:171], v219 offset:34816
	ds_read_b128 v[172:175], v219 offset:35840
	ds_read_b128 v[176:179], v219 offset:36864
	ds_read_b128 v[180:183], v219 offset:37888
	ds_read_b128 v[184:187], v219 offset:38912
	ds_read_b128 v[194:197], v219 offset:39936
	s_add_u32 s36, s42, 0x80000
	s_addc_u32 s37, s43, 0
	s_add_i32 m0, s48, 0x4000
	s_nop 0
	global_load_lds_dwordx4 v213, s[36:37]
	s_nop 0
	s_add_i32 m0, s48, 0x6000
	s_nop 0
	global_load_lds_dwordx4 v214, s[36:37]
	s_waitcnt vmcnt(8)
	s_waitcnt lgkmcnt(0)
	s_barrier
	v_mfma_f32_16x16x32_bf16 v[152:155], v[100:103], v[160:163], v[152:155]
	v_mfma_f32_16x16x32_bf16 v[144:147], v[116:119], v[160:163], v[144:147]
	v_mfma_f32_16x16x32_bf16 v[112:115], v[116:119], v[168:171], v[112:115]
	v_mfma_f32_16x16x32_bf16 v[120:123], v[100:103], v[168:171], v[120:123]
	v_mfma_f32_16x16x32_bf16 v[92:95], v[100:103], v[176:179], v[92:95]
	v_mfma_f32_16x16x32_bf16 v[88:91], v[116:119], v[176:179], v[88:91]
	v_mfma_f32_16x16x32_bf16 v[72:75], v[116:119], v[184:187], v[72:75]
	v_mfma_f32_16x16x32_bf16 v[76:79], v[100:103], v[184:187], v[76:79]
	v_mfma_f32_16x16x32_bf16 v[152:155], v[108:111], v[164:167], v[152:155]
	v_mfma_f32_16x16x32_bf16 v[144:147], v[124:127], v[164:167], v[144:147]
	v_mfma_f32_16x16x32_bf16 v[112:115], v[124:127], v[172:175], v[112:115]
	v_mfma_f32_16x16x32_bf16 v[120:123], v[108:111], v[172:175], v[120:123]
	v_mfma_f32_16x16x32_bf16 v[92:95], v[108:111], v[180:183], v[92:95]
	v_mfma_f32_16x16x32_bf16 v[88:91], v[124:127], v[180:183], v[88:91]
	v_mfma_f32_16x16x32_bf16 v[72:75], v[124:127], v[194:197], v[72:75]
	v_mfma_f32_16x16x32_bf16 v[76:79], v[108:111], v[194:197], v[76:79]
	v_mfma_f32_16x16x32_bf16 v[136:139], v[132:135], v[160:163], v[136:139]
	v_mfma_f32_16x16x32_bf16 v[128:131], v[148:151], v[160:163], v[128:131]
	v_mfma_f32_16x16x32_bf16 v[96:99], v[148:151], v[168:171], v[96:99]
	v_mfma_f32_16x16x32_bf16 v[104:107], v[132:135], v[168:171], v[104:107]
	v_mfma_f32_16x16x32_bf16 v[84:87], v[132:135], v[176:179], v[84:87]
	v_mfma_f32_16x16x32_bf16 v[80:83], v[148:151], v[176:179], v[80:83]
	v_mfma_f32_16x16x32_bf16 v[64:67], v[148:151], v[184:187], v[64:67]
	v_mfma_f32_16x16x32_bf16 v[68:71], v[132:135], v[184:187], v[68:71]
	v_mfma_f32_16x16x32_bf16 v[136:139], v[140:143], v[164:167], v[136:139]
	v_mfma_f32_16x16x32_bf16 v[128:131], v[156:159], v[164:167], v[128:131]
	v_mfma_f32_16x16x32_bf16 v[96:99], v[156:159], v[172:175], v[96:99]
	v_mfma_f32_16x16x32_bf16 v[104:107], v[140:143], v[172:175], v[104:107]
	v_mfma_f32_16x16x32_bf16 v[84:87], v[140:143], v[180:183], v[84:87]
	v_mfma_f32_16x16x32_bf16 v[80:83], v[156:159], v[180:183], v[80:83]
	v_mfma_f32_16x16x32_bf16 v[64:67], v[156:159], v[194:197], v[64:67]
	v_mfma_f32_16x16x32_bf16 v[68:71], v[140:143], v[194:197], v[68:71]
	s_barrier
	ds_read_b128 v[160:163], v219 offset:49152
	ds_read_b128 v[164:167], v219 offset:50176
	ds_read_b128 v[168:171], v219 offset:51200
	ds_read_b128 v[172:175], v219 offset:52224
	ds_read_b128 v[176:179], v219 offset:53248
	ds_read_b128 v[180:183], v219 offset:54272
	ds_read_b128 v[184:187], v219 offset:55296
	ds_read_b128 v[194:197], v219 offset:56320
	s_add_i32 m0, s48, 0x18000
	s_nop 0
	global_load_lds_dwordx4 v213, s[40:41]
	s_nop 0
	s_add_i32 m0, s48, 0x1a000
	s_nop 0
	global_load_lds_dwordx4 v214, s[40:41]
	s_add_u32 s36, s38, 0x80080
	s_addc_u32 s37, s39, 0
	s_add_i32 m0, s48, 0x1c000
	s_nop 0
	global_load_lds_dwordx4 v213, s[36:37]
	s_nop 0
	s_add_i32 m0, s48, 0x1e000
	s_nop 0
	global_load_lds_dwordx4 v214, s[36:37]
	s_nop 0
	s_add_i32 m0, s48, 0x8000
	s_nop 0
	global_load_lds_dwordx4 v213, s[34:35]
	s_nop 0
	s_add_i32 m0, s48, 0xa000
	s_nop 0
	global_load_lds_dwordx4 v214, s[34:35]
	s_waitcnt vmcnt(8)
	s_waitcnt lgkmcnt(0)
	s_barrier
	v_mfma_f32_16x16x32_bf16 v[60:63], v[100:103], v[160:163], v[60:63]
	v_mfma_f32_16x16x32_bf16 v[56:59], v[116:119], v[160:163], v[56:59]
	v_mfma_f32_16x16x32_bf16 v[40:43], v[116:119], v[168:171], v[40:43]
	v_mfma_f32_16x16x32_bf16 v[44:47], v[100:103], v[168:171], v[44:47]
	v_mfma_f32_16x16x32_bf16 v[28:31], v[100:103], v[176:179], v[28:31]
	v_mfma_f32_16x16x32_bf16 v[24:27], v[116:119], v[176:179], v[24:27]
	v_mfma_f32_16x16x32_bf16 v[8:11], v[116:119], v[184:187], v[8:11]
	v_mfma_f32_16x16x32_bf16 v[12:15], v[100:103], v[184:187], v[12:15]
	v_mfma_f32_16x16x32_bf16 v[60:63], v[108:111], v[164:167], v[60:63]
	v_mfma_f32_16x16x32_bf16 v[56:59], v[124:127], v[164:167], v[56:59]
	v_mfma_f32_16x16x32_bf16 v[40:43], v[124:127], v[172:175], v[40:43]
	v_mfma_f32_16x16x32_bf16 v[44:47], v[108:111], v[172:175], v[44:47]
	v_mfma_f32_16x16x32_bf16 v[28:31], v[108:111], v[180:183], v[28:31]
	v_mfma_f32_16x16x32_bf16 v[24:27], v[124:127], v[180:183], v[24:27]
	v_mfma_f32_16x16x32_bf16 v[8:11], v[124:127], v[194:197], v[8:11]
	v_mfma_f32_16x16x32_bf16 v[12:15], v[108:111], v[194:197], v[12:15]
	v_mfma_f32_16x16x32_bf16 v[52:55], v[132:135], v[160:163], v[52:55]
	v_mfma_f32_16x16x32_bf16 v[48:51], v[148:151], v[160:163], v[48:51]
	v_mfma_f32_16x16x32_bf16 v[32:35], v[148:151], v[168:171], v[32:35]
	v_mfma_f32_16x16x32_bf16 v[36:39], v[132:135], v[168:171], v[36:39]
	v_mfma_f32_16x16x32_bf16 v[20:23], v[132:135], v[176:179], v[20:23]
	v_mfma_f32_16x16x32_bf16 v[16:19], v[148:151], v[176:179], v[16:19]
	v_mfma_f32_16x16x32_bf16 v[0:3], v[148:151], v[184:187], v[0:3]
	v_mfma_f32_16x16x32_bf16 v[4:7], v[132:135], v[184:187], v[4:7]
	v_mfma_f32_16x16x32_bf16 v[52:55], v[140:143], v[164:167], v[52:55]
	v_mfma_f32_16x16x32_bf16 v[48:51], v[156:159], v[164:167], v[48:51]
	v_mfma_f32_16x16x32_bf16 v[32:35], v[156:159], v[172:175], v[32:35]
	v_mfma_f32_16x16x32_bf16 v[36:39], v[140:143], v[172:175], v[36:39]
	v_mfma_f32_16x16x32_bf16 v[20:23], v[140:143], v[180:183], v[20:23]
	v_mfma_f32_16x16x32_bf16 v[16:19], v[156:159], v[180:183], v[16:19]
	v_mfma_f32_16x16x32_bf16 v[0:3], v[156:159], v[194:197], v[0:3]
	v_mfma_f32_16x16x32_bf16 v[4:7], v[140:143], v[194:197], v[4:7]
	s_barrier
	s_add_i32 s61, s61, 2
	s_add_u32 s59, s59, 0x100
	s_addc_u32 s60, s60, 0
	s_cmp_gt_u32 s61, 29
	s_mov_b64 s[36:37], s[30:31]
	s_cbranch_scc0 .LBB0_603
	s_and_b64 vcc, exec, s[20:21]
	s_cbranch_vccz .LBB0_606
	s_barrier

.LBB0_755:
	ds_read_b128 v[20:23], v205
	ds_read_b128 v[24:27], v205 offset:1024
	ds_read_b128 v[28:31], v205 offset:2048
	ds_read_b128 v[32:35], v205 offset:3072
	ds_read_b128 v[36:39], v204
	ds_read_b128 v[40:43], v204 offset:1024
	ds_read_b128 v[52:55], v204 offset:2048
	ds_read_b128 v[56:59], v204 offset:3072
	s_add_u32 s24, s26, 0x100
	s_addc_u32 s25, s27, 0
	s_and_b64 s[30:31], s[30:31], exec
	s_cselect_b32 s38, s59, s24
	s_cselect_b32 s39, s58, s25
	s_cselect_b32 s35, s15, s62
	s_cselect_b32 s34, s60, s61
	s_add_u32 s30, s38, 0x80
	s_addc_u32 s31, s39, 0
	s_add_u32 s36, s34, 0x80
	s_addc_u32 s37, s35, 0
	ds_read_b128 v[64:67], v206
	ds_read_b128 v[68:71], v206 offset:1024
	ds_read_b128 v[72:75], v206 offset:2048
	ds_read_b128 v[76:79], v206 offset:3072
	ds_read_b128 v[80:83], v206 offset:4096
	ds_read_b128 v[84:87], v206 offset:5120
	ds_read_b128 v[88:91], v206 offset:6144
	ds_read_b128 v[92:95], v206 offset:7168
	s_add_u32 s26, s26, 0x40080
	s_addc_u32 s27, s27, 0
	s_add_i32 m0, s46, 0xc000
	s_nop 0
	global_load_lds_dwordx4 v199, s[26:27]
	s_nop 0
	s_add_i32 m0, s46, 0xe000
	s_nop 0
	global_load_lds_dwordx4 v201, s[26:27]
	s_waitcnt vmcnt(8)
	s_waitcnt lgkmcnt(0)
	s_barrier
	v_mfma_i32_16x16x64_i8 v[184:187], v[20:23], v[64:67], v[184:187]
	v_mfma_i32_16x16x64_i8 v[176:179], v[28:31], v[64:67], v[176:179]
	v_mfma_i32_16x16x64_i8 v[160:163], v[28:31], v[72:75], v[160:163]
	v_mfma_i32_16x16x64_i8 v[168:171], v[20:23], v[72:75], v[168:171]
	v_mfma_i32_16x16x64_i8 v[152:155], v[20:23], v[80:83], v[152:155]
	v_mfma_i32_16x16x64_i8 v[144:147], v[28:31], v[80:83], v[144:147]
	v_mfma_i32_16x16x64_i8 v[128:131], v[28:31], v[88:91], v[128:131]
	v_mfma_i32_16x16x64_i8 v[136:139], v[20:23], v[88:91], v[136:139]
	v_mfma_i32_16x16x64_i8 v[184:187], v[24:27], v[68:71], v[184:187]
	v_mfma_i32_16x16x64_i8 v[176:179], v[32:35], v[68:71], v[176:179]
	v_mfma_i32_16x16x64_i8 v[160:163], v[32:35], v[76:79], v[160:163]
	v_mfma_i32_16x16x64_i8 v[168:171], v[24:27], v[76:79], v[168:171]
	v_mfma_i32_16x16x64_i8 v[152:155], v[24:27], v[84:87], v[152:155]
	v_mfma_i32_16x16x64_i8 v[144:147], v[32:35], v[84:87], v[144:147]
	v_mfma_i32_16x16x64_i8 v[128:131], v[32:35], v[92:95], v[128:131]
	v_mfma_i32_16x16x64_i8 v[136:139], v[24:27], v[92:95], v[136:139]
	v_mfma_i32_16x16x64_i8 v[188:191], v[36:39], v[64:67], v[188:191]
	v_mfma_i32_16x16x64_i8 v[64:67], v[52:55], v[64:67], v[180:183]
	v_mfma_i32_16x16x64_i8 v[188:191], v[40:43], v[68:71], v[188:191]
	v_mfma_i32_16x16x64_i8 v[64:67], v[56:59], v[68:71], v[64:67]
	v_mfma_i32_16x16x64_i8 v[68:71], v[36:39], v[72:75], v[172:175]
	v_mfma_i32_16x16x64_i8 v[72:75], v[52:55], v[72:75], v[164:167]
	v_mfma_i32_16x16x64_i8 v[68:71], v[40:43], v[76:79], v[68:71]
	v_mfma_i32_16x16x64_i8 v[72:75], v[56:59], v[76:79], v[72:75]
	v_mfma_i32_16x16x64_i8 v[76:79], v[36:39], v[80:83], v[156:159]
	v_mfma_i32_16x16x64_i8 v[80:83], v[52:55], v[80:83], v[148:151]
	v_mfma_i32_16x16x64_i8 v[76:79], v[40:43], v[84:87], v[76:79]
	v_mfma_i32_16x16x64_i8 v[80:83], v[56:59], v[84:87], v[80:83]
	v_mfma_i32_16x16x64_i8 v[84:87], v[36:39], v[88:91], v[140:143]
	v_mfma_i32_16x16x64_i8 v[88:91], v[52:55], v[88:91], v[132:135]
	v_mfma_i32_16x16x64_i8 v[84:87], v[40:43], v[92:95], v[84:87]
	v_mfma_i32_16x16x64_i8 v[88:91], v[56:59], v[92:95], v[88:91]
	s_barrier
	ds_read_b128 v[92:95], v206 offset:16384
	ds_read_b128 v[132:135], v206 offset:17408
	ds_read_b128 v[140:143], v206 offset:18432
	ds_read_b128 v[148:151], v206 offset:19456
	ds_read_b128 v[156:159], v206 offset:20480
	ds_read_b128 v[164:167], v206 offset:21504
	ds_read_b128 v[172:175], v206 offset:22528
	ds_read_b128 v[180:183], v206 offset:23552
	s_add_i32 m0, s46, 0x10000
	s_nop 0
	global_load_lds_dwordx4 v200, s[34:35]
	s_nop 0
	s_add_i32 m0, s46, 0x12000
	s_nop 0
	global_load_lds_dwordx4 v202, s[34:35]
	s_add_u32 s26, s34, 0x40000
	s_addc_u32 s27, s35, 0
	s_add_i32 m0, s46, 0x14000
	s_nop 0
	global_load_lds_dwordx4 v200, s[26:27]
	s_nop 0
	s_add_i32 m0, s46, 0x16000
	s_nop 0
	global_load_lds_dwordx4 v202, s[26:27]
	s_nop 0
	s_add_i32 m0, s46, 0
	s_nop 0
	global_load_lds_dwordx4 v199, s[38:39]
	s_nop 0
	s_add_i32 m0, s46, 0x2000
	s_nop 0
	global_load_lds_dwordx4 v201, s[38:39]
	s_waitcnt vmcnt(8)
	s_waitcnt lgkmcnt(0)
	s_barrier
	v_mfma_i32_16x16x64_i8 v[120:123], v[20:23], v[92:95], v[120:123]
	v_mfma_i32_16x16x64_i8 v[112:115], v[28:31], v[92:95], v[112:115]
	v_mfma_i32_16x16x64_i8 v[96:99], v[28:31], v[140:143], v[96:99]
	v_mfma_i32_16x16x64_i8 v[104:107], v[20:23], v[140:143], v[104:107]
	v_mfma_i32_16x16x64_i8 v[48:51], v[20:23], v[156:159], v[48:51]
	v_mfma_i32_16x16x64_i8 v[16:19], v[28:31], v[156:159], v[16:19]
	v_mfma_i32_16x16x64_i8 v[0:3], v[28:31], v[172:175], v[0:3]
	v_mfma_i32_16x16x64_i8 v[8:11], v[20:23], v[172:175], v[8:11]
	v_mfma_i32_16x16x64_i8 v[120:123], v[24:27], v[132:135], v[120:123]
	v_mfma_i32_16x16x64_i8 v[112:115], v[32:35], v[132:135], v[112:115]
	v_mfma_i32_16x16x64_i8 v[96:99], v[32:35], v[148:151], v[96:99]
	v_mfma_i32_16x16x64_i8 v[104:107], v[24:27], v[148:151], v[104:107]
	v_mfma_i32_16x16x64_i8 v[48:51], v[24:27], v[164:167], v[48:51]
	v_mfma_i32_16x16x64_i8 v[16:19], v[32:35], v[164:167], v[16:19]
	v_mfma_i32_16x16x64_i8 v[0:3], v[32:35], v[180:183], v[0:3]
	v_mfma_i32_16x16x64_i8 v[8:11], v[24:27], v[180:183], v[8:11]
	v_mfma_i32_16x16x64_i8 v[20:23], v[36:39], v[92:95], v[124:127]
	v_mfma_i32_16x16x64_i8 v[124:127], v[40:43], v[132:135], v[20:23]
	v_mfma_i32_16x16x64_i8 v[20:23], v[52:55], v[92:95], v[116:119]
	v_mfma_i32_16x16x64_i8 v[116:119], v[56:59], v[132:135], v[20:23]
	v_mfma_i32_16x16x64_i8 v[20:23], v[36:39], v[140:143], v[108:111]
	v_mfma_i32_16x16x64_i8 v[108:111], v[40:43], v[148:151], v[20:23]
	v_mfma_i32_16x16x64_i8 v[20:23], v[52:55], v[140:143], v[100:103]
	v_mfma_i32_16x16x64_i8 v[100:103], v[56:59], v[148:151], v[20:23]
	v_mfma_i32_16x16x64_i8 v[20:23], v[36:39], v[156:159], v[60:63]
	v_mfma_i32_16x16x64_i8 v[60:63], v[40:43], v[164:167], v[20:23]
	v_mfma_i32_16x16x64_i8 v[20:23], v[52:55], v[156:159], v[44:47]
	v_mfma_i32_16x16x64_i8 v[12:15], v[36:39], v[172:175], v[12:15]
	v_mfma_i32_16x16x64_i8 v[4:7], v[52:55], v[172:175], v[4:7]
	v_mfma_i32_16x16x64_i8 v[44:47], v[56:59], v[164:167], v[20:23]
	v_mfma_i32_16x16x64_i8 v[12:15], v[40:43], v[180:183], v[12:15]
	v_mfma_i32_16x16x64_i8 v[4:7], v[56:59], v[180:183], v[4:7]
	s_barrier
	ds_read_b128 v[36:39], v207
	ds_read_b128 v[28:31], v207 offset:1024
	ds_read_b128 v[24:27], v207 offset:2048
	ds_read_b128 v[20:23], v207 offset:3072
	ds_read_b128 v[56:59], v208
	ds_read_b128 v[52:55], v208 offset:1024
	ds_read_b128 v[40:43], v208 offset:2048
	ds_read_b128 v[32:35], v208 offset:3072
	ds_read_b128 v[92:95], v206 offset:32768
	ds_read_b128 v[132:135], v206 offset:33792
	ds_read_b128 v[140:143], v206 offset:34816
	ds_read_b128 v[148:151], v206 offset:35840
	ds_read_b128 v[192:195], v206 offset:36864
	ds_read_b128 v[210:213], v206 offset:37888
	ds_read_b128 v[214:217], v206 offset:38912
	ds_read_b128 v[218:221], v206 offset:39936
	s_add_u32 s26, s38, 0x40000
	s_addc_u32 s27, s39, 0
	s_add_i32 m0, s46, 0x4000
	s_nop 0
	global_load_lds_dwordx4 v199, s[26:27]
	s_nop 0
	s_add_i32 m0, s46, 0x6000
	s_nop 0
	global_load_lds_dwordx4 v201, s[26:27]
	s_waitcnt vmcnt(8)
	s_waitcnt lgkmcnt(0)
	s_barrier
	v_mfma_i32_16x16x64_i8 v[156:159], v[36:39], v[92:95], v[184:187]
	v_mfma_i32_16x16x64_i8 v[184:187], v[28:31], v[132:135], v[156:159]
	v_mfma_i32_16x16x64_i8 v[156:159], v[24:27], v[92:95], v[176:179]
	v_mfma_i32_16x16x64_i8 v[176:179], v[20:23], v[132:135], v[156:159]
	v_mfma_i32_16x16x64_i8 v[156:159], v[36:39], v[140:143], v[168:171]
	v_mfma_i32_16x16x64_i8 v[168:171], v[28:31], v[148:151], v[156:159]
	v_mfma_i32_16x16x64_i8 v[156:159], v[24:27], v[140:143], v[160:163]
	v_mfma_i32_16x16x64_i8 v[152:155], v[36:39], v[192:195], v[152:155]
	v_mfma_i32_16x16x64_i8 v[144:147], v[24:27], v[192:195], v[144:147]
	v_mfma_i32_16x16x64_i8 v[136:139], v[36:39], v[214:217], v[136:139]
	v_mfma_i32_16x16x64_i8 v[128:131], v[24:27], v[214:217], v[128:131]
	v_mfma_i32_16x16x64_i8 v[160:163], v[20:23], v[148:151], v[156:159]
	v_mfma_i32_16x16x64_i8 v[152:155], v[28:31], v[210:213], v[152:155]
	v_mfma_i32_16x16x64_i8 v[144:147], v[20:23], v[210:213], v[144:147]
	v_mfma_i32_16x16x64_i8 v[136:139], v[28:31], v[218:221], v[136:139]
	v_mfma_i32_16x16x64_i8 v[128:131], v[20:23], v[218:221], v[128:131]
	v_mfma_i32_16x16x64_i8 v[64:67], v[40:43], v[92:95], v[64:67]
	v_mfma_i32_16x16x64_i8 v[180:183], v[32:35], v[132:135], v[64:67]
	v_mfma_i32_16x16x64_i8 v[64:67], v[56:59], v[140:143], v[68:71]
	v_mfma_i32_16x16x64_i8 v[172:175], v[52:55], v[148:151], v[64:67]
	v_mfma_i32_16x16x64_i8 v[64:67], v[40:43], v[140:143], v[72:75]
	v_mfma_i32_16x16x64_i8 v[156:159], v[56:59], v[92:95], v[188:191]
	v_mfma_i32_16x16x64_i8 v[164:167], v[32:35], v[148:151], v[64:67]
	v_mfma_i32_16x16x64_i8 v[64:67], v[56:59], v[192:195], v[76:79]
	v_mfma_i32_16x16x64_i8 v[188:191], v[52:55], v[132:135], v[156:159]
	v_mfma_i32_16x16x64_i8 v[156:159], v[52:55], v[210:213], v[64:67]
	v_mfma_i32_16x16x64_i8 v[64:67], v[40:43], v[192:195], v[80:83]
	v_mfma_i32_16x16x64_i8 v[148:151], v[32:35], v[210:213], v[64:67]
	v_mfma_i32_16x16x64_i8 v[64:67], v[56:59], v[214:217], v[84:87]
	v_mfma_i32_16x16x64_i8 v[140:143], v[52:55], v[218:221], v[64:67]
	v_mfma_i32_16x16x64_i8 v[64:67], v[40:43], v[214:217], v[88:91]
	v_mfma_i32_16x16x64_i8 v[132:135], v[32:35], v[218:221], v[64:67]
	s_barrier
	ds_read_b128 v[92:95], v206 offset:49152
	ds_read_b128 v[88:91], v206 offset:50176
	ds_read_b128 v[84:87], v206 offset:51200
	ds_read_b128 v[80:83], v206 offset:52224
	ds_read_b128 v[76:79], v206 offset:53248
	ds_read_b128 v[72:75], v206 offset:54272
	ds_read_b128 v[68:71], v206 offset:55296
	ds_read_b128 v[64:67], v206 offset:56320
	s_add_i32 m0, s46, 0x18000
	s_nop 0
	global_load_lds_dwordx4 v200, s[36:37]
	s_nop 0
	s_add_i32 m0, s46, 0x1a000
	s_nop 0
	global_load_lds_dwordx4 v202, s[36:37]
	s_add_u32 s26, s34, 0x40080
	s_addc_u32 s27, s35, 0
	s_add_i32 m0, s46, 0x1c000
	s_nop 0
	global_load_lds_dwordx4 v200, s[26:27]
	s_nop 0
	s_add_i32 m0, s46, 0x1e000
	s_nop 0
	global_load_lds_dwordx4 v202, s[26:27]
	s_nop 0
	s_add_i32 m0, s46, 0x8000
	s_nop 0
	global_load_lds_dwordx4 v199, s[30:31]
	s_nop 0
	s_add_i32 m0, s46, 0xa000
	s_nop 0
	global_load_lds_dwordx4 v201, s[30:31]
	s_waitcnt vmcnt(8)
	s_waitcnt lgkmcnt(0)
	s_barrier
	v_mfma_i32_16x16x64_i8 v[120:123], v[36:39], v[92:95], v[120:123]
	v_mfma_i32_16x16x64_i8 v[112:115], v[24:27], v[92:95], v[112:115]
	v_mfma_i32_16x16x64_i8 v[96:99], v[24:27], v[84:87], v[96:99]
	v_mfma_i32_16x16x64_i8 v[104:107], v[36:39], v[84:87], v[104:107]
	v_mfma_i32_16x16x64_i8 v[48:51], v[36:39], v[76:79], v[48:51]
	v_mfma_i32_16x16x64_i8 v[16:19], v[24:27], v[76:79], v[16:19]
	v_mfma_i32_16x16x64_i8 v[0:3], v[24:27], v[68:71], v[0:3]
	v_mfma_i32_16x16x64_i8 v[8:11], v[36:39], v[68:71], v[8:11]
	v_mfma_i32_16x16x64_i8 v[120:123], v[28:31], v[88:91], v[120:123]
	v_mfma_i32_16x16x64_i8 v[112:115], v[20:23], v[88:91], v[112:115]
	v_mfma_i32_16x16x64_i8 v[96:99], v[20:23], v[80:83], v[96:99]
	v_mfma_i32_16x16x64_i8 v[104:107], v[28:31], v[80:83], v[104:107]
	v_mfma_i32_16x16x64_i8 v[48:51], v[28:31], v[72:75], v[48:51]
	v_mfma_i32_16x16x64_i8 v[16:19], v[20:23], v[72:75], v[16:19]
	v_mfma_i32_16x16x64_i8 v[0:3], v[20:23], v[64:67], v[0:3]
	v_mfma_i32_16x16x64_i8 v[8:11], v[28:31], v[64:67], v[8:11]
	v_mfma_i32_16x16x64_i8 v[124:127], v[56:59], v[92:95], v[124:127]
	v_mfma_i32_16x16x64_i8 v[116:119], v[40:43], v[92:95], v[116:119]
	v_mfma_i32_16x16x64_i8 v[100:103], v[40:43], v[84:87], v[100:103]
	v_mfma_i32_16x16x64_i8 v[108:111], v[56:59], v[84:87], v[108:111]
	v_mfma_i32_16x16x64_i8 v[60:63], v[56:59], v[76:79], v[60:63]
	v_mfma_i32_16x16x64_i8 v[44:47], v[40:43], v[76:79], v[44:47]
	v_mfma_i32_16x16x64_i8 v[4:7], v[40:43], v[68:71], v[4:7]
	v_mfma_i32_16x16x64_i8 v[12:15], v[56:59], v[68:71], v[12:15]
	v_mfma_i32_16x16x64_i8 v[124:127], v[52:55], v[88:91], v[124:127]
	v_mfma_i32_16x16x64_i8 v[116:119], v[32:35], v[88:91], v[116:119]
	v_mfma_i32_16x16x64_i8 v[100:103], v[32:35], v[80:83], v[100:103]
	v_mfma_i32_16x16x64_i8 v[108:111], v[52:55], v[80:83], v[108:111]
	v_mfma_i32_16x16x64_i8 v[60:63], v[52:55], v[72:75], v[60:63]
	v_mfma_i32_16x16x64_i8 v[44:47], v[32:35], v[72:75], v[44:47]
	v_mfma_i32_16x16x64_i8 v[4:7], v[32:35], v[64:67], v[4:7]
	v_mfma_i32_16x16x64_i8 v[12:15], v[52:55], v[64:67], v[12:15]
	s_barrier
	s_add_i32 s17, s17, 2
	s_add_u32 s61, s61, 0x100
	s_addc_u32 s62, s62, 0
	s_cmp_gt_u32 s17, 13
	s_cbranch_scc1 .LBB0_757
	s_mov_b64 s[26:27], s[24:25]
	s_branch .LBB0_753

.LBB0_838:
	ds_read_b128 v[112:115], v181
	ds_read_b128 v[116:119], v181 offset:1024
	ds_read_b128 v[136:139], v181 offset:2048
	ds_read_b128 v[140:143], v181 offset:3072
	ds_read_b128 v[144:147], v182
	ds_read_b128 v[148:151], v182 offset:1024
	ds_read_b128 v[156:159], v182 offset:2048
	ds_read_b128 v[160:163], v182 offset:3072
	s_cmpk_eq_i32 s55, 0x54
	s_cselect_b32 s28, s18, s51
	s_cselect_b32 s29, s19, s52
	s_cselect_b32 s24, s20, s53
	s_cselect_b32 s25, s21, s54
	s_add_u32 s22, s28, 0x80
	s_addc_u32 s23, s29, 0
	ds_read_b128 v[164:167], v183
	ds_read_b128 v[168:171], v183 offset:1024
	ds_read_b128 v[188:191], v183 offset:2048
	ds_read_b128 v[192:195], v183 offset:3072
	ds_read_b128 v[196:199], v183 offset:4096
	ds_read_b128 v[200:203], v183 offset:5120
	ds_read_b128 v[204:207], v183 offset:6144
	ds_read_b128 v[208:211], v183 offset:7168
	s_add_u32 s26, s24, 0x80
	s_addc_u32 s27, s25, 0
	s_add_i32 m0, s36, 0xc000
	s_nop 0
	global_load_lds_dwordx4 v175, s[6:7]
	s_nop 0
	s_add_i32 m0, s36, 0xe000
	s_nop 0
	global_load_lds_dwordx4 v177, s[6:7]
	s_waitcnt vmcnt(8)
	s_waitcnt lgkmcnt(0)
	s_barrier
	v_mfma_f32_16x16x32_bf16 v[132:135], v[112:115], v[164:167], v[132:135]
	v_mfma_f32_16x16x32_bf16 v[128:131], v[136:139], v[164:167], v[128:131]
	v_mfma_f32_16x16x32_bf16 v[104:107], v[136:139], v[188:191], v[104:107]
	v_mfma_f32_16x16x32_bf16 v[108:111], v[112:115], v[188:191], v[108:111]
	v_mfma_f32_16x16x32_bf16 v[92:95], v[112:115], v[196:199], v[92:95]
	v_mfma_f32_16x16x32_bf16 v[88:91], v[136:139], v[196:199], v[88:91]
	v_mfma_f32_16x16x32_bf16 v[72:75], v[136:139], v[204:207], v[72:75]
	v_mfma_f32_16x16x32_bf16 v[76:79], v[112:115], v[204:207], v[76:79]
	v_mfma_f32_16x16x32_bf16 v[132:135], v[116:119], v[168:171], v[132:135]
	v_mfma_f32_16x16x32_bf16 v[128:131], v[140:143], v[168:171], v[128:131]
	v_mfma_f32_16x16x32_bf16 v[104:107], v[140:143], v[192:195], v[104:107]
	v_mfma_f32_16x16x32_bf16 v[108:111], v[116:119], v[192:195], v[108:111]
	v_mfma_f32_16x16x32_bf16 v[92:95], v[116:119], v[200:203], v[92:95]
	v_mfma_f32_16x16x32_bf16 v[88:91], v[140:143], v[200:203], v[88:91]
	v_mfma_f32_16x16x32_bf16 v[72:75], v[140:143], v[208:211], v[72:75]
	v_mfma_f32_16x16x32_bf16 v[76:79], v[116:119], v[208:211], v[76:79]
	v_mfma_f32_16x16x32_bf16 v[124:127], v[144:147], v[164:167], v[124:127]
	v_mfma_f32_16x16x32_bf16 v[120:123], v[156:159], v[164:167], v[120:123]
	v_mfma_f32_16x16x32_bf16 v[96:99], v[156:159], v[188:191], v[96:99]
	v_mfma_f32_16x16x32_bf16 v[100:103], v[144:147], v[188:191], v[100:103]
	v_mfma_f32_16x16x32_bf16 v[84:87], v[144:147], v[196:199], v[84:87]
	v_mfma_f32_16x16x32_bf16 v[80:83], v[156:159], v[196:199], v[80:83]
	v_mfma_f32_16x16x32_bf16 v[64:67], v[156:159], v[204:207], v[64:67]
	v_mfma_f32_16x16x32_bf16 v[68:71], v[144:147], v[204:207], v[68:71]
	v_mfma_f32_16x16x32_bf16 v[124:127], v[148:151], v[168:171], v[124:127]
	v_mfma_f32_16x16x32_bf16 v[120:123], v[160:163], v[168:171], v[120:123]
	v_mfma_f32_16x16x32_bf16 v[96:99], v[160:163], v[192:195], v[96:99]
	v_mfma_f32_16x16x32_bf16 v[100:103], v[148:151], v[192:195], v[100:103]
	v_mfma_f32_16x16x32_bf16 v[84:87], v[148:151], v[200:203], v[84:87]
	v_mfma_f32_16x16x32_bf16 v[80:83], v[160:163], v[200:203], v[80:83]
	v_mfma_f32_16x16x32_bf16 v[64:67], v[160:163], v[208:211], v[64:67]
	v_mfma_f32_16x16x32_bf16 v[68:71], v[148:151], v[208:211], v[68:71]
	s_barrier
	ds_read_b128 v[164:167], v183 offset:16384
	ds_read_b128 v[168:171], v183 offset:17408
	ds_read_b128 v[188:191], v183 offset:18432
	ds_read_b128 v[192:195], v183 offset:19456
	ds_read_b128 v[196:199], v183 offset:20480
	ds_read_b128 v[200:203], v183 offset:21504
	ds_read_b128 v[204:207], v183 offset:22528
	ds_read_b128 v[208:211], v183 offset:23552
	s_add_i32 m0, s36, 0x10000
	s_nop 0
	global_load_lds_dwordx4 v176, s[24:25]
	s_nop 0
	s_add_i32 m0, s36, 0x12000
	s_nop 0
	global_load_lds_dwordx4 v178, s[24:25]
	s_add_u32 s56, s24, 0x160000
	s_addc_u32 s57, s25, 0
	s_add_i32 m0, s36, 0x14000
	s_nop 0
	global_load_lds_dwordx4 v176, s[56:57]
	s_nop 0
	s_add_i32 m0, s36, 0x16000
	s_nop 0
	global_load_lds_dwordx4 v178, s[56:57]
	s_nop 0
	s_add_i32 m0, s36, 0
	s_nop 0
	global_load_lds_dwordx4 v175, s[28:29]
	s_nop 0
	s_add_i32 m0, s36, 0x2000
	s_nop 0
	global_load_lds_dwordx4 v177, s[28:29]
	s_waitcnt vmcnt(8)
	s_waitcnt lgkmcnt(0)
	s_barrier
	v_mfma_f32_16x16x32_bf16 v[60:63], v[112:115], v[164:167], v[60:63]
	v_mfma_f32_16x16x32_bf16 v[56:59], v[136:139], v[164:167], v[56:59]
	v_mfma_f32_16x16x32_bf16 v[40:43], v[136:139], v[188:191], v[40:43]
	v_mfma_f32_16x16x32_bf16 v[44:47], v[112:115], v[188:191], v[44:47]
	v_mfma_f32_16x16x32_bf16 v[28:31], v[112:115], v[196:199], v[28:31]
	v_mfma_f32_16x16x32_bf16 v[24:27], v[136:139], v[196:199], v[24:27]
	v_mfma_f32_16x16x32_bf16 v[8:11], v[136:139], v[204:207], v[8:11]
	v_mfma_f32_16x16x32_bf16 v[12:15], v[112:115], v[204:207], v[12:15]
	v_mfma_f32_16x16x32_bf16 v[60:63], v[116:119], v[168:171], v[60:63]
	v_mfma_f32_16x16x32_bf16 v[56:59], v[140:143], v[168:171], v[56:59]
	v_mfma_f32_16x16x32_bf16 v[40:43], v[140:143], v[192:195], v[40:43]
	v_mfma_f32_16x16x32_bf16 v[44:47], v[116:119], v[192:195], v[44:47]
	v_mfma_f32_16x16x32_bf16 v[28:31], v[116:119], v[200:203], v[28:31]
	v_mfma_f32_16x16x32_bf16 v[24:27], v[140:143], v[200:203], v[24:27]
	v_mfma_f32_16x16x32_bf16 v[8:11], v[140:143], v[208:211], v[8:11]
	v_mfma_f32_16x16x32_bf16 v[12:15], v[116:119], v[208:211], v[12:15]
	v_mfma_f32_16x16x32_bf16 v[52:55], v[144:147], v[164:167], v[52:55]
	v_mfma_f32_16x16x32_bf16 v[48:51], v[156:159], v[164:167], v[48:51]
	v_mfma_f32_16x16x32_bf16 v[32:35], v[156:159], v[188:191], v[32:35]
	v_mfma_f32_16x16x32_bf16 v[36:39], v[144:147], v[188:191], v[36:39]
	v_mfma_f32_16x16x32_bf16 v[20:23], v[144:147], v[196:199], v[20:23]
	v_mfma_f32_16x16x32_bf16 v[16:19], v[156:159], v[196:199], v[16:19]
	v_mfma_f32_16x16x32_bf16 v[0:3], v[156:159], v[204:207], v[0:3]
	v_mfma_f32_16x16x32_bf16 v[4:7], v[144:147], v[204:207], v[4:7]
	v_mfma_f32_16x16x32_bf16 v[52:55], v[148:151], v[168:171], v[52:55]
	v_mfma_f32_16x16x32_bf16 v[48:51], v[160:163], v[168:171], v[48:51]
	v_mfma_f32_16x16x32_bf16 v[32:35], v[160:163], v[192:195], v[32:35]
	v_mfma_f32_16x16x32_bf16 v[36:39], v[148:151], v[192:195], v[36:39]
	v_mfma_f32_16x16x32_bf16 v[20:23], v[148:151], v[200:203], v[20:23]
	v_mfma_f32_16x16x32_bf16 v[16:19], v[160:163], v[200:203], v[16:19]
	v_mfma_f32_16x16x32_bf16 v[0:3], v[160:163], v[208:211], v[0:3]
	v_mfma_f32_16x16x32_bf16 v[4:7], v[148:151], v[208:211], v[4:7]
	s_barrier
	ds_read_b128 v[112:115], v184
	ds_read_b128 v[116:119], v184 offset:1024
	ds_read_b128 v[136:139], v184 offset:2048
	ds_read_b128 v[140:143], v184 offset:3072
	ds_read_b128 v[144:147], v185
	ds_read_b128 v[148:151], v185 offset:1024
	ds_read_b128 v[156:159], v185 offset:2048
	ds_read_b128 v[160:163], v185 offset:3072
	ds_read_b128 v[164:167], v183 offset:32768
	ds_read_b128 v[168:171], v183 offset:33792
	ds_read_b128 v[188:191], v183 offset:34816
	ds_read_b128 v[192:195], v183 offset:35840
	ds_read_b128 v[196:199], v183 offset:36864
	ds_read_b128 v[200:203], v183 offset:37888
	ds_read_b128 v[204:207], v183 offset:38912
	ds_read_b128 v[208:211], v183 offset:39936
	s_add_u32 s28, s28, 0x160000
	s_addc_u32 s29, s29, 0
	s_add_i32 m0, s36, 0x4000
	s_nop 0
	global_load_lds_dwordx4 v175, s[28:29]
	s_nop 0
	s_add_i32 m0, s36, 0x6000
	s_nop 0
	global_load_lds_dwordx4 v177, s[28:29]
	s_waitcnt vmcnt(8)
	s_waitcnt lgkmcnt(0)
	s_barrier
	v_mfma_f32_16x16x32_bf16 v[132:135], v[112:115], v[164:167], v[132:135]
	v_mfma_f32_16x16x32_bf16 v[128:131], v[136:139], v[164:167], v[128:131]
	v_mfma_f32_16x16x32_bf16 v[104:107], v[136:139], v[188:191], v[104:107]
	v_mfma_f32_16x16x32_bf16 v[108:111], v[112:115], v[188:191], v[108:111]
	v_mfma_f32_16x16x32_bf16 v[92:95], v[112:115], v[196:199], v[92:95]
	v_mfma_f32_16x16x32_bf16 v[88:91], v[136:139], v[196:199], v[88:91]
	v_mfma_f32_16x16x32_bf16 v[72:75], v[136:139], v[204:207], v[72:75]
	v_mfma_f32_16x16x32_bf16 v[76:79], v[112:115], v[204:207], v[76:79]
	v_mfma_f32_16x16x32_bf16 v[132:135], v[116:119], v[168:171], v[132:135]
	v_mfma_f32_16x16x32_bf16 v[128:131], v[140:143], v[168:171], v[128:131]
	v_mfma_f32_16x16x32_bf16 v[104:107], v[140:143], v[192:195], v[104:107]
	v_mfma_f32_16x16x32_bf16 v[108:111], v[116:119], v[192:195], v[108:111]
	v_mfma_f32_16x16x32_bf16 v[92:95], v[116:119], v[200:203], v[92:95]
	v_mfma_f32_16x16x32_bf16 v[88:91], v[140:143], v[200:203], v[88:91]
	v_mfma_f32_16x16x32_bf16 v[72:75], v[140:143], v[208:211], v[72:75]
	v_mfma_f32_16x16x32_bf16 v[76:79], v[116:119], v[208:211], v[76:79]
	v_mfma_f32_16x16x32_bf16 v[124:127], v[144:147], v[164:167], v[124:127]
	v_mfma_f32_16x16x32_bf16 v[120:123], v[156:159], v[164:167], v[120:123]
	v_mfma_f32_16x16x32_bf16 v[96:99], v[156:159], v[188:191], v[96:99]
	v_mfma_f32_16x16x32_bf16 v[100:103], v[144:147], v[188:191], v[100:103]
	v_mfma_f32_16x16x32_bf16 v[84:87], v[144:147], v[196:199], v[84:87]
	v_mfma_f32_16x16x32_bf16 v[80:83], v[156:159], v[196:199], v[80:83]
	v_mfma_f32_16x16x32_bf16 v[64:67], v[156:159], v[204:207], v[64:67]
	v_mfma_f32_16x16x32_bf16 v[68:71], v[144:147], v[204:207], v[68:71]
	v_mfma_f32_16x16x32_bf16 v[124:127], v[148:151], v[168:171], v[124:127]
	v_mfma_f32_16x16x32_bf16 v[120:123], v[160:163], v[168:171], v[120:123]
	v_mfma_f32_16x16x32_bf16 v[96:99], v[160:163], v[192:195], v[96:99]
	v_mfma_f32_16x16x32_bf16 v[100:103], v[148:151], v[192:195], v[100:103]
	v_mfma_f32_16x16x32_bf16 v[84:87], v[148:151], v[200:203], v[84:87]
	v_mfma_f32_16x16x32_bf16 v[80:83], v[160:163], v[200:203], v[80:83]
	v_mfma_f32_16x16x32_bf16 v[64:67], v[160:163], v[208:211], v[64:67]
	v_mfma_f32_16x16x32_bf16 v[68:71], v[148:151], v[208:211], v[68:71]
	s_barrier
	ds_read_b128 v[164:167], v183 offset:49152
	ds_read_b128 v[168:171], v183 offset:50176
	ds_read_b128 v[188:191], v183 offset:51200
	ds_read_b128 v[192:195], v183 offset:52224
	ds_read_b128 v[196:199], v183 offset:53248
	ds_read_b128 v[200:203], v183 offset:54272
	ds_read_b128 v[204:207], v183 offset:55296
	ds_read_b128 v[208:211], v183 offset:56320
	s_add_i32 m0, s36, 0x18000
	s_nop 0
	global_load_lds_dwordx4 v176, s[26:27]
	s_nop 0
	s_add_i32 m0, s36, 0x1a000
	s_nop 0
	global_load_lds_dwordx4 v178, s[26:27]
	s_add_u32 s24, s24, 0x160080
	s_addc_u32 s25, s25, 0
	s_add_i32 m0, s36, 0x1c000
	s_nop 0
	global_load_lds_dwordx4 v176, s[24:25]
	s_nop 0
	s_add_i32 m0, s36, 0x1e000
	s_nop 0
	global_load_lds_dwordx4 v178, s[24:25]
	s_nop 0
	s_add_i32 m0, s36, 0x8000
	s_nop 0
	global_load_lds_dwordx4 v175, s[22:23]
	s_nop 0
	s_add_i32 m0, s36, 0xa000
	s_nop 0
	global_load_lds_dwordx4 v177, s[22:23]
	s_waitcnt vmcnt(8)
	s_waitcnt lgkmcnt(0)
	s_barrier
	v_mfma_f32_16x16x32_bf16 v[60:63], v[112:115], v[164:167], v[60:63]
	v_mfma_f32_16x16x32_bf16 v[56:59], v[136:139], v[164:167], v[56:59]
	v_mfma_f32_16x16x32_bf16 v[40:43], v[136:139], v[188:191], v[40:43]
	v_mfma_f32_16x16x32_bf16 v[44:47], v[112:115], v[188:191], v[44:47]
	v_mfma_f32_16x16x32_bf16 v[28:31], v[112:115], v[196:199], v[28:31]
	v_mfma_f32_16x16x32_bf16 v[24:27], v[136:139], v[196:199], v[24:27]
	v_mfma_f32_16x16x32_bf16 v[8:11], v[136:139], v[204:207], v[8:11]
	v_mfma_f32_16x16x32_bf16 v[12:15], v[112:115], v[204:207], v[12:15]
	v_mfma_f32_16x16x32_bf16 v[60:63], v[116:119], v[168:171], v[60:63]
	v_mfma_f32_16x16x32_bf16 v[56:59], v[140:143], v[168:171], v[56:59]
	v_mfma_f32_16x16x32_bf16 v[40:43], v[140:143], v[192:195], v[40:43]
	v_mfma_f32_16x16x32_bf16 v[44:47], v[116:119], v[192:195], v[44:47]
	v_mfma_f32_16x16x32_bf16 v[28:31], v[116:119], v[200:203], v[28:31]
	v_mfma_f32_16x16x32_bf16 v[24:27], v[140:143], v[200:203], v[24:27]
	v_mfma_f32_16x16x32_bf16 v[8:11], v[140:143], v[208:211], v[8:11]
	v_mfma_f32_16x16x32_bf16 v[12:15], v[116:119], v[208:211], v[12:15]
	v_mfma_f32_16x16x32_bf16 v[52:55], v[144:147], v[164:167], v[52:55]
	v_mfma_f32_16x16x32_bf16 v[48:51], v[156:159], v[164:167], v[48:51]
	v_mfma_f32_16x16x32_bf16 v[32:35], v[156:159], v[188:191], v[32:35]
	v_mfma_f32_16x16x32_bf16 v[36:39], v[144:147], v[188:191], v[36:39]
	v_mfma_f32_16x16x32_bf16 v[20:23], v[144:147], v[196:199], v[20:23]
	v_mfma_f32_16x16x32_bf16 v[16:19], v[156:159], v[196:199], v[16:19]
	v_mfma_f32_16x16x32_bf16 v[0:3], v[156:159], v[204:207], v[0:3]
	v_mfma_f32_16x16x32_bf16 v[4:7], v[144:147], v[204:207], v[4:7]
	v_mfma_f32_16x16x32_bf16 v[52:55], v[148:151], v[168:171], v[52:55]
	v_mfma_f32_16x16x32_bf16 v[48:51], v[160:163], v[168:171], v[48:51]
	v_mfma_f32_16x16x32_bf16 v[32:35], v[160:163], v[192:195], v[32:35]
	v_mfma_f32_16x16x32_bf16 v[36:39], v[148:151], v[192:195], v[36:39]
	v_mfma_f32_16x16x32_bf16 v[20:23], v[148:151], v[200:203], v[20:23]
	v_mfma_f32_16x16x32_bf16 v[16:19], v[160:163], v[200:203], v[16:19]
	v_mfma_f32_16x16x32_bf16 v[0:3], v[160:163], v[208:211], v[0:3]
	v_mfma_f32_16x16x32_bf16 v[4:7], v[148:151], v[208:211], v[4:7]
	s_barrier
	s_add_i32 s55, s55, 2
	s_add_u32 s51, s51, 0x100
	s_addc_u32 s52, s52, 0
	s_add_u32 s53, s53, 0x100
	s_addc_u32 s54, s54, 0
	s_add_u32 s6, s6, 0x100
	s_addc_u32 s7, s7, 0
	s_cmpk_gt_u32 s55, 0x55
	s_cbranch_scc0 .LBB0_838
	s_and_b64 vcc, exec, s[16:17]
	s_cbranch_vccz .LBB0_841
	s_barrier

.LBB0_930:
	s_ashr_i32 s37, s36, 31
	s_lshl_b64 s[38:39], s[36:37], 19
	s_add_u32 s38, s19, s38
	s_addc_u32 s39, s21, s39
	s_and_b64 s[40:41], s[4:5], exec
	s_cselect_b32 s9, s39, s45
	s_cselect_b32 s76, s38, s44
	s_ashr_i32 s35, s34, 31
	s_lshl_b64 s[40:41], s[34:35], 19
	s_add_u32 s40, s23, s40
	s_addc_u32 s41, s25, s41
	s_and_b64 s[46:47], s[4:5], exec
	ds_read_b128 v[0:3], v226 offset:3072
	ds_read_b128 v[4:7], v226 offset:2048
	ds_read_b128 v[8:11], v226 offset:1024
	ds_read_b128 v[12:15], v226
	ds_read_b128 v[16:19], v227 offset:3072
	ds_read_b128 v[20:23], v227 offset:2048
	ds_read_b128 v[24:27], v227 offset:1024
	ds_read_b128 v[28:31], v227
	s_cselect_b32 s35, s41, s43
	s_cselect_b32 s77, s40, s42
	s_lshl_b32 s46, s78, 11
	s_and_b32 s46, s46, 0x800
	s_or_b32 s54, s46, s56
	s_lshl_b64 s[48:49], s[36:37], 11
	s_add_u32 s46, s44, 0x100
	s_addc_u32 s47, s45, 0
	s_add_u32 s80, s42, 0x100
	s_addc_u32 s81, s43, 0
	s_add_u32 s50, s44, 0x180
	s_addc_u32 s51, s45, 0
	s_add_u32 s52, s42, 0x180
	s_addc_u32 s53, s43, 0
	ds_read_b128 v[32:35], v228
	ds_read_b128 v[36:39], v228 offset:1024
	ds_read_b128 v[40:43], v228 offset:2048
	ds_read_b128 v[44:47], v228 offset:3072
	ds_read_b128 v[48:51], v228 offset:4096
	ds_read_b128 v[52:55], v228 offset:5120
	ds_read_b128 v[56:59], v228 offset:6144
	ds_read_b128 v[60:63], v228 offset:7168
	s_add_u32 s82, s44, 0x40080
	s_addc_u32 s83, s45, 0
	s_add_i32 m0, s31, 0xc000
	s_nop 0
	global_load_lds_dwordx4 v219, s[82:83]
	s_nop 0
	s_add_i32 m0, s31, 0xe000
	s_nop 0
	global_load_lds_dwordx4 v221, s[82:83]
	s_waitcnt vmcnt(8)
	s_waitcnt lgkmcnt(0)
	s_barrier
	s_waitcnt lgkmcnt(7)
	v_mfma_i32_16x16x64_i8 v[64:67], v[28:31], v[32:35], 0
	s_mov_b32 s37, 0
	v_mfma_i32_16x16x64_i8 v[68:71], v[20:23], v[32:35], 0
	s_waitcnt lgkmcnt(5)
	v_mfma_i32_16x16x64_i8 v[72:75], v[28:31], v[40:43], 0
	v_mfma_i32_16x16x64_i8 v[76:79], v[20:23], v[40:43], 0
	s_waitcnt lgkmcnt(3)
	v_mfma_i32_16x16x64_i8 v[80:83], v[28:31], v[48:51], 0
	v_mfma_i32_16x16x64_i8 v[84:87], v[20:23], v[48:51], 0
	s_waitcnt lgkmcnt(1)
	v_mfma_i32_16x16x64_i8 v[92:95], v[20:23], v[56:59], 0
	v_mfma_i32_16x16x64_i8 v[136:139], v[24:27], v[36:39], v[64:67]
	v_mfma_i32_16x16x64_i8 v[148:151], v[24:27], v[44:47], v[72:75]
	v_mfma_i32_16x16x64_i8 v[144:147], v[16:19], v[36:39], v[68:71]
	v_mfma_i32_16x16x64_i8 v[76:79], v[16:19], v[44:47], v[76:79]
	v_mfma_i32_16x16x64_i8 v[80:83], v[24:27], v[52:55], v[80:83]
	v_mfma_i32_16x16x64_i8 v[88:91], v[28:31], v[56:59], 0
	v_mfma_i32_16x16x64_i8 v[84:87], v[16:19], v[52:55], v[84:87]
	s_waitcnt lgkmcnt(0)
	v_mfma_i32_16x16x64_i8 v[92:95], v[16:19], v[60:63], v[92:95]
	v_mfma_i32_16x16x64_i8 v[88:91], v[24:27], v[60:63], v[88:91]
	v_mfma_i32_16x16x64_i8 v[96:99], v[12:15], v[32:35], 0
	v_mfma_i32_16x16x64_i8 v[32:35], v[4:7], v[32:35], 0
	v_mfma_i32_16x16x64_i8 v[96:99], v[8:11], v[36:39], v[96:99]
	v_mfma_i32_16x16x64_i8 v[32:35], v[0:3], v[36:39], v[32:35]
	v_mfma_i32_16x16x64_i8 v[36:39], v[12:15], v[40:43], 0
	v_mfma_i32_16x16x64_i8 v[40:43], v[4:7], v[40:43], 0
	v_mfma_i32_16x16x64_i8 v[36:39], v[8:11], v[44:47], v[36:39]
	v_mfma_i32_16x16x64_i8 v[40:43], v[0:3], v[44:47], v[40:43]
	v_mfma_i32_16x16x64_i8 v[44:47], v[12:15], v[48:51], 0
	v_mfma_i32_16x16x64_i8 v[48:51], v[4:7], v[48:51], 0
	v_mfma_i32_16x16x64_i8 v[44:47], v[8:11], v[52:55], v[44:47]
	v_mfma_i32_16x16x64_i8 v[48:51], v[0:3], v[52:55], v[48:51]
	v_mfma_i32_16x16x64_i8 v[52:55], v[12:15], v[56:59], 0
	v_mfma_i32_16x16x64_i8 v[56:59], v[4:7], v[56:59], 0
	v_mfma_i32_16x16x64_i8 v[52:55], v[8:11], v[60:63], v[52:55]
	v_mfma_i32_16x16x64_i8 v[56:59], v[0:3], v[60:63], v[56:59]
	s_barrier
	ds_read_b128 v[60:63], v228 offset:16384
	ds_read_b128 v[100:103], v228 offset:17408
	ds_read_b128 v[104:107], v228 offset:18432
	ds_read_b128 v[108:111], v228 offset:19456
	ds_read_b128 v[112:115], v228 offset:20480
	ds_read_b128 v[116:119], v228 offset:21504
	ds_read_b128 v[120:123], v228 offset:22528
	ds_read_b128 v[124:127], v228 offset:23552
	s_add_i32 m0, s31, 0x10000
	s_nop 0
	global_load_lds_dwordx4 v220, s[80:81]
	s_nop 0
	s_add_i32 m0, s31, 0x12000
	s_nop 0
	global_load_lds_dwordx4 v222, s[80:81]
	s_add_u32 s80, s42, 0x40100
	s_addc_u32 s81, s43, 0
	s_add_i32 m0, s31, 0x14000
	s_nop 0
	global_load_lds_dwordx4 v220, s[80:81]
	s_nop 0
	s_add_i32 m0, s31, 0x16000
	s_nop 0
	global_load_lds_dwordx4 v222, s[80:81]
	s_nop 0
	s_add_i32 m0, s31, 0
	s_nop 0
	global_load_lds_dwordx4 v219, s[46:47]
	s_nop 0
	s_add_i32 m0, s31, 0x2000
	s_nop 0
	global_load_lds_dwordx4 v221, s[46:47]
	s_waitcnt vmcnt(8)
	s_waitcnt lgkmcnt(0)
	s_barrier
	v_mfma_i32_16x16x64_i8 v[132:135], v[20:23], v[60:63], 0
	v_mfma_i32_16x16x64_i8 v[168:171], v[16:19], v[100:103], v[132:135]
	v_mfma_i32_16x16x64_i8 v[132:135], v[28:31], v[104:107], 0
	v_mfma_i32_16x16x64_i8 v[204:207], v[24:27], v[108:111], v[132:135]
	v_mfma_i32_16x16x64_i8 v[132:135], v[20:23], v[104:107], 0
	v_mfma_i32_16x16x64_i8 v[128:131], v[28:31], v[60:63], 0
	v_mfma_i32_16x16x64_i8 v[214:217], v[16:19], v[108:111], v[132:135]
	v_mfma_i32_16x16x64_i8 v[132:135], v[28:31], v[112:115], 0
	v_mfma_i32_16x16x64_i8 v[128:131], v[24:27], v[100:103], v[128:131]
	v_mfma_i32_16x16x64_i8 v[232:235], v[24:27], v[116:119], v[132:135]
	v_mfma_i32_16x16x64_i8 v[132:135], v[20:23], v[112:115], 0
	v_mfma_i32_16x16x64_i8 v[28:31], v[28:31], v[120:123], 0
	v_mfma_i32_16x16x64_i8 v[20:23], v[20:23], v[120:123], 0
	v_mfma_i32_16x16x64_i8 v[236:239], v[16:19], v[116:119], v[132:135]
	v_mfma_i32_16x16x64_i8 v[24:27], v[24:27], v[124:127], v[28:31]
	v_mfma_i32_16x16x64_i8 v[16:19], v[16:19], v[124:127], v[20:23]
	v_mfma_i32_16x16x64_i8 v[20:23], v[12:15], v[60:63], 0
	v_mfma_i32_16x16x64_i8 v[28:31], v[4:7], v[60:63], 0
	v_mfma_i32_16x16x64_i8 v[20:23], v[8:11], v[100:103], v[20:23]
	v_mfma_i32_16x16x64_i8 v[28:31], v[0:3], v[100:103], v[28:31]
	v_mfma_i32_16x16x64_i8 v[60:63], v[12:15], v[104:107], 0
	v_mfma_i32_16x16x64_i8 v[100:103], v[4:7], v[104:107], 0
	v_mfma_i32_16x16x64_i8 v[104:107], v[12:15], v[112:115], 0
	v_mfma_i32_16x16x64_i8 v[100:103], v[0:3], v[108:111], v[100:103]
	v_mfma_i32_16x16x64_i8 v[240:243], v[8:11], v[116:119], v[104:107]
	v_mfma_i32_16x16x64_i8 v[104:107], v[4:7], v[112:115], 0
	v_mfma_i32_16x16x64_i8 v[12:15], v[12:15], v[120:123], 0
	v_mfma_i32_16x16x64_i8 v[4:7], v[4:7], v[120:123], 0
	v_mfma_i32_16x16x64_i8 v[60:63], v[8:11], v[108:111], v[60:63]
	v_mfma_i32_16x16x64_i8 v[244:247], v[0:3], v[116:119], v[104:107]
	v_mfma_i32_16x16x64_i8 v[8:11], v[8:11], v[124:127], v[12:15]
	v_mfma_i32_16x16x64_i8 v[0:3], v[0:3], v[124:127], v[4:7]
	s_barrier
	s_nop 1
	ds_read_b128 v[4:7], v229
	ds_read_b128 v[12:15], v229 offset:1024
	ds_read_b128 v[104:107], v229 offset:2048
	ds_read_b128 v[116:119], v229 offset:3072
	ds_read_b128 v[124:127], v230
	ds_read_b128 v[248:251], v230 offset:1024
	ds_read_b128 v[208:211], v230 offset:2048
	ds_read_b128 v[64:67], v230 offset:3072
	ds_read_b128 v[108:111], v228 offset:32768
	ds_read_b128 v[112:115], v228 offset:33792
	ds_read_b128 v[120:123], v228 offset:34816
	ds_read_b128 v[132:135], v228 offset:35840
	ds_read_b128 v[140:143], v228 offset:36864
	ds_read_b128 v[152:155], v228 offset:37888
	ds_read_b128 v[68:71], v228 offset:38912
	ds_read_b128 v[72:75], v228 offset:39936
	s_add_u32 s44, s44, 0x40100
	s_addc_u32 s45, s45, 0
	s_add_i32 m0, s31, 0x4000
	s_nop 0
	global_load_lds_dwordx4 v219, s[44:45]
	s_nop 0
	s_add_i32 m0, s31, 0x6000
	s_nop 0
	global_load_lds_dwordx4 v221, s[44:45]
	s_waitcnt vmcnt(8)
	s_waitcnt lgkmcnt(0)
	s_barrier
	v_mfma_i32_16x16x64_i8 v[76:79], v[104:107], v[120:123], v[76:79]
	v_mfma_i32_16x16x64_i8 v[180:183], v[116:119], v[132:135], v[76:79]
	v_mfma_i32_16x16x64_i8 v[76:79], v[4:7], v[140:143], v[80:83]
	v_mfma_i32_16x16x64_i8 v[136:139], v[4:7], v[108:111], v[136:139]
	v_mfma_i32_16x16x64_i8 v[164:167], v[12:15], v[152:155], v[76:79]
	v_mfma_i32_16x16x64_i8 v[76:79], v[104:107], v[140:143], v[84:87]
	v_mfma_i32_16x16x64_i8 v[200:203], v[12:15], v[112:115], v[136:139]
	v_mfma_i32_16x16x64_i8 v[136:139], v[104:107], v[108:111], v[144:147]
	v_mfma_i32_16x16x64_i8 v[160:163], v[116:119], v[152:155], v[76:79]
	v_mfma_i32_16x16x64_i8 v[76:79], v[4:7], v[68:71], v[88:91]
	v_mfma_i32_16x16x64_i8 v[196:199], v[116:119], v[112:115], v[136:139]
	v_mfma_i32_16x16x64_i8 v[136:139], v[4:7], v[120:123], v[148:151]
	v_mfma_i32_16x16x64_i8 v[148:151], v[12:15], v[72:75], v[76:79]
	v_mfma_i32_16x16x64_i8 v[76:79], v[104:107], v[68:71], v[92:95]
	v_mfma_i32_16x16x64_i8 v[184:187], v[12:15], v[132:135], v[136:139]
	v_mfma_i32_16x16x64_i8 v[144:147], v[116:119], v[72:75], v[76:79]
	v_mfma_i32_16x16x64_i8 v[32:35], v[208:211], v[108:111], v[32:35]
	v_mfma_i32_16x16x64_i8 v[188:191], v[64:67], v[112:115], v[32:35]
	v_mfma_i32_16x16x64_i8 v[32:35], v[124:127], v[120:123], v[36:39]
	v_mfma_i32_16x16x64_i8 v[176:179], v[248:251], v[132:135], v[32:35]
	v_mfma_i32_16x16x64_i8 v[32:35], v[208:211], v[120:123], v[40:43]
	v_mfma_i32_16x16x64_i8 v[172:175], v[64:67], v[132:135], v[32:35]
	v_mfma_i32_16x16x64_i8 v[32:35], v[124:127], v[140:143], v[44:47]
	v_mfma_i32_16x16x64_i8 v[156:159], v[248:251], v[152:155], v[32:35]
	v_mfma_i32_16x16x64_i8 v[32:35], v[208:211], v[140:143], v[48:51]
	v_mfma_i32_16x16x64_i8 v[152:155], v[64:67], v[152:155], v[32:35]
	v_mfma_i32_16x16x64_i8 v[32:35], v[124:127], v[68:71], v[52:55]
	v_mfma_i32_16x16x64_i8 v[76:79], v[124:127], v[108:111], v[96:99]
	v_mfma_i32_16x16x64_i8 v[140:143], v[248:251], v[72:75], v[32:35]
	v_mfma_i32_16x16x64_i8 v[32:35], v[208:211], v[68:71], v[56:59]
	v_mfma_i32_16x16x64_i8 v[192:195], v[248:251], v[112:115], v[76:79]
	v_mfma_i32_16x16x64_i8 v[136:139], v[64:67], v[72:75], v[32:35]
	s_barrier
	s_nop 3
	ds_read_b128 v[32:35], v228 offset:49152
	ds_read_b128 v[36:39], v228 offset:50176
	ds_read_b128 v[40:43], v228 offset:51200
	ds_read_b128 v[44:47], v228 offset:52224
	ds_read_b128 v[48:51], v228 offset:53248
	ds_read_b128 v[52:55], v228 offset:54272
	ds_read_b128 v[56:59], v228 offset:55296
	ds_read_b128 v[88:91], v228 offset:56320
	s_add_i32 m0, s31, 0x18000
	s_nop 0
	global_load_lds_dwordx4 v220, s[52:53]
	s_nop 0
	s_add_i32 m0, s31, 0x1a000
	s_nop 0
	global_load_lds_dwordx4 v222, s[52:53]
	s_add_u32 s44, s42, 0x40180
	s_addc_u32 s45, s43, 0
	s_add_i32 m0, s31, 0x1c000
	s_nop 0
	global_load_lds_dwordx4 v220, s[44:45]
	s_nop 0
	s_add_i32 m0, s31, 0x1e000
	s_nop 0
	global_load_lds_dwordx4 v222, s[44:45]
	s_nop 0
	s_add_i32 m0, s31, 0x8000
	s_nop 0
	global_load_lds_dwordx4 v219, s[50:51]
	s_nop 0
	s_add_i32 m0, s31, 0xa000
	s_nop 0
	global_load_lds_dwordx4 v221, s[50:51]
	s_waitcnt vmcnt(8)
	s_waitcnt lgkmcnt(0)
	s_barrier
	v_mfma_i32_16x16x64_i8 v[68:71], v[4:7], v[32:35], v[128:131]
	v_mfma_i32_16x16x64_i8 v[132:135], v[12:15], v[36:39], v[68:71]
	v_mfma_i32_16x16x64_i8 v[68:71], v[104:107], v[32:35], v[168:171]
	v_mfma_i32_16x16x64_i8 v[128:131], v[116:119], v[36:39], v[68:71]
	v_mfma_i32_16x16x64_i8 v[68:71], v[4:7], v[40:43], v[204:207]
	v_mfma_i32_16x16x64_i8 v[112:115], v[12:15], v[44:47], v[68:71]
	v_mfma_i32_16x16x64_i8 v[68:71], v[104:107], v[40:43], v[214:217]
	v_mfma_i32_16x16x64_i8 v[108:111], v[116:119], v[44:47], v[68:71]
	v_mfma_i32_16x16x64_i8 v[68:71], v[4:7], v[48:51], v[232:235]
	v_mfma_i32_16x16x64_i8 v[4:7], v[4:7], v[56:59], v[24:27]
	v_mfma_i32_16x16x64_i8 v[96:99], v[12:15], v[52:55], v[68:71]
	v_mfma_i32_16x16x64_i8 v[68:71], v[104:107], v[48:51], v[236:239]
	v_mfma_i32_16x16x64_i8 v[76:79], v[12:15], v[88:91], v[4:7]
	v_mfma_i32_16x16x64_i8 v[4:7], v[104:107], v[56:59], v[16:19]
	v_mfma_i32_16x16x64_i8 v[92:95], v[116:119], v[52:55], v[68:71]
	v_mfma_i32_16x16x64_i8 v[72:75], v[116:119], v[88:91], v[4:7]
	v_mfma_i32_16x16x64_i8 v[4:7], v[124:127], v[32:35], v[20:23]
	v_mfma_i32_16x16x64_i8 v[120:123], v[248:251], v[36:39], v[4:7]
	v_mfma_i32_16x16x64_i8 v[4:7], v[208:211], v[32:35], v[28:31]
	v_mfma_i32_16x16x64_i8 v[116:119], v[64:67], v[36:39], v[4:7]
	v_mfma_i32_16x16x64_i8 v[4:7], v[124:127], v[40:43], v[60:63]
	v_mfma_i32_16x16x64_i8 v[104:107], v[248:251], v[44:47], v[4:7]
	v_mfma_i32_16x16x64_i8 v[4:7], v[208:211], v[40:43], v[100:103]
	v_mfma_i32_16x16x64_i8 v[100:103], v[64:67], v[44:47], v[4:7]
	v_mfma_i32_16x16x64_i8 v[4:7], v[124:127], v[48:51], v[240:243]
	v_mfma_i32_16x16x64_i8 v[84:87], v[248:251], v[52:55], v[4:7]
	v_mfma_i32_16x16x64_i8 v[4:7], v[208:211], v[48:51], v[244:247]
	v_mfma_i32_16x16x64_i8 v[80:83], v[64:67], v[52:55], v[4:7]
	v_mfma_i32_16x16x64_i8 v[4:7], v[124:127], v[56:59], v[8:11]
	v_mfma_i32_16x16x64_i8 v[0:3], v[208:211], v[56:59], v[0:3]
	v_mfma_i32_16x16x64_i8 v[68:71], v[248:251], v[88:91], v[4:7]
	v_mfma_i32_16x16x64_i8 v[64:67], v[64:67], v[88:91], v[0:3]
	s_barrier
	s_add_u32 s44, s27, s48
	s_addc_u32 s45, s29, s49
	s_add_u32 s79, s42, 0x200
	s_addc_u32 s80, s43, 0
	s_add_i32 s81, s54, 0
	s_add_i32 s81, s81, 0x20000

.LBB0_933:
	ds_read_b128 v[0:3], v227
	ds_read_b128 v[4:7], v227 offset:1024
	ds_read_b128 v[8:11], v227 offset:2048
	ds_read_b128 v[12:15], v227 offset:3072
	ds_read_b128 v[16:19], v226
	ds_read_b128 v[20:23], v226 offset:1024
	ds_read_b128 v[24:27], v226 offset:2048
	ds_read_b128 v[28:31], v226 offset:3072
	s_add_u32 s42, s46, 0x100
	s_addc_u32 s43, s47, 0
	s_and_b64 s[48:49], s[48:49], exec
	s_cselect_b32 s54, s76, s42
	s_cselect_b32 s55, s9, s43
	s_cselect_b32 s51, s35, s80
	s_cselect_b32 s50, s77, s79
	s_add_u32 s48, s54, 0x80
	s_addc_u32 s49, s55, 0
	s_add_u32 s52, s50, 0x80
	s_addc_u32 s53, s51, 0
	ds_read_b128 v[32:35], v228
	ds_read_b128 v[36:39], v228 offset:1024
	ds_read_b128 v[40:43], v228 offset:2048
	ds_read_b128 v[44:47], v228 offset:3072
	ds_read_b128 v[48:51], v228 offset:4096
	ds_read_b128 v[52:55], v228 offset:5120
	ds_read_b128 v[56:59], v228 offset:6144
	ds_read_b128 v[60:63], v228 offset:7168
	s_add_u32 s46, s46, 0x40080
	s_addc_u32 s47, s47, 0
	s_add_i32 m0, s31, 0xc000
	s_nop 0
	global_load_lds_dwordx4 v219, s[46:47]
	s_nop 0
	s_add_i32 m0, s31, 0xe000
	s_nop 0
	global_load_lds_dwordx4 v221, s[46:47]
	s_waitcnt vmcnt(8)
	s_waitcnt lgkmcnt(0)
	s_barrier
	v_mfma_i32_16x16x64_i8 v[180:183], v[8:11], v[40:43], v[180:183]
	v_mfma_i32_16x16x64_i8 v[164:167], v[0:3], v[48:51], v[164:167]
	v_mfma_i32_16x16x64_i8 v[148:151], v[0:3], v[56:59], v[148:151]
	v_mfma_i32_16x16x64_i8 v[160:163], v[8:11], v[48:51], v[160:163]
	v_mfma_i32_16x16x64_i8 v[144:147], v[8:11], v[56:59], v[144:147]
	v_mfma_i32_16x16x64_i8 v[88:91], v[0:3], v[32:35], v[200:203]
	v_mfma_i32_16x16x64_i8 v[168:171], v[0:3], v[40:43], v[184:187]
	v_mfma_i32_16x16x64_i8 v[124:127], v[8:11], v[32:35], v[196:199]
	v_mfma_i32_16x16x64_i8 v[180:183], v[12:15], v[44:47], v[180:183]
	v_mfma_i32_16x16x64_i8 v[164:167], v[4:7], v[52:55], v[164:167]
	v_mfma_i32_16x16x64_i8 v[148:151], v[4:7], v[60:63], v[148:151]
	v_mfma_i32_16x16x64_i8 v[160:163], v[12:15], v[52:55], v[160:163]
	v_mfma_i32_16x16x64_i8 v[144:147], v[12:15], v[60:63], v[144:147]
	v_mfma_i32_16x16x64_i8 v[88:91], v[4:7], v[36:39], v[88:91]
	v_mfma_i32_16x16x64_i8 v[168:171], v[4:7], v[44:47], v[168:171]
	v_mfma_i32_16x16x64_i8 v[124:127], v[12:15], v[36:39], v[124:127]
	v_mfma_i32_16x16x64_i8 v[184:187], v[16:19], v[32:35], v[192:195]
	v_mfma_i32_16x16x64_i8 v[32:35], v[24:27], v[32:35], v[188:191]
	v_mfma_i32_16x16x64_i8 v[192:195], v[20:23], v[36:39], v[184:187]
	v_mfma_i32_16x16x64_i8 v[32:35], v[28:31], v[36:39], v[32:35]
	v_mfma_i32_16x16x64_i8 v[36:39], v[16:19], v[40:43], v[176:179]
	v_mfma_i32_16x16x64_i8 v[40:43], v[24:27], v[40:43], v[172:175]
	v_mfma_i32_16x16x64_i8 v[36:39], v[20:23], v[44:47], v[36:39]
	v_mfma_i32_16x16x64_i8 v[40:43], v[28:31], v[44:47], v[40:43]
	v_mfma_i32_16x16x64_i8 v[44:47], v[16:19], v[48:51], v[156:159]
	v_mfma_i32_16x16x64_i8 v[48:51], v[24:27], v[48:51], v[152:155]
	v_mfma_i32_16x16x64_i8 v[44:47], v[20:23], v[52:55], v[44:47]
	v_mfma_i32_16x16x64_i8 v[48:51], v[28:31], v[52:55], v[48:51]
	v_mfma_i32_16x16x64_i8 v[52:55], v[16:19], v[56:59], v[140:143]
	v_mfma_i32_16x16x64_i8 v[56:59], v[24:27], v[56:59], v[136:139]
	v_mfma_i32_16x16x64_i8 v[52:55], v[20:23], v[60:63], v[52:55]
	v_mfma_i32_16x16x64_i8 v[56:59], v[28:31], v[60:63], v[56:59]
	s_barrier
	ds_read_b128 v[60:63], v228 offset:16384
	ds_read_b128 v[136:139], v228 offset:17408
	ds_read_b128 v[140:143], v228 offset:18432
	ds_read_b128 v[152:155], v228 offset:19456
	ds_read_b128 v[156:159], v228 offset:20480
	ds_read_b128 v[172:175], v228 offset:21504
	ds_read_b128 v[176:179], v228 offset:22528
	ds_read_b128 v[184:187], v228 offset:23552
	s_add_i32 m0, s31, 0x10000
	s_nop 0
	global_load_lds_dwordx4 v220, s[50:51]
	s_nop 0
	s_add_i32 m0, s31, 0x12000
	s_nop 0
	global_load_lds_dwordx4 v222, s[50:51]
	s_add_u32 s46, s50, 0x40000
	s_addc_u32 s47, s51, 0
	s_add_i32 m0, s31, 0x14000
	s_nop 0
	global_load_lds_dwordx4 v220, s[46:47]
	s_nop 0
	s_add_i32 m0, s31, 0x16000
	s_nop 0
	global_load_lds_dwordx4 v222, s[46:47]
	s_nop 0
	s_add_i32 m0, s31, 0
	s_nop 0
	global_load_lds_dwordx4 v219, s[54:55]
	s_nop 0
	s_add_i32 m0, s31, 0x2000
	s_nop 0
	global_load_lds_dwordx4 v221, s[54:55]
	s_waitcnt vmcnt(8)
	s_waitcnt lgkmcnt(0)
	s_barrier
	v_mfma_i32_16x16x64_i8 v[132:135], v[0:3], v[60:63], v[132:135]
	v_mfma_i32_16x16x64_i8 v[112:115], v[0:3], v[140:143], v[112:115]
	v_mfma_i32_16x16x64_i8 v[96:99], v[0:3], v[156:159], v[96:99]
	v_mfma_i32_16x16x64_i8 v[0:3], v[0:3], v[176:179], v[76:79]
	v_mfma_i32_16x16x64_i8 v[128:131], v[8:11], v[60:63], v[128:131]
	v_mfma_i32_16x16x64_i8 v[108:111], v[8:11], v[140:143], v[108:111]
	v_mfma_i32_16x16x64_i8 v[92:95], v[8:11], v[156:159], v[92:95]
	v_mfma_i32_16x16x64_i8 v[76:79], v[4:7], v[184:187], v[0:3]
	v_mfma_i32_16x16x64_i8 v[0:3], v[8:11], v[176:179], v[72:75]
	v_mfma_i32_16x16x64_i8 v[132:135], v[4:7], v[136:139], v[132:135]
	v_mfma_i32_16x16x64_i8 v[128:131], v[12:15], v[136:139], v[128:131]
	v_mfma_i32_16x16x64_i8 v[112:115], v[4:7], v[152:155], v[112:115]
	v_mfma_i32_16x16x64_i8 v[108:111], v[12:15], v[152:155], v[108:111]
	v_mfma_i32_16x16x64_i8 v[96:99], v[4:7], v[172:175], v[96:99]
	v_mfma_i32_16x16x64_i8 v[92:95], v[12:15], v[172:175], v[92:95]
	v_mfma_i32_16x16x64_i8 v[72:75], v[12:15], v[184:187], v[0:3]
	v_mfma_i32_16x16x64_i8 v[0:3], v[16:19], v[60:63], v[120:123]
	v_mfma_i32_16x16x64_i8 v[120:123], v[20:23], v[136:139], v[0:3]
	v_mfma_i32_16x16x64_i8 v[0:3], v[24:27], v[60:63], v[116:119]
	v_mfma_i32_16x16x64_i8 v[116:119], v[28:31], v[136:139], v[0:3]
	v_mfma_i32_16x16x64_i8 v[0:3], v[16:19], v[140:143], v[104:107]
	v_mfma_i32_16x16x64_i8 v[104:107], v[20:23], v[152:155], v[0:3]
	v_mfma_i32_16x16x64_i8 v[0:3], v[24:27], v[140:143], v[100:103]
	v_mfma_i32_16x16x64_i8 v[100:103], v[28:31], v[152:155], v[0:3]
	v_mfma_i32_16x16x64_i8 v[0:3], v[16:19], v[156:159], v[84:87]
	v_mfma_i32_16x16x64_i8 v[84:87], v[20:23], v[172:175], v[0:3]
	v_mfma_i32_16x16x64_i8 v[0:3], v[24:27], v[156:159], v[80:83]
	v_mfma_i32_16x16x64_i8 v[80:83], v[28:31], v[172:175], v[0:3]
	v_mfma_i32_16x16x64_i8 v[0:3], v[16:19], v[176:179], v[68:71]
	v_mfma_i32_16x16x64_i8 v[68:71], v[20:23], v[184:187], v[0:3]
	v_mfma_i32_16x16x64_i8 v[0:3], v[24:27], v[176:179], v[64:67]
	v_mfma_i32_16x16x64_i8 v[64:67], v[28:31], v[184:187], v[0:3]
	s_barrier
	ds_read_b128 v[16:19], v229
	ds_read_b128 v[8:11], v229 offset:1024
	ds_read_b128 v[4:7], v229 offset:2048
	s_nop 1
	ds_read_b128 v[0:3], v229 offset:3072
	ds_read_b128 v[28:31], v230
	ds_read_b128 v[24:27], v230 offset:1024
	ds_read_b128 v[20:23], v230 offset:2048
	ds_read_b128 v[12:15], v230 offset:3072
	ds_read_b128 v[60:63], v228 offset:32768
	ds_read_b128 v[136:139], v228 offset:33792
	ds_read_b128 v[140:143], v228 offset:34816
	ds_read_b128 v[152:155], v228 offset:35840
	ds_read_b128 v[204:207], v228 offset:36864
	ds_read_b128 v[208:211], v228 offset:37888
	ds_read_b128 v[214:217], v228 offset:38912
	ds_read_b128 v[232:235], v228 offset:39936
	s_add_u32 s46, s54, 0x40000
	s_addc_u32 s47, s55, 0
	s_add_i32 m0, s31, 0x4000
	s_nop 0
	global_load_lds_dwordx4 v219, s[46:47]
	s_nop 0
	s_add_i32 m0, s31, 0x6000
	s_nop 0
	global_load_lds_dwordx4 v221, s[46:47]
	s_waitcnt vmcnt(8)
	s_waitcnt lgkmcnt(0)
	s_barrier
	v_mfma_i32_16x16x64_i8 v[88:91], v[16:19], v[60:63], v[88:91]
	v_mfma_i32_16x16x64_i8 v[200:203], v[8:11], v[136:139], v[88:91]
	v_mfma_i32_16x16x64_i8 v[88:91], v[4:7], v[60:63], v[124:127]
	v_mfma_i32_16x16x64_i8 v[196:199], v[0:3], v[136:139], v[88:91]
	v_mfma_i32_16x16x64_i8 v[88:91], v[16:19], v[140:143], v[168:171]
	v_mfma_i32_16x16x64_i8 v[184:187], v[8:11], v[152:155], v[88:91]
	v_mfma_i32_16x16x64_i8 v[88:91], v[4:7], v[140:143], v[180:183]
	v_mfma_i32_16x16x64_i8 v[180:183], v[0:3], v[152:155], v[88:91]
	v_mfma_i32_16x16x64_i8 v[88:91], v[16:19], v[204:207], v[164:167]
	v_mfma_i32_16x16x64_i8 v[164:167], v[8:11], v[208:211], v[88:91]
	v_mfma_i32_16x16x64_i8 v[88:91], v[4:7], v[204:207], v[160:163]
	v_mfma_i32_16x16x64_i8 v[160:163], v[0:3], v[208:211], v[88:91]
	v_mfma_i32_16x16x64_i8 v[88:91], v[16:19], v[214:217], v[148:151]
	v_mfma_i32_16x16x64_i8 v[148:151], v[8:11], v[232:235], v[88:91]
	v_mfma_i32_16x16x64_i8 v[88:91], v[4:7], v[214:217], v[144:147]
	v_mfma_i32_16x16x64_i8 v[144:147], v[0:3], v[232:235], v[88:91]
	v_mfma_i32_16x16x64_i8 v[32:35], v[20:23], v[60:63], v[32:35]
	v_mfma_i32_16x16x64_i8 v[188:191], v[12:15], v[136:139], v[32:35]
	v_mfma_i32_16x16x64_i8 v[32:35], v[28:31], v[140:143], v[36:39]
	v_mfma_i32_16x16x64_i8 v[176:179], v[24:27], v[152:155], v[32:35]
	v_mfma_i32_16x16x64_i8 v[32:35], v[20:23], v[140:143], v[40:43]
	v_mfma_i32_16x16x64_i8 v[172:175], v[12:15], v[152:155], v[32:35]
	v_mfma_i32_16x16x64_i8 v[32:35], v[28:31], v[204:207], v[44:47]
	v_mfma_i32_16x16x64_i8 v[156:159], v[24:27], v[208:211], v[32:35]
	v_mfma_i32_16x16x64_i8 v[32:35], v[20:23], v[204:207], v[48:51]
	v_mfma_i32_16x16x64_i8 v[152:155], v[12:15], v[208:211], v[32:35]
	v_mfma_i32_16x16x64_i8 v[32:35], v[28:31], v[214:217], v[52:55]
	v_mfma_i32_16x16x64_i8 v[88:91], v[28:31], v[60:63], v[192:195]
	v_mfma_i32_16x16x64_i8 v[140:143], v[24:27], v[232:235], v[32:35]
	v_mfma_i32_16x16x64_i8 v[32:35], v[20:23], v[214:217], v[56:59]
	v_mfma_i32_16x16x64_i8 v[192:195], v[24:27], v[136:139], v[88:91]
	v_mfma_i32_16x16x64_i8 v[136:139], v[12:15], v[232:235], v[32:35]
	s_barrier
	ds_read_b128 v[60:63], v228 offset:49152
	ds_read_b128 v[56:59], v228 offset:50176
	ds_read_b128 v[52:55], v228 offset:51200
	ds_read_b128 v[48:51], v228 offset:52224
	ds_read_b128 v[44:47], v228 offset:53248
	ds_read_b128 v[40:43], v228 offset:54272
	ds_read_b128 v[36:39], v228 offset:55296
	ds_read_b128 v[32:35], v228 offset:56320
	s_add_i32 m0, s31, 0x18000
	s_nop 0
	global_load_lds_dwordx4 v220, s[52:53]
	s_nop 0
	s_add_i32 m0, s31, 0x1a000
	s_nop 0
	global_load_lds_dwordx4 v222, s[52:53]
	s_add_u32 s46, s50, 0x40080
	s_addc_u32 s47, s51, 0
	s_add_i32 m0, s31, 0x1c000
	s_nop 0
	global_load_lds_dwordx4 v220, s[46:47]
	s_nop 0
	s_add_i32 m0, s31, 0x1e000
	s_nop 0
	global_load_lds_dwordx4 v222, s[46:47]
	s_nop 0
	s_add_i32 m0, s31, 0x8000
	s_nop 0
	global_load_lds_dwordx4 v219, s[48:49]
	s_nop 0
	s_add_i32 m0, s31, 0xa000
	s_nop 0
	global_load_lds_dwordx4 v221, s[48:49]
	s_waitcnt vmcnt(8)
	s_waitcnt lgkmcnt(0)
	s_barrier
	v_mfma_i32_16x16x64_i8 v[88:91], v[16:19], v[60:63], v[132:135]
	v_mfma_i32_16x16x64_i8 v[132:135], v[8:11], v[56:59], v[88:91]
	v_mfma_i32_16x16x64_i8 v[88:91], v[4:7], v[60:63], v[128:131]
	v_mfma_i32_16x16x64_i8 v[128:131], v[0:3], v[56:59], v[88:91]
	v_mfma_i32_16x16x64_i8 v[88:91], v[16:19], v[52:55], v[112:115]
	v_mfma_i32_16x16x64_i8 v[112:115], v[8:11], v[48:51], v[88:91]
	v_mfma_i32_16x16x64_i8 v[88:91], v[4:7], v[52:55], v[108:111]
	v_mfma_i32_16x16x64_i8 v[108:111], v[0:3], v[48:51], v[88:91]
	v_mfma_i32_16x16x64_i8 v[88:91], v[16:19], v[44:47], v[96:99]
	v_mfma_i32_16x16x64_i8 v[96:99], v[8:11], v[40:43], v[88:91]
	v_mfma_i32_16x16x64_i8 v[88:91], v[4:7], v[44:47], v[92:95]
	v_mfma_i32_16x16x64_i8 v[76:79], v[16:19], v[36:39], v[76:79]
	v_mfma_i32_16x16x64_i8 v[72:75], v[4:7], v[36:39], v[72:75]
	v_mfma_i32_16x16x64_i8 v[92:95], v[0:3], v[40:43], v[88:91]
	v_mfma_i32_16x16x64_i8 v[76:79], v[8:11], v[32:35], v[76:79]
	v_mfma_i32_16x16x64_i8 v[72:75], v[0:3], v[32:35], v[72:75]
	v_mfma_i32_16x16x64_i8 v[88:91], v[28:31], v[60:63], v[120:123]
	v_mfma_i32_16x16x64_i8 v[120:123], v[24:27], v[56:59], v[88:91]
	v_mfma_i32_16x16x64_i8 v[88:91], v[20:23], v[60:63], v[116:119]
	v_mfma_i32_16x16x64_i8 v[116:119], v[12:15], v[56:59], v[88:91]
	v_mfma_i32_16x16x64_i8 v[88:91], v[28:31], v[52:55], v[104:107]
	v_mfma_i32_16x16x64_i8 v[104:107], v[24:27], v[48:51], v[88:91]
	v_mfma_i32_16x16x64_i8 v[88:91], v[20:23], v[52:55], v[100:103]
	v_mfma_i32_16x16x64_i8 v[84:87], v[28:31], v[44:47], v[84:87]
	v_mfma_i32_16x16x64_i8 v[80:83], v[20:23], v[44:47], v[80:83]
	v_mfma_i32_16x16x64_i8 v[68:71], v[28:31], v[36:39], v[68:71]
	v_mfma_i32_16x16x64_i8 v[64:67], v[20:23], v[36:39], v[64:67]
	v_mfma_i32_16x16x64_i8 v[100:103], v[12:15], v[48:51], v[88:91]
	v_mfma_i32_16x16x64_i8 v[84:87], v[24:27], v[40:43], v[84:87]
	v_mfma_i32_16x16x64_i8 v[80:83], v[12:15], v[40:43], v[80:83]
	v_mfma_i32_16x16x64_i8 v[68:71], v[24:27], v[32:35], v[68:71]
	v_mfma_i32_16x16x64_i8 v[64:67], v[12:15], v[32:35], v[64:67]
	s_barrier
	s_add_i32 s37, s37, 2
	s_add_u32 s79, s79, 0x100
	s_addc_u32 s80, s80, 0
	s_cmp_gt_u32 s37, 13
	s_cbranch_scc1 .LBB0_935
	s_mov_b64 s[46:47], s[42:43]
	s_branch .LBB0_931

.LBB0_1108:
	s_ashr_i32 s23, s22, 31
	s_lshl_b64 s[24:25], s[22:23], 20
	s_add_u32 s24, s42, s24
	s_addc_u32 s25, s43, s25
	s_and_b64 s[26:27], s[4:5], exec
	ds_read_b128 v[0:3], v143
	ds_read_b128 v[4:7], v143 offset:1024
	ds_read_b128 v[8:11], v143 offset:2048
	s_waitcnt vmcnt(2)
	ds_read_b128 v[12:15], v143 offset:3072
	s_waitcnt vmcnt(1)
	ds_read_b128 v[16:19], v144
	s_waitcnt vmcnt(0)
	ds_read_b128 v[20:23], v144 offset:1024
	ds_read_b128 v[24:27], v144 offset:2048
	ds_read_b128 v[28:31], v144 offset:3072
	s_cselect_b32 s23, s25, s31
	s_cselect_b32 s51, s24, s30
	s_ashr_i32 s21, s20, 31
	s_lshl_b64 s[26:27], s[20:21], 20
	s_add_u32 s26, s44, s26
	s_addc_u32 s27, s45, s27
	s_and_b64 s[36:37], s[4:5], exec
	s_cselect_b32 s21, s27, s35
	s_cselect_b32 s52, s26, s34
	s_add_u32 s40, s30, 0x100
	s_addc_u32 s41, s31, 0
	s_add_u32 s54, s34, 0x100
	s_addc_u32 s55, s35, 0
	s_add_u32 s36, s30, 0x180
	s_addc_u32 s37, s31, 0
	ds_read_b128 v[32:35], v145
	ds_read_b128 v[36:39], v145 offset:1024
	ds_read_b128 v[40:43], v145 offset:2048
	ds_read_b128 v[44:47], v145 offset:3072
	ds_read_b128 v[48:51], v145 offset:4096
	ds_read_b128 v[52:55], v145 offset:5120
	ds_read_b128 v[56:59], v145 offset:6144
	ds_read_b128 v[60:63], v145 offset:7168
	s_add_u32 s38, s34, 0x180
	s_addc_u32 s39, s35, 0
	s_add_u32 s56, s30, 0x80080
	s_addc_u32 s57, s31, 0
	s_add_i32 m0, s2, 0xc000
	s_nop 0
	global_load_lds_dwordx4 v139, s[56:57]
	s_nop 0
	s_add_i32 m0, s2, 0xe000
	s_nop 0
	global_load_lds_dwordx4 v141, s[56:57]
	s_waitcnt vmcnt(8)
	s_waitcnt lgkmcnt(0)
	s_barrier
	v_mfma_f32_16x16x32_bf16 v[64:67], v[0:3], v[32:35], 0
	v_mfma_f32_16x16x32_bf16 v[68:71], v[8:11], v[32:35], 0
	v_mfma_f32_16x16x32_bf16 v[76:79], v[8:11], v[40:43], 0
	v_mfma_f32_16x16x32_bf16 v[72:75], v[0:3], v[40:43], 0
	v_mfma_f32_16x16x32_bf16 v[80:83], v[0:3], v[48:51], 0
	v_mfma_f32_16x16x32_bf16 v[84:87], v[8:11], v[48:51], 0
	v_mfma_f32_16x16x32_bf16 v[92:95], v[8:11], v[56:59], 0
	v_mfma_f32_16x16x32_bf16 v[88:91], v[0:3], v[56:59], 0
	v_mfma_f32_16x16x32_bf16 v[64:67], v[4:7], v[36:39], v[64:67]
	v_mfma_f32_16x16x32_bf16 v[68:71], v[12:15], v[36:39], v[68:71]
	v_mfma_f32_16x16x32_bf16 v[76:79], v[12:15], v[44:47], v[76:79]
	v_mfma_f32_16x16x32_bf16 v[72:75], v[4:7], v[44:47], v[72:75]
	v_mfma_f32_16x16x32_bf16 v[80:83], v[4:7], v[52:55], v[80:83]
	v_mfma_f32_16x16x32_bf16 v[84:87], v[12:15], v[52:55], v[84:87]
	v_mfma_f32_16x16x32_bf16 v[96:99], v[12:15], v[60:63], v[92:95]
	v_mfma_f32_16x16x32_bf16 v[88:91], v[4:7], v[60:63], v[88:91]
	v_mfma_f32_16x16x32_bf16 v[92:95], v[16:19], v[32:35], 0
	v_mfma_f32_16x16x32_bf16 v[32:35], v[24:27], v[32:35], 0
	v_mfma_f32_16x16x32_bf16 v[104:107], v[20:23], v[36:39], v[92:95]
	v_mfma_f32_16x16x32_bf16 v[32:35], v[28:31], v[36:39], v[32:35]
	v_mfma_f32_16x16x32_bf16 v[36:39], v[16:19], v[40:43], 0
	v_mfma_f32_16x16x32_bf16 v[40:43], v[24:27], v[40:43], 0
	v_mfma_f32_16x16x32_bf16 v[36:39], v[20:23], v[44:47], v[36:39]
	v_mfma_f32_16x16x32_bf16 v[40:43], v[28:31], v[44:47], v[40:43]
	v_mfma_f32_16x16x32_bf16 v[44:47], v[16:19], v[48:51], 0
	v_mfma_f32_16x16x32_bf16 v[48:51], v[24:27], v[48:51], 0
	v_mfma_f32_16x16x32_bf16 v[44:47], v[20:23], v[52:55], v[44:47]
	v_mfma_f32_16x16x32_bf16 v[48:51], v[28:31], v[52:55], v[48:51]
	v_mfma_f32_16x16x32_bf16 v[52:55], v[16:19], v[56:59], 0
	v_mfma_f32_16x16x32_bf16 v[56:59], v[24:27], v[56:59], 0
	v_mfma_f32_16x16x32_bf16 v[52:55], v[20:23], v[60:63], v[52:55]
	v_mfma_f32_16x16x32_bf16 v[60:63], v[28:31], v[60:63], v[56:59]
	s_barrier
	s_nop 3
	ds_read_b128 v[56:59], v145 offset:16384
	ds_read_b128 v[92:95], v145 offset:17408
	ds_read_b128 v[100:103], v145 offset:18432
	ds_read_b128 v[108:111], v145 offset:19456
	ds_read_b128 v[112:115], v145 offset:20480
	ds_read_b128 v[116:119], v145 offset:21504
	ds_read_b128 v[120:123], v145 offset:22528
	ds_read_b128 v[124:127], v145 offset:23552
	s_add_i32 m0, s2, 0x10000
	s_nop 0
	global_load_lds_dwordx4 v140, s[54:55]
	s_nop 0
	s_add_i32 m0, s2, 0x12000
	s_nop 0
	global_load_lds_dwordx4 v142, s[54:55]
	s_add_u32 s54, s34, 0x80100
	s_addc_u32 s55, s35, 0
	s_add_i32 m0, s2, 0x14000
	s_nop 0
	global_load_lds_dwordx4 v140, s[54:55]
	s_nop 0
	s_add_i32 m0, s2, 0x16000
	s_nop 0
	global_load_lds_dwordx4 v142, s[54:55]
	s_nop 0
	s_add_i32 m0, s2, 0
	s_nop 0
	global_load_lds_dwordx4 v139, s[40:41]
	s_nop 0
	s_add_i32 m0, s2, 0x2000
	s_nop 0
	global_load_lds_dwordx4 v141, s[40:41]
	s_waitcnt vmcnt(8)
	s_waitcnt lgkmcnt(0)
	s_barrier
	v_mfma_f32_16x16x32_bf16 v[132:135], v[0:3], v[56:59], 0
	v_mfma_f32_16x16x32_bf16 v[152:155], v[0:3], v[100:103], 0
	v_mfma_f32_16x16x32_bf16 v[160:163], v[0:3], v[112:115], 0
	v_mfma_f32_16x16x32_bf16 v[0:3], v[0:3], v[120:123], 0
	v_mfma_f32_16x16x32_bf16 v[132:135], v[4:7], v[92:95], v[132:135]
	v_mfma_f32_16x16x32_bf16 v[152:155], v[4:7], v[108:111], v[152:155]
	v_mfma_f32_16x16x32_bf16 v[160:163], v[4:7], v[116:119], v[160:163]
	v_mfma_f32_16x16x32_bf16 v[0:3], v[4:7], v[124:127], v[0:3]
	v_mfma_f32_16x16x32_bf16 v[4:7], v[8:11], v[120:123], 0
	v_mfma_f32_16x16x32_bf16 v[148:151], v[8:11], v[56:59], 0
	v_mfma_f32_16x16x32_bf16 v[156:159], v[8:11], v[100:103], 0
	v_mfma_f32_16x16x32_bf16 v[164:167], v[8:11], v[112:115], 0
	v_mfma_f32_16x16x32_bf16 v[4:7], v[12:15], v[124:127], v[4:7]
	v_mfma_f32_16x16x32_bf16 v[148:151], v[12:15], v[92:95], v[148:151]
	v_mfma_f32_16x16x32_bf16 v[156:159], v[12:15], v[108:111], v[156:159]
	v_mfma_f32_16x16x32_bf16 v[164:167], v[12:15], v[116:119], v[164:167]
	v_mfma_f32_16x16x32_bf16 v[12:15], v[24:27], v[56:59], 0
	v_mfma_f32_16x16x32_bf16 v[168:171], v[28:31], v[92:95], v[12:15]
	v_mfma_f32_16x16x32_bf16 v[12:15], v[16:19], v[100:103], 0
	v_mfma_f32_16x16x32_bf16 v[172:175], v[20:23], v[108:111], v[12:15]
	v_mfma_f32_16x16x32_bf16 v[12:15], v[24:27], v[100:103], 0
	v_mfma_f32_16x16x32_bf16 v[176:179], v[28:31], v[108:111], v[12:15]
	v_mfma_f32_16x16x32_bf16 v[12:15], v[16:19], v[112:115], 0
	v_mfma_f32_16x16x32_bf16 v[180:183], v[20:23], v[116:119], v[12:15]
	v_mfma_f32_16x16x32_bf16 v[12:15], v[24:27], v[112:115], 0
	v_mfma_f32_16x16x32_bf16 v[8:11], v[16:19], v[56:59], 0
	v_mfma_f32_16x16x32_bf16 v[184:187], v[28:31], v[116:119], v[12:15]
	v_mfma_f32_16x16x32_bf16 v[12:15], v[16:19], v[120:123], 0
	v_mfma_f32_16x16x32_bf16 v[8:11], v[20:23], v[92:95], v[8:11]
	v_mfma_f32_16x16x32_bf16 v[188:191], v[20:23], v[124:127], v[12:15]
	v_mfma_f32_16x16x32_bf16 v[12:15], v[24:27], v[120:123], 0
	v_mfma_f32_16x16x32_bf16 v[192:195], v[28:31], v[124:127], v[12:15]
	s_barrier
	s_nop 4
	ds_read_b128 v[12:15], v146
	ds_read_b128 v[16:19], v146 offset:1024
	ds_read_b128 v[24:27], v146 offset:2048
	ds_read_b128 v[196:199], v146 offset:3072
	ds_read_b128 v[200:203], v147
	ds_read_b128 v[204:207], v147 offset:1024
	ds_read_b128 v[208:211], v147 offset:2048
	ds_read_b128 v[212:215], v147 offset:3072
	ds_read_b128 v[20:23], v145 offset:32768
	ds_read_b128 v[28:31], v145 offset:33792
	ds_read_b128 v[216:219], v145 offset:34816
	ds_read_b128 v[220:223], v145 offset:35840
	ds_read_b128 v[224:227], v145 offset:36864
	ds_read_b128 v[228:231], v145 offset:37888
	ds_read_b128 v[232:235], v145 offset:38912
	ds_read_b128 v[236:239], v145 offset:39936
	s_add_u32 s40, s30, 0x80100
	s_addc_u32 s41, s31, 0
	s_add_i32 m0, s2, 0x4000
	s_nop 0
	global_load_lds_dwordx4 v139, s[40:41]
	s_nop 0
	s_add_i32 m0, s2, 0x6000
	s_nop 0
	global_load_lds_dwordx4 v141, s[40:41]
	s_waitcnt vmcnt(8)
	s_waitcnt lgkmcnt(0)
	s_barrier
	v_mfma_f32_16x16x32_bf16 v[56:59], v[12:15], v[20:23], v[64:67]
	v_mfma_f32_16x16x32_bf16 v[116:119], v[16:19], v[28:31], v[56:59]
	v_mfma_f32_16x16x32_bf16 v[56:59], v[24:27], v[20:23], v[68:71]
	v_mfma_f32_16x16x32_bf16 v[112:115], v[196:199], v[28:31], v[56:59]
	v_mfma_f32_16x16x32_bf16 v[56:59], v[12:15], v[216:219], v[72:75]
	v_mfma_f32_16x16x32_bf16 v[108:111], v[16:19], v[220:223], v[56:59]
	v_mfma_f32_16x16x32_bf16 v[56:59], v[24:27], v[216:219], v[76:79]
	v_mfma_f32_16x16x32_bf16 v[100:103], v[196:199], v[220:223], v[56:59]
	v_mfma_f32_16x16x32_bf16 v[56:59], v[12:15], v[224:227], v[80:83]
	v_mfma_f32_16x16x32_bf16 v[92:95], v[16:19], v[228:231], v[56:59]
	v_mfma_f32_16x16x32_bf16 v[56:59], v[24:27], v[224:227], v[84:87]
	v_mfma_f32_16x16x32_bf16 v[84:87], v[196:199], v[228:231], v[56:59]
	v_mfma_f32_16x16x32_bf16 v[56:59], v[12:15], v[232:235], v[88:91]
	v_mfma_f32_16x16x32_bf16 v[72:75], v[16:19], v[236:239], v[56:59]
	v_mfma_f32_16x16x32_bf16 v[56:59], v[24:27], v[232:235], v[96:99]
	v_mfma_f32_16x16x32_bf16 v[56:59], v[196:199], v[236:239], v[56:59]
	v_mfma_f32_16x16x32_bf16 v[64:67], v[200:203], v[20:23], v[104:107]
	v_mfma_f32_16x16x32_bf16 v[20:23], v[208:211], v[20:23], v[32:35]
	v_mfma_f32_16x16x32_bf16 v[120:123], v[212:215], v[28:31], v[20:23]
	v_mfma_f32_16x16x32_bf16 v[20:23], v[200:203], v[216:219], v[36:39]
	v_mfma_f32_16x16x32_bf16 v[104:107], v[204:207], v[220:223], v[20:23]
	v_mfma_f32_16x16x32_bf16 v[20:23], v[208:211], v[216:219], v[40:43]
	v_mfma_f32_16x16x32_bf16 v[96:99], v[212:215], v[220:223], v[20:23]
	v_mfma_f32_16x16x32_bf16 v[20:23], v[200:203], v[224:227], v[44:47]
	v_mfma_f32_16x16x32_bf16 v[88:91], v[204:207], v[228:231], v[20:23]
	v_mfma_f32_16x16x32_bf16 v[20:23], v[208:211], v[224:227], v[48:51]
	v_mfma_f32_16x16x32_bf16 v[80:83], v[212:215], v[228:231], v[20:23]
	v_mfma_f32_16x16x32_bf16 v[20:23], v[200:203], v[232:235], v[52:55]
	v_mfma_f32_16x16x32_bf16 v[124:127], v[204:207], v[28:31], v[64:67]
	v_mfma_f32_16x16x32_bf16 v[64:67], v[204:207], v[236:239], v[20:23]
	v_mfma_f32_16x16x32_bf16 v[20:23], v[208:211], v[232:235], v[60:63]
	v_mfma_f32_16x16x32_bf16 v[48:51], v[212:215], v[236:239], v[20:23]
	s_barrier
	ds_read_b128 v[32:35], v145 offset:49152
	ds_read_b128 v[40:43], v145 offset:50176
	ds_read_b128 v[216:219], v145 offset:51200
	ds_read_b128 v[220:223], v145 offset:52224
	ds_read_b128 v[224:227], v145 offset:53248
	ds_read_b128 v[228:231], v145 offset:54272
	ds_read_b128 v[232:235], v145 offset:55296
	ds_read_b128 v[236:239], v145 offset:56320
	s_add_i32 m0, s2, 0x18000
	s_nop 0
	global_load_lds_dwordx4 v140, s[38:39]
	s_nop 0
	s_add_i32 m0, s2, 0x1a000
	s_nop 0
	global_load_lds_dwordx4 v142, s[38:39]
	s_add_u32 s38, s34, 0x80180
	s_addc_u32 s39, s35, 0
	s_add_i32 m0, s2, 0x1c000
	s_nop 0
	global_load_lds_dwordx4 v140, s[38:39]
	s_nop 0
	s_add_i32 m0, s2, 0x1e000
	s_nop 0
	global_load_lds_dwordx4 v142, s[38:39]
	s_nop 0
	s_add_i32 m0, s2, 0x8000
	s_nop 0
	global_load_lds_dwordx4 v139, s[36:37]
	s_nop 0
	s_add_i32 m0, s2, 0xa000
	s_nop 0
	global_load_lds_dwordx4 v141, s[36:37]
	s_waitcnt vmcnt(8)
	s_waitcnt lgkmcnt(0)
	s_barrier
	v_mfma_f32_16x16x32_bf16 v[20:23], v[12:15], v[32:35], v[132:135]
	v_mfma_f32_16x16x32_bf16 v[76:79], v[16:19], v[40:43], v[20:23]
	v_mfma_f32_16x16x32_bf16 v[20:23], v[24:27], v[32:35], v[148:151]
	v_mfma_f32_16x16x32_bf16 v[60:63], v[196:199], v[40:43], v[20:23]
	v_mfma_f32_16x16x32_bf16 v[20:23], v[12:15], v[216:219], v[152:155]
	v_mfma_f32_16x16x32_bf16 v[44:47], v[16:19], v[220:223], v[20:23]
	v_mfma_f32_16x16x32_bf16 v[20:23], v[24:27], v[216:219], v[156:159]
	v_mfma_f32_16x16x32_bf16 v[36:39], v[196:199], v[220:223], v[20:23]
	v_mfma_f32_16x16x32_bf16 v[20:23], v[12:15], v[224:227], v[160:163]
	v_mfma_f32_16x16x32_bf16 v[0:3], v[12:15], v[232:235], v[0:3]
	v_mfma_f32_16x16x32_bf16 v[28:31], v[16:19], v[228:231], v[20:23]
	v_mfma_f32_16x16x32_bf16 v[20:23], v[24:27], v[224:227], v[164:167]
	v_mfma_f32_16x16x32_bf16 v[12:15], v[16:19], v[236:239], v[0:3]
	v_mfma_f32_16x16x32_bf16 v[0:3], v[24:27], v[232:235], v[4:7]
	v_mfma_f32_16x16x32_bf16 v[20:23], v[196:199], v[228:231], v[20:23]
	v_mfma_f32_16x16x32_bf16 v[4:7], v[196:199], v[236:239], v[0:3]
	v_mfma_f32_16x16x32_bf16 v[0:3], v[200:203], v[32:35], v[8:11]
	v_mfma_f32_16x16x32_bf16 v[68:71], v[204:207], v[40:43], v[0:3]
	v_mfma_f32_16x16x32_bf16 v[0:3], v[208:211], v[32:35], v[168:171]
	v_mfma_f32_16x16x32_bf16 v[52:55], v[212:215], v[40:43], v[0:3]
	v_mfma_f32_16x16x32_bf16 v[0:3], v[200:203], v[216:219], v[172:175]
	v_mfma_f32_16x16x32_bf16 v[40:43], v[204:207], v[220:223], v[0:3]
	v_mfma_f32_16x16x32_bf16 v[0:3], v[208:211], v[216:219], v[176:179]
	v_mfma_f32_16x16x32_bf16 v[32:35], v[212:215], v[220:223], v[0:3]
	v_mfma_f32_16x16x32_bf16 v[0:3], v[200:203], v[224:227], v[180:183]
	v_mfma_f32_16x16x32_bf16 v[24:27], v[204:207], v[228:231], v[0:3]
	v_mfma_f32_16x16x32_bf16 v[0:3], v[208:211], v[224:227], v[184:187]
	v_mfma_f32_16x16x32_bf16 v[16:19], v[212:215], v[228:231], v[0:3]
	v_mfma_f32_16x16x32_bf16 v[0:3], v[200:203], v[232:235], v[188:191]
	v_mfma_f32_16x16x32_bf16 v[8:11], v[204:207], v[236:239], v[0:3]
	v_mfma_f32_16x16x32_bf16 v[0:3], v[208:211], v[232:235], v[192:195]
	v_mfma_f32_16x16x32_bf16 v[0:3], v[212:215], v[236:239], v[0:3]
	s_barrier
	s_add_u32 s53, s30, 0x200
	s_addc_u32 s54, s31, 0
	s_add_u32 s55, s34, 0x200
	s_addc_u32 s56, s35, 0
	s_add_u32 s30, s30, 0x80180
	s_addc_u32 s31, s31, 0
	s_mov_b32 s57, 0
.LBB0_1109:
	ds_read_b128 v[132:135], v143
	ds_read_b128 v[148:151], v143 offset:1024
	ds_read_b128 v[152:155], v143 offset:2048
	ds_read_b128 v[156:159], v143 offset:3072
	ds_read_b128 v[160:163], v144
	ds_read_b128 v[164:167], v144 offset:1024
	ds_read_b128 v[168:171], v144 offset:2048
	ds_read_b128 v[172:175], v144 offset:3072
	s_cmp_eq_u32 s57, 28
	s_cselect_b32 s40, s51, s53
	s_cselect_b32 s41, s23, s54
	s_cselect_b32 s36, s52, s55
	s_cselect_b32 s37, s21, s56
	s_add_u32 s34, s40, 0x80
	s_addc_u32 s35, s41, 0
	ds_read_b128 v[176:179], v145
	ds_read_b128 v[180:183], v145 offset:1024
	ds_read_b128 v[184:187], v145 offset:2048
	ds_read_b128 v[188:191], v145 offset:3072
	ds_read_b128 v[192:195], v145 offset:4096
	ds_read_b128 v[196:199], v145 offset:5120
	ds_read_b128 v[200:203], v145 offset:6144
	ds_read_b128 v[204:207], v145 offset:7168
	s_add_u32 s38, s36, 0x80
	s_addc_u32 s39, s37, 0
	s_add_i32 m0, s2, 0xc000
	s_nop 0
	global_load_lds_dwordx4 v139, s[30:31]
	s_nop 0
	s_add_i32 m0, s2, 0xe000
	s_nop 0
	global_load_lds_dwordx4 v141, s[30:31]
	s_waitcnt vmcnt(8)
	s_waitcnt lgkmcnt(0)
	s_barrier
	v_mfma_f32_16x16x32_bf16 v[116:119], v[132:135], v[176:179], v[116:119]
	v_mfma_f32_16x16x32_bf16 v[112:115], v[152:155], v[176:179], v[112:115]
	v_mfma_f32_16x16x32_bf16 v[100:103], v[152:155], v[184:187], v[100:103]
	v_mfma_f32_16x16x32_bf16 v[108:111], v[132:135], v[184:187], v[108:111]
	v_mfma_f32_16x16x32_bf16 v[92:95], v[132:135], v[192:195], v[92:95]
	v_mfma_f32_16x16x32_bf16 v[84:87], v[152:155], v[192:195], v[84:87]
	v_mfma_f32_16x16x32_bf16 v[56:59], v[152:155], v[200:203], v[56:59]
	v_mfma_f32_16x16x32_bf16 v[72:75], v[132:135], v[200:203], v[72:75]
	v_mfma_f32_16x16x32_bf16 v[116:119], v[148:151], v[180:183], v[116:119]
	v_mfma_f32_16x16x32_bf16 v[112:115], v[156:159], v[180:183], v[112:115]
	v_mfma_f32_16x16x32_bf16 v[100:103], v[156:159], v[188:191], v[100:103]
	v_mfma_f32_16x16x32_bf16 v[108:111], v[148:151], v[188:191], v[108:111]
	v_mfma_f32_16x16x32_bf16 v[92:95], v[148:151], v[196:199], v[92:95]
	v_mfma_f32_16x16x32_bf16 v[84:87], v[156:159], v[196:199], v[84:87]
	v_mfma_f32_16x16x32_bf16 v[56:59], v[156:159], v[204:207], v[56:59]
	v_mfma_f32_16x16x32_bf16 v[72:75], v[148:151], v[204:207], v[72:75]
	v_mfma_f32_16x16x32_bf16 v[124:127], v[160:163], v[176:179], v[124:127]
	v_mfma_f32_16x16x32_bf16 v[120:123], v[168:171], v[176:179], v[120:123]
	v_mfma_f32_16x16x32_bf16 v[96:99], v[168:171], v[184:187], v[96:99]
	v_mfma_f32_16x16x32_bf16 v[104:107], v[160:163], v[184:187], v[104:107]
	v_mfma_f32_16x16x32_bf16 v[88:91], v[160:163], v[192:195], v[88:91]
	v_mfma_f32_16x16x32_bf16 v[80:83], v[168:171], v[192:195], v[80:83]
	v_mfma_f32_16x16x32_bf16 v[48:51], v[168:171], v[200:203], v[48:51]
	v_mfma_f32_16x16x32_bf16 v[64:67], v[160:163], v[200:203], v[64:67]
	v_mfma_f32_16x16x32_bf16 v[124:127], v[164:167], v[180:183], v[124:127]
	v_mfma_f32_16x16x32_bf16 v[120:123], v[172:175], v[180:183], v[120:123]
	v_mfma_f32_16x16x32_bf16 v[96:99], v[172:175], v[188:191], v[96:99]
	v_mfma_f32_16x16x32_bf16 v[104:107], v[164:167], v[188:191], v[104:107]
	v_mfma_f32_16x16x32_bf16 v[88:91], v[164:167], v[196:199], v[88:91]
	v_mfma_f32_16x16x32_bf16 v[80:83], v[172:175], v[196:199], v[80:83]
	v_mfma_f32_16x16x32_bf16 v[48:51], v[172:175], v[204:207], v[48:51]
	v_mfma_f32_16x16x32_bf16 v[64:67], v[164:167], v[204:207], v[64:67]
	s_barrier
	ds_read_b128 v[176:179], v145 offset:16384
	ds_read_b128 v[180:183], v145 offset:17408
	ds_read_b128 v[184:187], v145 offset:18432
	ds_read_b128 v[188:191], v145 offset:19456
	ds_read_b128 v[192:195], v145 offset:20480
	ds_read_b128 v[196:199], v145 offset:21504
	ds_read_b128 v[200:203], v145 offset:22528
	ds_read_b128 v[204:207], v145 offset:23552
	s_add_i32 m0, s2, 0x10000
	s_nop 0
	global_load_lds_dwordx4 v140, s[36:37]
	s_nop 0
	s_add_i32 m0, s2, 0x12000
	s_nop 0
	global_load_lds_dwordx4 v142, s[36:37]
	s_add_u32 s58, s36, 0x80000
	s_addc_u32 s59, s37, 0
	s_add_i32 m0, s2, 0x14000
	s_nop 0
	global_load_lds_dwordx4 v140, s[58:59]
	s_nop 0
	s_add_i32 m0, s2, 0x16000
	s_nop 0
	global_load_lds_dwordx4 v142, s[58:59]
	s_nop 0
	s_add_i32 m0, s2, 0
	s_nop 0
	global_load_lds_dwordx4 v139, s[40:41]
	s_nop 0
	s_add_i32 m0, s2, 0x2000
	s_nop 0
	global_load_lds_dwordx4 v141, s[40:41]
	s_waitcnt vmcnt(8)
	s_waitcnt lgkmcnt(0)
	s_barrier
	v_mfma_f32_16x16x32_bf16 v[76:79], v[132:135], v[176:179], v[76:79]
	v_mfma_f32_16x16x32_bf16 v[60:63], v[152:155], v[176:179], v[60:63]
	v_mfma_f32_16x16x32_bf16 v[36:39], v[152:155], v[184:187], v[36:39]
	v_mfma_f32_16x16x32_bf16 v[44:47], v[132:135], v[184:187], v[44:47]
	v_mfma_f32_16x16x32_bf16 v[28:31], v[132:135], v[192:195], v[28:31]
	v_mfma_f32_16x16x32_bf16 v[20:23], v[152:155], v[192:195], v[20:23]
	v_mfma_f32_16x16x32_bf16 v[4:7], v[152:155], v[200:203], v[4:7]
	v_mfma_f32_16x16x32_bf16 v[12:15], v[132:135], v[200:203], v[12:15]
	v_mfma_f32_16x16x32_bf16 v[76:79], v[148:151], v[180:183], v[76:79]
	v_mfma_f32_16x16x32_bf16 v[60:63], v[156:159], v[180:183], v[60:63]
	v_mfma_f32_16x16x32_bf16 v[36:39], v[156:159], v[188:191], v[36:39]
	v_mfma_f32_16x16x32_bf16 v[44:47], v[148:151], v[188:191], v[44:47]
	v_mfma_f32_16x16x32_bf16 v[28:31], v[148:151], v[196:199], v[28:31]
	v_mfma_f32_16x16x32_bf16 v[20:23], v[156:159], v[196:199], v[20:23]
	v_mfma_f32_16x16x32_bf16 v[4:7], v[156:159], v[204:207], v[4:7]
	v_mfma_f32_16x16x32_bf16 v[12:15], v[148:151], v[204:207], v[12:15]
	v_mfma_f32_16x16x32_bf16 v[68:71], v[160:163], v[176:179], v[68:71]
	v_mfma_f32_16x16x32_bf16 v[52:55], v[168:171], v[176:179], v[52:55]
	v_mfma_f32_16x16x32_bf16 v[32:35], v[168:171], v[184:187], v[32:35]
	v_mfma_f32_16x16x32_bf16 v[40:43], v[160:163], v[184:187], v[40:43]
	v_mfma_f32_16x16x32_bf16 v[24:27], v[160:163], v[192:195], v[24:27]
	v_mfma_f32_16x16x32_bf16 v[16:19], v[168:171], v[192:195], v[16:19]
	v_mfma_f32_16x16x32_bf16 v[0:3], v[168:171], v[200:203], v[0:3]
	v_mfma_f32_16x16x32_bf16 v[8:11], v[160:163], v[200:203], v[8:11]
	v_mfma_f32_16x16x32_bf16 v[68:71], v[164:167], v[180:183], v[68:71]
	v_mfma_f32_16x16x32_bf16 v[52:55], v[172:175], v[180:183], v[52:55]
	v_mfma_f32_16x16x32_bf16 v[32:35], v[172:175], v[188:191], v[32:35]
	v_mfma_f32_16x16x32_bf16 v[40:43], v[164:167], v[188:191], v[40:43]
	v_mfma_f32_16x16x32_bf16 v[24:27], v[164:167], v[196:199], v[24:27]
	v_mfma_f32_16x16x32_bf16 v[16:19], v[172:175], v[196:199], v[16:19]
	v_mfma_f32_16x16x32_bf16 v[0:3], v[172:175], v[204:207], v[0:3]
	v_mfma_f32_16x16x32_bf16 v[8:11], v[164:167], v[204:207], v[8:11]
	s_barrier
	ds_read_b128 v[132:135], v146
	ds_read_b128 v[148:151], v146 offset:1024
	ds_read_b128 v[152:155], v146 offset:2048
	ds_read_b128 v[156:159], v146 offset:3072
	ds_read_b128 v[160:163], v147
	ds_read_b128 v[164:167], v147 offset:1024
	ds_read_b128 v[168:171], v147 offset:2048
	ds_read_b128 v[172:175], v147 offset:3072
	ds_read_b128 v[176:179], v145 offset:32768
	ds_read_b128 v[180:183], v145 offset:33792
	ds_read_b128 v[184:187], v145 offset:34816
	ds_read_b128 v[188:191], v145 offset:35840
	ds_read_b128 v[192:195], v145 offset:36864
	ds_read_b128 v[196:199], v145 offset:37888
	ds_read_b128 v[200:203], v145 offset:38912
	ds_read_b128 v[204:207], v145 offset:39936
	s_add_u32 s40, s40, 0x80000
	s_addc_u32 s41, s41, 0
	s_add_i32 m0, s2, 0x4000
	s_nop 0
	global_load_lds_dwordx4 v139, s[40:41]
	s_nop 0
	s_add_i32 m0, s2, 0x6000
	s_nop 0
	global_load_lds_dwordx4 v141, s[40:41]
	s_waitcnt vmcnt(8)
	s_waitcnt lgkmcnt(0)
	s_barrier
	v_mfma_f32_16x16x32_bf16 v[116:119], v[132:135], v[176:179], v[116:119]
	v_mfma_f32_16x16x32_bf16 v[112:115], v[152:155], v[176:179], v[112:115]
	v_mfma_f32_16x16x32_bf16 v[100:103], v[152:155], v[184:187], v[100:103]
	v_mfma_f32_16x16x32_bf16 v[108:111], v[132:135], v[184:187], v[108:111]
	v_mfma_f32_16x16x32_bf16 v[92:95], v[132:135], v[192:195], v[92:95]
	v_mfma_f32_16x16x32_bf16 v[84:87], v[152:155], v[192:195], v[84:87]
	v_mfma_f32_16x16x32_bf16 v[56:59], v[152:155], v[200:203], v[56:59]
	v_mfma_f32_16x16x32_bf16 v[72:75], v[132:135], v[200:203], v[72:75]
	v_mfma_f32_16x16x32_bf16 v[116:119], v[148:151], v[180:183], v[116:119]
	v_mfma_f32_16x16x32_bf16 v[112:115], v[156:159], v[180:183], v[112:115]
	v_mfma_f32_16x16x32_bf16 v[100:103], v[156:159], v[188:191], v[100:103]
	v_mfma_f32_16x16x32_bf16 v[108:111], v[148:151], v[188:191], v[108:111]
	v_mfma_f32_16x16x32_bf16 v[92:95], v[148:151], v[196:199], v[92:95]
	v_mfma_f32_16x16x32_bf16 v[84:87], v[156:159], v[196:199], v[84:87]
	v_mfma_f32_16x16x32_bf16 v[56:59], v[156:159], v[204:207], v[56:59]
	v_mfma_f32_16x16x32_bf16 v[72:75], v[148:151], v[204:207], v[72:75]
	v_mfma_f32_16x16x32_bf16 v[124:127], v[160:163], v[176:179], v[124:127]
	v_mfma_f32_16x16x32_bf16 v[120:123], v[168:171], v[176:179], v[120:123]
	v_mfma_f32_16x16x32_bf16 v[96:99], v[168:171], v[184:187], v[96:99]
	v_mfma_f32_16x16x32_bf16 v[104:107], v[160:163], v[184:187], v[104:107]
	v_mfma_f32_16x16x32_bf16 v[88:91], v[160:163], v[192:195], v[88:91]
	v_mfma_f32_16x16x32_bf16 v[80:83], v[168:171], v[192:195], v[80:83]
	v_mfma_f32_16x16x32_bf16 v[48:51], v[168:171], v[200:203], v[48:51]
	v_mfma_f32_16x16x32_bf16 v[64:67], v[160:163], v[200:203], v[64:67]
	v_mfma_f32_16x16x32_bf16 v[124:127], v[164:167], v[180:183], v[124:127]
	v_mfma_f32_16x16x32_bf16 v[120:123], v[172:175], v[180:183], v[120:123]
	v_mfma_f32_16x16x32_bf16 v[96:99], v[172:175], v[188:191], v[96:99]
	v_mfma_f32_16x16x32_bf16 v[104:107], v[164:167], v[188:191], v[104:107]
	v_mfma_f32_16x16x32_bf16 v[88:91], v[164:167], v[196:199], v[88:91]
	v_mfma_f32_16x16x32_bf16 v[80:83], v[172:175], v[196:199], v[80:83]
	v_mfma_f32_16x16x32_bf16 v[48:51], v[172:175], v[204:207], v[48:51]
	v_mfma_f32_16x16x32_bf16 v[64:67], v[164:167], v[204:207], v[64:67]
	s_barrier
	ds_read_b128 v[176:179], v145 offset:49152
	ds_read_b128 v[180:183], v145 offset:50176
	ds_read_b128 v[184:187], v145 offset:51200
	ds_read_b128 v[188:191], v145 offset:52224
	ds_read_b128 v[192:195], v145 offset:53248
	ds_read_b128 v[196:199], v145 offset:54272
	ds_read_b128 v[200:203], v145 offset:55296
	ds_read_b128 v[204:207], v145 offset:56320
	s_add_i32 m0, s2, 0x18000
	s_nop 0
	global_load_lds_dwordx4 v140, s[38:39]
	s_nop 0
	s_add_i32 m0, s2, 0x1a000
	s_nop 0
	global_load_lds_dwordx4 v142, s[38:39]
	s_add_u32 s36, s36, 0x80080
	s_addc_u32 s37, s37, 0
	s_add_i32 m0, s2, 0x1c000
	s_nop 0
	global_load_lds_dwordx4 v140, s[36:37]
	s_nop 0
	s_add_i32 m0, s2, 0x1e000
	s_nop 0
	global_load_lds_dwordx4 v142, s[36:37]
	s_nop 0
	s_add_i32 m0, s2, 0x8000
	s_nop 0
	global_load_lds_dwordx4 v139, s[34:35]
	s_nop 0
	s_add_i32 m0, s2, 0xa000
	s_nop 0
	global_load_lds_dwordx4 v141, s[34:35]
	s_waitcnt vmcnt(8)
	s_waitcnt lgkmcnt(0)
	s_barrier
	v_mfma_f32_16x16x32_bf16 v[76:79], v[132:135], v[176:179], v[76:79]
	v_mfma_f32_16x16x32_bf16 v[60:63], v[152:155], v[176:179], v[60:63]
	v_mfma_f32_16x16x32_bf16 v[36:39], v[152:155], v[184:187], v[36:39]
	v_mfma_f32_16x16x32_bf16 v[44:47], v[132:135], v[184:187], v[44:47]
	v_mfma_f32_16x16x32_bf16 v[28:31], v[132:135], v[192:195], v[28:31]
	v_mfma_f32_16x16x32_bf16 v[20:23], v[152:155], v[192:195], v[20:23]
	v_mfma_f32_16x16x32_bf16 v[4:7], v[152:155], v[200:203], v[4:7]
	v_mfma_f32_16x16x32_bf16 v[12:15], v[132:135], v[200:203], v[12:15]
	v_mfma_f32_16x16x32_bf16 v[76:79], v[148:151], v[180:183], v[76:79]
	v_mfma_f32_16x16x32_bf16 v[60:63], v[156:159], v[180:183], v[60:63]
	v_mfma_f32_16x16x32_bf16 v[36:39], v[156:159], v[188:191], v[36:39]
	v_mfma_f32_16x16x32_bf16 v[44:47], v[148:151], v[188:191], v[44:47]
	v_mfma_f32_16x16x32_bf16 v[28:31], v[148:151], v[196:199], v[28:31]
	v_mfma_f32_16x16x32_bf16 v[20:23], v[156:159], v[196:199], v[20:23]
	v_mfma_f32_16x16x32_bf16 v[4:7], v[156:159], v[204:207], v[4:7]
	v_mfma_f32_16x16x32_bf16 v[12:15], v[148:151], v[204:207], v[12:15]
	v_mfma_f32_16x16x32_bf16 v[68:71], v[160:163], v[176:179], v[68:71]
	v_mfma_f32_16x16x32_bf16 v[52:55], v[168:171], v[176:179], v[52:55]
	v_mfma_f32_16x16x32_bf16 v[32:35], v[168:171], v[184:187], v[32:35]
	v_mfma_f32_16x16x32_bf16 v[40:43], v[160:163], v[184:187], v[40:43]
	v_mfma_f32_16x16x32_bf16 v[24:27], v[160:163], v[192:195], v[24:27]
	v_mfma_f32_16x16x32_bf16 v[16:19], v[168:171], v[192:195], v[16:19]
	v_mfma_f32_16x16x32_bf16 v[0:3], v[168:171], v[200:203], v[0:3]
	v_mfma_f32_16x16x32_bf16 v[8:11], v[160:163], v[200:203], v[8:11]
	v_mfma_f32_16x16x32_bf16 v[68:71], v[164:167], v[180:183], v[68:71]
	v_mfma_f32_16x16x32_bf16 v[52:55], v[172:175], v[180:183], v[52:55]
	v_mfma_f32_16x16x32_bf16 v[32:35], v[172:175], v[188:191], v[32:35]
	v_mfma_f32_16x16x32_bf16 v[40:43], v[164:167], v[188:191], v[40:43]
	v_mfma_f32_16x16x32_bf16 v[24:27], v[164:167], v[196:199], v[24:27]
	v_mfma_f32_16x16x32_bf16 v[16:19], v[172:175], v[196:199], v[16:19]
	v_mfma_f32_16x16x32_bf16 v[0:3], v[172:175], v[204:207], v[0:3]
	v_mfma_f32_16x16x32_bf16 v[8:11], v[164:167], v[204:207], v[8:11]
	s_barrier
	s_add_i32 s57, s57, 2
	s_add_u32 s53, s53, 0x100
	s_addc_u32 s54, s54, 0
	s_add_u32 s55, s55, 0x100
	s_addc_u32 s56, s56, 0
	s_add_u32 s30, s30, 0x100
	s_addc_u32 s31, s31, 0
	s_cmp_gt_u32 s57, 29
	s_cbranch_scc0 .LBB0_1109
	s_and_b64 vcc, exec, s[10:11]
	s_cbranch_vccz .LBB0_1112
	s_barrier

.LBB0_1410:
	ds_read_b128 v[0:3], v138
	ds_read_b128 v[4:7], v138 offset:1024
	ds_read_b128 v[8:11], v138 offset:2048
	ds_read_b128 v[12:15], v138 offset:3072
	ds_read_b128 v[16:19], v139
	ds_read_b128 v[20:23], v139 offset:1024
	ds_read_b128 v[24:27], v139 offset:2048
	ds_read_b128 v[28:31], v139 offset:3072
	s_lshl_b64 s[20:21], s[16:17], 19
	s_add_u32 s20, s39, s20
	s_addc_u32 s21, s40, s21
	s_and_b64 s[6:7], exec, s[6:7]
	s_cselect_b32 s2, s21, s29
	s_cselect_b32 s15, s20, s28
	s_add_u32 s6, s28, 0x100
	s_addc_u32 s7, s29, 0
	s_add_u32 s36, s26, 0x100
	s_addc_u32 s37, s27, 0
	s_add_u32 s30, s28, 0x180
	s_addc_u32 s31, s29, 0
	ds_read_b128 v[32:35], v140
	ds_read_b128 v[36:39], v140 offset:1024
	ds_read_b128 v[40:43], v140 offset:2048
	ds_read_b128 v[44:47], v140 offset:3072
	ds_read_b128 v[48:51], v140 offset:4096
	ds_read_b128 v[52:55], v140 offset:5120
	ds_read_b128 v[56:59], v140 offset:6144
	ds_read_b128 v[60:63], v140 offset:7168
	s_add_u32 s34, s26, 0x180
	s_addc_u32 s35, s27, 0
	s_add_u32 s54, s28, 0x40080
	s_addc_u32 s55, s29, 0
	s_add_i32 m0, s47, 0xc000
	s_nop 0
	global_load_lds_dwordx4 v134, s[54:55]
	s_nop 0
	s_add_i32 m0, s47, 0xe000
	s_nop 0
	global_load_lds_dwordx4 v136, s[54:55]
	s_waitcnt vmcnt(8)
	s_waitcnt lgkmcnt(0)
	s_barrier
	v_mfma_f32_16x16x128_f8f6f4 v[64:67], v[0:7], v[32:39], 0
	v_mfma_f32_16x16x128_f8f6f4 v[68:71], v[8:15], v[32:39], 0
	v_mfma_f32_16x16x128_f8f6f4 v[76:79], v[8:15], v[40:47], 0
	v_mfma_f32_16x16x128_f8f6f4 v[72:75], v[0:7], v[40:47], 0
	v_mfma_f32_16x16x128_f8f6f4 v[80:83], v[0:7], v[48:55], 0
	v_mfma_f32_16x16x128_f8f6f4 v[88:91], v[8:15], v[48:55], 0
	v_mfma_f32_16x16x128_f8f6f4 v[104:107], v[8:15], v[56:63], 0
	v_mfma_f32_16x16x128_f8f6f4 v[92:95], v[0:7], v[56:63], 0
	v_mfma_f32_16x16x128_f8f6f4 v[108:111], v[16:23], v[32:39], 0
	v_mfma_f32_16x16x128_f8f6f4 v[124:127], v[24:31], v[32:39], 0
	v_mfma_f32_16x16x128_f8f6f4 v[166:169], v[24:31], v[40:47], 0
	v_mfma_f32_16x16x128_f8f6f4 v[162:165], v[16:23], v[40:47], 0
	v_mfma_f32_16x16x128_f8f6f4 v[170:173], v[16:23], v[48:55], 0
	v_mfma_f32_16x16x128_f8f6f4 v[174:177], v[24:31], v[48:55], 0
	v_mfma_f32_16x16x128_f8f6f4 v[182:185], v[24:31], v[56:63], 0
	v_mfma_f32_16x16x128_f8f6f4 v[178:181], v[16:23], v[56:63], 0
	s_barrier
	ds_read_b128 v[32:35], v140 offset:16384
	ds_read_b128 v[36:39], v140 offset:17408
	ds_read_b128 v[40:43], v140 offset:18432
	ds_read_b128 v[44:47], v140 offset:19456
	ds_read_b128 v[48:51], v140 offset:20480
	ds_read_b128 v[52:55], v140 offset:21504
	ds_read_b128 v[56:59], v140 offset:22528
	ds_read_b128 v[60:63], v140 offset:23552
	s_add_i32 m0, s47, 0x10000
	s_nop 0
	global_load_lds_dwordx4 v135, s[36:37]
	s_nop 0
	s_add_i32 m0, s47, 0x12000
	s_nop 0
	global_load_lds_dwordx4 v137, s[36:37]
	s_add_u32 s36, s26, 0x40100
	s_addc_u32 s37, s27, 0
	s_add_i32 m0, s47, 0x14000
	s_nop 0
	global_load_lds_dwordx4 v135, s[36:37]
	s_nop 0
	s_add_i32 m0, s47, 0x16000
	s_nop 0
	global_load_lds_dwordx4 v137, s[36:37]
	s_nop 0
	s_add_i32 m0, s47, 0
	s_nop 0
	global_load_lds_dwordx4 v134, s[6:7]
	s_nop 0
	s_add_i32 m0, s47, 0x2000
	s_nop 0
	global_load_lds_dwordx4 v136, s[6:7]
	s_waitcnt vmcnt(8)
	s_waitcnt lgkmcnt(0)
	s_barrier
	v_mfma_f32_16x16x128_f8f6f4 v[186:189], v[0:7], v[32:39], 0
	v_mfma_f32_16x16x128_f8f6f4 v[190:193], v[8:15], v[32:39], 0
	v_mfma_f32_16x16x128_f8f6f4 v[198:201], v[8:15], v[40:47], 0
	v_mfma_f32_16x16x128_f8f6f4 v[194:197], v[0:7], v[40:47], 0
	v_mfma_f32_16x16x128_f8f6f4 v[202:205], v[0:7], v[48:55], 0
	v_mfma_f32_16x16x128_f8f6f4 v[206:209], v[8:15], v[48:55], 0
	v_mfma_f32_16x16x128_f8f6f4 v[214:217], v[8:15], v[56:63], 0
	v_mfma_f32_16x16x128_f8f6f4 v[210:213], v[0:7], v[56:63], 0
	v_mfma_f32_16x16x128_f8f6f4 v[218:221], v[16:23], v[32:39], 0
	v_mfma_f32_16x16x128_f8f6f4 v[222:225], v[24:31], v[32:39], 0
	v_mfma_f32_16x16x128_f8f6f4 v[230:233], v[24:31], v[40:47], 0
	v_mfma_f32_16x16x128_f8f6f4 v[226:229], v[16:23], v[40:47], 0
	v_mfma_f32_16x16x128_f8f6f4 v[234:237], v[16:23], v[48:55], 0
	v_mfma_f32_16x16x128_f8f6f4 v[238:241], v[24:31], v[48:55], 0
	v_mfma_f32_16x16x128_f8f6f4 v[246:249], v[24:31], v[56:63], 0
	v_mfma_f32_16x16x128_f8f6f4 v[242:245], v[16:23], v[56:63], 0
	s_barrier
	ds_read_b128 v[0:3], v141
	ds_read_b128 v[4:7], v141 offset:1024
	ds_read_b128 v[8:11], v141 offset:2048
	ds_read_b128 v[12:15], v141 offset:3072
	ds_read_b128 v[146:149], v142
	ds_read_b128 v[150:153], v142 offset:1024
	ds_read_b128 v[154:157], v142 offset:2048
	ds_read_b128 v[158:161], v142 offset:3072
	ds_read_b128 v[16:19], v140 offset:32768
	ds_read_b128 v[20:23], v140 offset:33792
	ds_read_b128 v[24:27], v140 offset:34816
	ds_read_b128 v[28:31], v140 offset:35840
	ds_read_b128 v[32:35], v140 offset:36864
	ds_read_b128 v[36:39], v140 offset:37888
	ds_read_b128 v[40:43], v140 offset:38912
	ds_read_b128 v[44:47], v140 offset:39936
	s_add_u32 s28, s28, 0x40100
	s_addc_u32 s29, s29, 0
	s_add_i32 m0, s47, 0x4000
	s_nop 0
	global_load_lds_dwordx4 v134, s[28:29]
	s_nop 0
	s_add_i32 m0, s47, 0x6000
	s_nop 0
	global_load_lds_dwordx4 v136, s[28:29]
	s_waitcnt vmcnt(8)
	s_waitcnt lgkmcnt(0)
	s_barrier
	v_mfma_f32_16x16x128_f8f6f4 v[112:115], v[0:7], v[16:23], v[64:67]
	v_mfma_f32_16x16x128_f8f6f4 v[116:119], v[8:15], v[16:23], v[68:71]
	v_mfma_f32_16x16x128_f8f6f4 v[100:103], v[0:7], v[24:31], v[72:75]
	v_mfma_f32_16x16x128_f8f6f4 v[96:99], v[8:15], v[24:31], v[76:79]
	v_mfma_f32_16x16x128_f8f6f4 v[84:87], v[0:7], v[32:39], v[80:83]
	v_mfma_f32_16x16x128_f8f6f4 v[80:83], v[8:15], v[32:39], v[88:91]
	v_mfma_f32_16x16x128_f8f6f4 v[60:63], v[0:7], v[40:47], v[92:95]
	v_mfma_f32_16x16x128_f8f6f4 v[56:59], v[8:15], v[40:47], v[104:107]
	v_mfma_f32_16x16x128_f8f6f4 v[120:123], v[146:153], v[16:23], v[108:111]
	v_mfma_f32_16x16x128_f8f6f4 v[124:127], v[154:161], v[16:23], v[124:127]
	v_mfma_f32_16x16x128_f8f6f4 v[108:111], v[146:153], v[24:31], v[162:165]
	v_mfma_f32_16x16x128_f8f6f4 v[104:107], v[154:161], v[24:31], v[166:169]
	v_mfma_f32_16x16x128_f8f6f4 v[92:95], v[146:153], v[32:39], v[170:173]
	v_mfma_f32_16x16x128_f8f6f4 v[88:91], v[154:161], v[32:39], v[174:177]
	v_mfma_f32_16x16x128_f8f6f4 v[76:79], v[146:153], v[40:47], v[178:181]
	v_mfma_f32_16x16x128_f8f6f4 v[72:75], v[154:161], v[40:47], v[182:185]
	s_barrier
	ds_read_b128 v[24:27], v140 offset:49152
	ds_read_b128 v[28:31], v140 offset:50176
	ds_read_b128 v[162:165], v140 offset:51200
	ds_read_b128 v[166:169], v140 offset:52224
	ds_read_b128 v[170:173], v140 offset:53248
	ds_read_b128 v[174:177], v140 offset:54272
	ds_read_b128 v[178:181], v140 offset:55296
	ds_read_b128 v[182:185], v140 offset:56320
	s_add_i32 m0, s47, 0x18000
	s_nop 0
	global_load_lds_dwordx4 v135, s[34:35]
	s_nop 0
	s_add_i32 m0, s47, 0x1a000
	s_nop 0
	global_load_lds_dwordx4 v137, s[34:35]
	s_add_u32 s28, s26, 0x40180
	s_addc_u32 s29, s27, 0
	s_add_i32 m0, s47, 0x1c000
	s_nop 0
	global_load_lds_dwordx4 v135, s[28:29]
	s_nop 0
	s_add_i32 m0, s47, 0x1e000
	s_nop 0
	global_load_lds_dwordx4 v137, s[28:29]
	s_nop 0
	s_add_i32 m0, s47, 0x8000
	s_nop 0
	global_load_lds_dwordx4 v134, s[30:31]
	s_nop 0
	s_add_i32 m0, s47, 0xa000
	s_nop 0
	global_load_lds_dwordx4 v136, s[30:31]
	s_waitcnt vmcnt(8)
	s_waitcnt lgkmcnt(0)
	s_barrier
	v_mfma_f32_16x16x128_f8f6f4 v[52:55], v[0:7], v[24:31], v[186:189]
	v_mfma_f32_16x16x128_f8f6f4 v[48:51], v[8:15], v[24:31], v[190:193]
	v_mfma_f32_16x16x128_f8f6f4 v[36:39], v[0:7], v[162:169], v[194:197]
	v_mfma_f32_16x16x128_f8f6f4 v[32:35], v[8:15], v[162:169], v[198:201]
	v_mfma_f32_16x16x128_f8f6f4 v[20:23], v[0:7], v[170:177], v[202:205]
	v_mfma_f32_16x16x128_f8f6f4 v[16:19], v[8:15], v[170:177], v[206:209]
	v_mfma_f32_16x16x128_f8f6f4 v[4:7], v[0:7], v[178:185], v[210:213]
	v_mfma_f32_16x16x128_f8f6f4 v[0:3], v[8:15], v[178:185], v[214:217]
	v_mfma_f32_16x16x128_f8f6f4 v[68:71], v[146:153], v[24:31], v[218:221]
	v_mfma_f32_16x16x128_f8f6f4 v[64:67], v[154:161], v[24:31], v[222:225]
	v_mfma_f32_16x16x128_f8f6f4 v[44:47], v[146:153], v[162:169], v[226:229]
	v_mfma_f32_16x16x128_f8f6f4 v[40:43], v[154:161], v[162:169], v[230:233]
	v_mfma_f32_16x16x128_f8f6f4 v[28:31], v[146:153], v[170:177], v[234:237]
	v_mfma_f32_16x16x128_f8f6f4 v[24:27], v[154:161], v[170:177], v[238:241]
	v_mfma_f32_16x16x128_f8f6f4 v[12:15], v[146:153], v[178:185], v[242:245]
	v_mfma_f32_16x16x128_f8f6f4 v[8:11], v[154:161], v[178:185], v[246:249]
	s_barrier
	s_add_u32 s17, s26, 0x200
	s_addc_u32 s54, s27, 0
	s_mov_b32 s55, 0
.LBB0_1411:
	ds_read_b128 v[146:149], v138
	ds_read_b128 v[150:153], v138 offset:1024
	ds_read_b128 v[154:157], v138 offset:2048
	ds_read_b128 v[158:161], v138 offset:3072
	ds_read_b128 v[162:165], v139
	ds_read_b128 v[166:169], v139 offset:1024
	ds_read_b128 v[170:173], v139 offset:2048
	ds_read_b128 v[174:177], v139 offset:3072
	s_add_u32 s26, s6, 0x100
	s_addc_u32 s27, s7, 0
	s_cmp_eq_u32 s55, 12
	s_cselect_b32 s36, s15, s26
	s_cselect_b32 s37, s2, s27
	s_cselect_b32 s30, s18, s17
	s_cselect_b32 s31, s19, s54
	s_add_u32 s28, s36, 0x80
	s_addc_u32 s29, s37, 0
	ds_read_b128 v[178:181], v140
	ds_read_b128 v[182:185], v140 offset:1024
	ds_read_b128 v[186:189], v140 offset:2048
	ds_read_b128 v[190:193], v140 offset:3072
	ds_read_b128 v[194:197], v140 offset:4096
	ds_read_b128 v[198:201], v140 offset:5120
	ds_read_b128 v[202:205], v140 offset:6144
	ds_read_b128 v[206:209], v140 offset:7168
	s_add_u32 s34, s30, 0x80
	s_addc_u32 s35, s31, 0
	s_add_u32 s6, s6, 0x40080
	s_addc_u32 s7, s7, 0
	s_add_i32 m0, s47, 0xc000
	s_nop 0
	global_load_lds_dwordx4 v134, s[6:7]
	s_nop 0
	s_add_i32 m0, s47, 0xe000
	s_nop 0
	global_load_lds_dwordx4 v136, s[6:7]
	s_waitcnt vmcnt(8)
	s_waitcnt lgkmcnt(0)
	s_barrier
	v_mfma_f32_16x16x128_f8f6f4 v[112:115], v[146:153], v[178:185], v[112:115]
	v_mfma_f32_16x16x128_f8f6f4 v[116:119], v[154:161], v[178:185], v[116:119]
	v_mfma_f32_16x16x128_f8f6f4 v[96:99], v[154:161], v[186:193], v[96:99]
	v_mfma_f32_16x16x128_f8f6f4 v[100:103], v[146:153], v[186:193], v[100:103]
	v_mfma_f32_16x16x128_f8f6f4 v[210:213], v[146:153], v[194:201], v[84:87]
	v_mfma_f32_16x16x128_f8f6f4 v[214:217], v[154:161], v[194:201], v[80:83]
	v_mfma_f32_16x16x128_f8f6f4 v[222:225], v[154:161], v[202:209], v[56:59]
	v_mfma_f32_16x16x128_f8f6f4 v[218:221], v[146:153], v[202:209], v[60:63]
	v_mfma_f32_16x16x128_f8f6f4 v[120:123], v[162:169], v[178:185], v[120:123]
	v_mfma_f32_16x16x128_f8f6f4 v[124:127], v[170:177], v[178:185], v[124:127]
	v_mfma_f32_16x16x128_f8f6f4 v[108:111], v[162:169], v[186:193], v[108:111]
	v_mfma_f32_16x16x128_f8f6f4 v[104:107], v[170:177], v[186:193], v[104:107]
	v_mfma_f32_16x16x128_f8f6f4 v[178:181], v[162:169], v[194:201], v[92:95]
	v_mfma_f32_16x16x128_f8f6f4 v[182:185], v[170:177], v[194:201], v[88:91]
	v_mfma_f32_16x16x128_f8f6f4 v[186:189], v[162:169], v[202:209], v[76:79]
	v_mfma_f32_16x16x128_f8f6f4 v[190:193], v[170:177], v[202:209], v[72:75]
	s_barrier
	ds_read_b128 v[56:59], v140 offset:16384
	ds_read_b128 v[60:63], v140 offset:17408
	s_nop 2
	ds_read_b128 v[72:75], v140 offset:18432
	ds_read_b128 v[76:79], v140 offset:19456
	ds_read_b128 v[80:83], v140 offset:20480
	ds_read_b128 v[84:87], v140 offset:21504
	ds_read_b128 v[88:91], v140 offset:22528
	ds_read_b128 v[92:95], v140 offset:23552
	s_add_i32 m0, s47, 0x10000
	s_nop 0
	global_load_lds_dwordx4 v135, s[30:31]
	s_nop 0
	s_add_i32 m0, s47, 0x12000
	s_nop 0
	global_load_lds_dwordx4 v137, s[30:31]
	s_add_u32 s6, s30, 0x40000
	s_addc_u32 s7, s31, 0
	s_add_i32 m0, s47, 0x14000
	s_nop 0
	global_load_lds_dwordx4 v135, s[6:7]
	s_nop 0
	s_add_i32 m0, s47, 0x16000
	s_nop 0
	global_load_lds_dwordx4 v137, s[6:7]
	s_nop 0
	s_add_i32 m0, s47, 0
	s_nop 0
	global_load_lds_dwordx4 v134, s[36:37]
	s_nop 0
	s_add_i32 m0, s47, 0x2000
	s_nop 0
	global_load_lds_dwordx4 v136, s[36:37]
	s_waitcnt vmcnt(8)
	s_waitcnt lgkmcnt(0)
	s_barrier
	v_mfma_f32_16x16x128_f8f6f4 v[52:55], v[146:153], v[56:63], v[52:55]
	v_mfma_f32_16x16x128_f8f6f4 v[48:51], v[154:161], v[56:63], v[48:51]
	v_mfma_f32_16x16x128_f8f6f4 v[198:201], v[154:161], v[72:79], v[32:35]
	v_mfma_f32_16x16x128_f8f6f4 v[194:197], v[146:153], v[72:79], v[36:39]
	v_mfma_f32_16x16x128_f8f6f4 v[202:205], v[146:153], v[80:87], v[20:23]
	v_mfma_f32_16x16x128_f8f6f4 v[206:209], v[154:161], v[80:87], v[16:19]
	v_mfma_f32_16x16x128_f8f6f4 v[230:233], v[154:161], v[88:95], v[0:3]
	v_mfma_f32_16x16x128_f8f6f4 v[226:229], v[146:153], v[88:95], v[4:7]
	v_mfma_f32_16x16x128_f8f6f4 v[68:71], v[162:169], v[56:63], v[68:71]
	v_mfma_f32_16x16x128_f8f6f4 v[64:67], v[170:177], v[56:63], v[64:67]
	v_mfma_f32_16x16x128_f8f6f4 v[238:241], v[170:177], v[72:79], v[40:43]
	v_mfma_f32_16x16x128_f8f6f4 v[234:237], v[162:169], v[72:79], v[44:47]
	v_mfma_f32_16x16x128_f8f6f4 v[242:245], v[162:169], v[80:87], v[28:31]
	v_mfma_f32_16x16x128_f8f6f4 v[246:249], v[170:177], v[80:87], v[24:27]
	v_mfma_f32_16x16x128_f8f6f4 v[130:133], v[170:177], v[88:95], v[8:11]
	v_mfma_f32_16x16x128_f8f6f4 v[250:253], v[162:169], v[88:95], v[12:15]
	s_barrier
	ds_read_b128 v[0:3], v141
	ds_read_b128 v[4:7], v141 offset:1024
	s_nop 2
	ds_read_b128 v[8:11], v141 offset:2048
	ds_read_b128 v[12:15], v141 offset:3072
	ds_read_b128 v[146:149], v142
	ds_read_b128 v[150:153], v142 offset:1024
	ds_read_b128 v[154:157], v142 offset:2048
	ds_read_b128 v[158:161], v142 offset:3072
	ds_read_b128 v[16:19], v140 offset:32768
	ds_read_b128 v[20:23], v140 offset:33792
	ds_read_b128 v[24:27], v140 offset:34816
	ds_read_b128 v[28:31], v140 offset:35840
	ds_read_b128 v[32:35], v140 offset:36864
	ds_read_b128 v[36:39], v140 offset:37888
	ds_read_b128 v[40:43], v140 offset:38912
	ds_read_b128 v[44:47], v140 offset:39936
	s_add_u32 s6, s36, 0x40000
	s_addc_u32 s7, s37, 0
	s_add_i32 m0, s47, 0x4000
	s_nop 0
	global_load_lds_dwordx4 v134, s[6:7]
	s_nop 0
	s_add_i32 m0, s47, 0x6000
	s_nop 0
	global_load_lds_dwordx4 v136, s[6:7]
	s_waitcnt vmcnt(8)
	s_waitcnt lgkmcnt(0)
	s_barrier
	v_mfma_f32_16x16x128_f8f6f4 v[112:115], v[0:7], v[16:23], v[112:115]
	v_mfma_f32_16x16x128_f8f6f4 v[116:119], v[8:15], v[16:23], v[116:119]
	v_mfma_f32_16x16x128_f8f6f4 v[96:99], v[8:15], v[24:31], v[96:99]
	v_mfma_f32_16x16x128_f8f6f4 v[100:103], v[0:7], v[24:31], v[100:103]
	v_mfma_f32_16x16x128_f8f6f4 v[84:87], v[0:7], v[32:39], v[210:213]
	v_mfma_f32_16x16x128_f8f6f4 v[80:83], v[8:15], v[32:39], v[214:217]
	v_mfma_f32_16x16x128_f8f6f4 v[56:59], v[8:15], v[40:47], v[222:225]
	v_mfma_f32_16x16x128_f8f6f4 v[60:63], v[0:7], v[40:47], v[218:221]
	v_mfma_f32_16x16x128_f8f6f4 v[120:123], v[146:153], v[16:23], v[120:123]
	v_mfma_f32_16x16x128_f8f6f4 v[124:127], v[154:161], v[16:23], v[124:127]
	v_mfma_f32_16x16x128_f8f6f4 v[104:107], v[154:161], v[24:31], v[104:107]
	v_mfma_f32_16x16x128_f8f6f4 v[108:111], v[146:153], v[24:31], v[108:111]
	v_mfma_f32_16x16x128_f8f6f4 v[92:95], v[146:153], v[32:39], v[178:181]
	v_mfma_f32_16x16x128_f8f6f4 v[88:91], v[154:161], v[32:39], v[182:185]
	v_mfma_f32_16x16x128_f8f6f4 v[72:75], v[154:161], v[40:47], v[190:193]
	v_mfma_f32_16x16x128_f8f6f4 v[76:79], v[146:153], v[40:47], v[186:189]
	s_barrier
	ds_read_b128 v[24:27], v140 offset:49152
	ds_read_b128 v[28:31], v140 offset:50176
	ds_read_b128 v[162:165], v140 offset:51200
	ds_read_b128 v[166:169], v140 offset:52224
	ds_read_b128 v[170:173], v140 offset:53248
	ds_read_b128 v[174:177], v140 offset:54272
	ds_read_b128 v[178:181], v140 offset:55296
	ds_read_b128 v[182:185], v140 offset:56320
	s_add_i32 m0, s47, 0x18000
	s_nop 0
	global_load_lds_dwordx4 v135, s[34:35]
	s_nop 0
	s_add_i32 m0, s47, 0x1a000
	s_nop 0
	global_load_lds_dwordx4 v137, s[34:35]
	s_add_u32 s6, s30, 0x40080
	s_addc_u32 s7, s31, 0
	s_add_i32 m0, s47, 0x1c000
	s_nop 0
	global_load_lds_dwordx4 v135, s[6:7]
	s_nop 0
	s_add_i32 m0, s47, 0x1e000
	s_nop 0
	global_load_lds_dwordx4 v137, s[6:7]
	s_nop 0
	s_add_i32 m0, s47, 0x8000
	s_nop 0
	global_load_lds_dwordx4 v134, s[28:29]
	s_nop 0
	s_add_i32 m0, s47, 0xa000
	s_nop 0
	global_load_lds_dwordx4 v136, s[28:29]
	s_waitcnt vmcnt(8)
	s_waitcnt lgkmcnt(0)
	s_barrier
	v_mfma_f32_16x16x128_f8f6f4 v[52:55], v[0:7], v[24:31], v[52:55]
	v_mfma_f32_16x16x128_f8f6f4 v[48:51], v[8:15], v[24:31], v[48:51]
	v_mfma_f32_16x16x128_f8f6f4 v[36:39], v[0:7], v[162:169], v[194:197]
	v_mfma_f32_16x16x128_f8f6f4 v[32:35], v[8:15], v[162:169], v[198:201]
	v_mfma_f32_16x16x128_f8f6f4 v[20:23], v[0:7], v[170:177], v[202:205]
	v_mfma_f32_16x16x128_f8f6f4 v[16:19], v[8:15], v[170:177], v[206:209]
	v_mfma_f32_16x16x128_f8f6f4 v[4:7], v[0:7], v[178:185], v[226:229]
	v_mfma_f32_16x16x128_f8f6f4 v[0:3], v[8:15], v[178:185], v[230:233]
	v_mfma_f32_16x16x128_f8f6f4 v[68:71], v[146:153], v[24:31], v[68:71]
	v_mfma_f32_16x16x128_f8f6f4 v[64:67], v[154:161], v[24:31], v[64:67]
	v_mfma_f32_16x16x128_f8f6f4 v[44:47], v[146:153], v[162:169], v[234:237]
	v_mfma_f32_16x16x128_f8f6f4 v[40:43], v[154:161], v[162:169], v[238:241]
	v_mfma_f32_16x16x128_f8f6f4 v[28:31], v[146:153], v[170:177], v[242:245]
	v_mfma_f32_16x16x128_f8f6f4 v[24:27], v[154:161], v[170:177], v[246:249]
	v_mfma_f32_16x16x128_f8f6f4 v[12:15], v[146:153], v[178:185], v[250:253]
	v_mfma_f32_16x16x128_f8f6f4 v[8:11], v[154:161], v[178:185], v[130:133]
	s_barrier
	s_add_i32 s55, s55, 2
	s_add_u32 s17, s17, 0x100
	s_addc_u32 s54, s54, 0
	s_cmp_gt_u32 s55, 13
	s_mov_b64 s[6:7], s[26:27]
	s_cbranch_scc0 .LBB0_1411
	s_and_b64 vcc, exec, s[12:13]
	s_cbranch_vccz .LBB0_1414
	s_barrier

.LBB0_1487:
	ds_read_b128 v[0:3], v153
	ds_read_b128 v[4:7], v153 offset:1024
	ds_read_b128 v[8:11], v153 offset:2048
	ds_read_b128 v[12:15], v153 offset:3072
	ds_read_b128 v[16:19], v154
	ds_read_b128 v[20:23], v154 offset:1024
	ds_read_b128 v[24:27], v154 offset:2048
	ds_read_b128 v[28:31], v154 offset:3072
	s_add_u32 s26, s28, 0x100
	s_addc_u32 s27, s29, 0
	s_add_u32 s36, s24, 0x100
	s_addc_u32 s37, s25, 0
	s_add_u32 s30, s28, 0x180
	s_addc_u32 s31, s29, 0
	ds_read_b128 v[32:35], v155
	ds_read_b128 v[36:39], v155 offset:1024
	ds_read_b128 v[40:43], v155 offset:2048
	ds_read_b128 v[44:47], v155 offset:3072
	ds_read_b128 v[48:51], v155 offset:4096
	ds_read_b128 v[52:55], v155 offset:5120
	ds_read_b128 v[56:59], v155 offset:6144
	ds_read_b128 v[60:63], v155 offset:7168
	s_add_u32 s34, s24, 0x180
	s_addc_u32 s35, s25, 0
	s_add_u32 s52, s28, 0xe0080
	s_addc_u32 s53, s29, 0
	s_add_i32 m0, s44, 0xc000
	s_nop 0
	global_load_lds_dwordx4 v149, s[52:53]
	s_nop 0
	s_add_i32 m0, s44, 0xe000
	s_nop 0
	global_load_lds_dwordx4 v151, s[52:53]
	s_waitcnt vmcnt(8)
	s_waitcnt lgkmcnt(0)
	s_barrier
	v_mfma_f32_16x16x128_f8f6f4 v[64:67], v[0:7], v[32:39], 0
	v_mfma_f32_16x16x128_f8f6f4 v[68:71], v[8:15], v[32:39], 0
	v_mfma_f32_16x16x128_f8f6f4 v[76:79], v[8:15], v[40:47], 0
	v_mfma_f32_16x16x128_f8f6f4 v[72:75], v[0:7], v[40:47], 0
	v_mfma_f32_16x16x128_f8f6f4 v[80:83], v[0:7], v[48:55], 0
	v_mfma_f32_16x16x128_f8f6f4 v[88:91], v[8:15], v[48:55], 0
	v_mfma_f32_16x16x128_f8f6f4 v[104:107], v[8:15], v[56:63], 0
	v_mfma_f32_16x16x128_f8f6f4 v[92:95], v[0:7], v[56:63], 0
	v_mfma_f32_16x16x128_f8f6f4 v[108:111], v[16:23], v[32:39], 0
	v_mfma_f32_16x16x128_f8f6f4 v[124:127], v[24:31], v[32:39], 0
	v_mfma_f32_16x16x128_f8f6f4 v[162:165], v[24:31], v[40:47], 0
	v_mfma_f32_16x16x128_f8f6f4 v[158:161], v[16:23], v[40:47], 0
	v_mfma_f32_16x16x128_f8f6f4 v[166:169], v[16:23], v[48:55], 0
	v_mfma_f32_16x16x128_f8f6f4 v[170:173], v[24:31], v[48:55], 0
	v_mfma_f32_16x16x128_f8f6f4 v[178:181], v[24:31], v[56:63], 0
	v_mfma_f32_16x16x128_f8f6f4 v[174:177], v[16:23], v[56:63], 0
	s_barrier
	ds_read_b128 v[32:35], v155 offset:16384
	ds_read_b128 v[36:39], v155 offset:17408
	ds_read_b128 v[40:43], v155 offset:18432
	ds_read_b128 v[44:47], v155 offset:19456
	ds_read_b128 v[48:51], v155 offset:20480
	ds_read_b128 v[52:55], v155 offset:21504
	ds_read_b128 v[56:59], v155 offset:22528
	ds_read_b128 v[60:63], v155 offset:23552
	s_add_i32 m0, s44, 0x10000
	s_nop 0
	global_load_lds_dwordx4 v150, s[36:37]
	s_nop 0
	s_add_i32 m0, s44, 0x12000
	s_nop 0
	global_load_lds_dwordx4 v152, s[36:37]
	s_add_u32 s36, s24, 0xe0100
	s_addc_u32 s37, s25, 0
	s_add_i32 m0, s44, 0x14000
	s_nop 0
	global_load_lds_dwordx4 v150, s[36:37]
	s_nop 0
	s_add_i32 m0, s44, 0x16000
	s_nop 0
	global_load_lds_dwordx4 v152, s[36:37]
	s_nop 0
	s_add_i32 m0, s44, 0
	s_nop 0
	global_load_lds_dwordx4 v149, s[26:27]
	s_nop 0
	s_add_i32 m0, s44, 0x2000
	s_nop 0
	global_load_lds_dwordx4 v151, s[26:27]
	s_waitcnt vmcnt(8)
	s_waitcnt lgkmcnt(0)
	s_barrier
	v_mfma_f32_16x16x128_f8f6f4 v[190:193], v[0:7], v[32:39], 0
	v_mfma_f32_16x16x128_f8f6f4 v[194:197], v[8:15], v[32:39], 0
	v_mfma_f32_16x16x128_f8f6f4 v[202:205], v[8:15], v[40:47], 0
	v_mfma_f32_16x16x128_f8f6f4 v[198:201], v[0:7], v[40:47], 0
	v_mfma_f32_16x16x128_f8f6f4 v[206:209], v[0:7], v[48:55], 0
	v_mfma_f32_16x16x128_f8f6f4 v[210:213], v[8:15], v[48:55], 0
	v_mfma_f32_16x16x128_f8f6f4 v[218:221], v[8:15], v[56:63], 0
	v_mfma_f32_16x16x128_f8f6f4 v[214:217], v[0:7], v[56:63], 0
	v_mfma_f32_16x16x128_f8f6f4 v[222:225], v[16:23], v[32:39], 0
	v_mfma_f32_16x16x128_f8f6f4 v[226:229], v[24:31], v[32:39], 0
	v_mfma_f32_16x16x128_f8f6f4 v[234:237], v[24:31], v[40:47], 0
	v_mfma_f32_16x16x128_f8f6f4 v[230:233], v[16:23], v[40:47], 0
	v_mfma_f32_16x16x128_f8f6f4 v[238:241], v[16:23], v[48:55], 0
	v_mfma_f32_16x16x128_f8f6f4 v[242:245], v[24:31], v[48:55], 0
	v_mfma_f32_16x16x128_f8f6f4 v[250:253], v[24:31], v[56:63], 0
	v_mfma_f32_16x16x128_f8f6f4 v[246:249], v[16:23], v[56:63], 0
	s_barrier
	ds_read_b128 v[0:3], v156
	ds_read_b128 v[4:7], v156 offset:1024
	ds_read_b128 v[16:19], v156 offset:2048
	ds_read_b128 v[20:23], v156 offset:3072
	ds_read_b128 v[132:135], v157
	ds_read_b128 v[136:139], v157 offset:1024
	ds_read_b128 v[140:143], v157 offset:2048
	ds_read_b128 v[144:147], v157 offset:3072
	ds_read_b128 v[8:11], v155 offset:32768
	ds_read_b128 v[12:15], v155 offset:33792
	ds_read_b128 v[24:27], v155 offset:34816
	ds_read_b128 v[28:31], v155 offset:35840
	ds_read_b128 v[32:35], v155 offset:36864
	ds_read_b128 v[36:39], v155 offset:37888
	ds_read_b128 v[40:43], v155 offset:38912
	ds_read_b128 v[44:47], v155 offset:39936
	s_add_u32 s28, s28, 0xe0100
	s_addc_u32 s29, s29, 0
	s_add_i32 m0, s44, 0x4000
	s_nop 0
	global_load_lds_dwordx4 v149, s[28:29]
	s_nop 0
	s_add_i32 m0, s44, 0x6000
	s_nop 0
	global_load_lds_dwordx4 v151, s[28:29]
	s_waitcnt vmcnt(8)
	s_waitcnt lgkmcnt(0)
	s_barrier
	v_mfma_f32_16x16x128_f8f6f4 v[112:115], v[0:7], v[8:15], v[64:67]
	v_mfma_f32_16x16x128_f8f6f4 v[116:119], v[16:23], v[8:15], v[68:71]
	v_mfma_f32_16x16x128_f8f6f4 v[100:103], v[0:7], v[24:31], v[72:75]
	v_mfma_f32_16x16x128_f8f6f4 v[96:99], v[16:23], v[24:31], v[76:79]
	v_mfma_f32_16x16x128_f8f6f4 v[84:87], v[0:7], v[32:39], v[80:83]
	v_mfma_f32_16x16x128_f8f6f4 v[80:83], v[16:23], v[32:39], v[88:91]
	v_mfma_f32_16x16x128_f8f6f4 v[60:63], v[0:7], v[40:47], v[92:95]
	v_mfma_f32_16x16x128_f8f6f4 v[52:55], v[16:23], v[40:47], v[104:107]
	v_mfma_f32_16x16x128_f8f6f4 v[120:123], v[132:139], v[8:15], v[108:111]
	v_mfma_f32_16x16x128_f8f6f4 v[124:127], v[140:147], v[8:15], v[124:127]
	v_mfma_f32_16x16x128_f8f6f4 v[108:111], v[132:139], v[24:31], v[158:161]
	v_mfma_f32_16x16x128_f8f6f4 v[104:107], v[140:147], v[24:31], v[162:165]
	v_mfma_f32_16x16x128_f8f6f4 v[92:95], v[132:139], v[32:39], v[166:169]
	v_mfma_f32_16x16x128_f8f6f4 v[88:91], v[140:147], v[32:39], v[170:173]
	v_mfma_f32_16x16x128_f8f6f4 v[56:59], v[132:139], v[40:47], v[174:177]
	v_mfma_f32_16x16x128_f8f6f4 v[48:51], v[140:147], v[40:47], v[178:181]
	s_barrier
	ds_read_b128 v[158:161], v155 offset:49152
	ds_read_b128 v[162:165], v155 offset:50176
	ds_read_b128 v[166:169], v155 offset:51200
	ds_read_b128 v[170:173], v155 offset:52224
	ds_read_b128 v[174:177], v155 offset:53248
	ds_read_b128 v[178:181], v155 offset:54272
	ds_read_b128 v[182:185], v155 offset:55296
	ds_read_b128 v[186:189], v155 offset:56320
	s_add_i32 m0, s44, 0x18000
	s_nop 0
	global_load_lds_dwordx4 v150, s[34:35]
	s_nop 0
	s_add_i32 m0, s44, 0x1a000
	s_nop 0
	global_load_lds_dwordx4 v152, s[34:35]
	s_add_u32 s28, s24, 0xe0180
	s_addc_u32 s29, s25, 0
	s_add_i32 m0, s44, 0x1c000
	s_nop 0
	global_load_lds_dwordx4 v150, s[28:29]
	s_nop 0
	s_add_i32 m0, s44, 0x1e000
	s_nop 0
	global_load_lds_dwordx4 v152, s[28:29]
	s_nop 0
	s_add_i32 m0, s44, 0x8000
	s_nop 0
	global_load_lds_dwordx4 v149, s[30:31]
	s_nop 0
	s_add_i32 m0, s44, 0xa000
	s_nop 0
	global_load_lds_dwordx4 v151, s[30:31]
	s_waitcnt vmcnt(8)
	s_waitcnt lgkmcnt(0)
	s_barrier
	v_mfma_f32_16x16x128_f8f6f4 v[68:71], v[0:7], v[158:165], v[190:193]
	v_mfma_f32_16x16x128_f8f6f4 v[64:67], v[16:23], v[158:165], v[194:197]
	v_mfma_f32_16x16x128_f8f6f4 v[36:39], v[16:23], v[166:173], v[202:205]
	v_mfma_f32_16x16x128_f8f6f4 v[44:47], v[0:7], v[166:173], v[198:201]
	v_mfma_f32_16x16x128_f8f6f4 v[28:31], v[0:7], v[174:181], v[206:209]
	v_mfma_f32_16x16x128_f8f6f4 v[24:27], v[16:23], v[174:181], v[210:213]
	v_mfma_f32_16x16x128_f8f6f4 v[8:11], v[16:23], v[182:189], v[218:221]
	v_mfma_f32_16x16x128_f8f6f4 v[12:15], v[0:7], v[182:189], v[214:217]
	v_mfma_f32_16x16x128_f8f6f4 v[76:79], v[132:139], v[158:165], v[222:225]
	v_mfma_f32_16x16x128_f8f6f4 v[72:75], v[140:147], v[158:165], v[226:229]
	v_mfma_f32_16x16x128_f8f6f4 v[32:35], v[140:147], v[166:173], v[234:237]
	v_mfma_f32_16x16x128_f8f6f4 v[40:43], v[132:139], v[166:173], v[230:233]
	v_mfma_f32_16x16x128_f8f6f4 v[20:23], v[132:139], v[174:181], v[238:241]
	v_mfma_f32_16x16x128_f8f6f4 v[16:19], v[140:147], v[174:181], v[242:245]
	v_mfma_f32_16x16x128_f8f6f4 v[0:3], v[140:147], v[182:189], v[250:253]
	v_mfma_f32_16x16x128_f8f6f4 v[4:7], v[132:139], v[182:189], v[246:249]
	s_barrier
	s_add_u32 s23, s24, 0x200
	s_addc_u32 s51, s25, 0
	s_mov_b32 s52, 0
.LBB0_1488:
	ds_read_b128 v[132:135], v153
	ds_read_b128 v[136:139], v153 offset:1024
	ds_read_b128 v[140:143], v153 offset:2048
	ds_read_b128 v[144:147], v153 offset:3072
	ds_read_b128 v[158:161], v154
	ds_read_b128 v[162:165], v154 offset:1024
	ds_read_b128 v[166:169], v154 offset:2048
	ds_read_b128 v[170:173], v154 offset:3072
	s_add_u32 s24, s26, 0x100
	s_addc_u32 s25, s27, 0
	s_cmp_eq_u32 s52, 52
	s_cselect_b32 s36, s6, s24
	s_cselect_b32 s37, s7, s25
	s_cselect_b32 s30, s20, s23
	s_cselect_b32 s31, s21, s51
	s_add_u32 s28, s36, 0x80
	s_addc_u32 s29, s37, 0
	ds_read_b128 v[174:177], v155
	ds_read_b128 v[178:181], v155 offset:1024
	ds_read_b128 v[182:185], v155 offset:2048
	ds_read_b128 v[186:189], v155 offset:3072
	ds_read_b128 v[190:193], v155 offset:4096
	ds_read_b128 v[194:197], v155 offset:5120
	ds_read_b128 v[198:201], v155 offset:6144
	ds_read_b128 v[202:205], v155 offset:7168
	s_add_u32 s34, s30, 0x80
	s_addc_u32 s35, s31, 0
	s_add_u32 s26, s26, 0xe0080
	s_addc_u32 s27, s27, 0
	s_add_i32 m0, s44, 0xc000
	s_nop 0
	global_load_lds_dwordx4 v149, s[26:27]
	s_nop 0
	s_add_i32 m0, s44, 0xe000
	s_nop 0
	global_load_lds_dwordx4 v151, s[26:27]
	s_waitcnt vmcnt(8)
	s_waitcnt lgkmcnt(0)
	s_barrier
	v_mfma_f32_16x16x128_f8f6f4 v[112:115], v[132:139], v[174:181], v[112:115]
	v_mfma_f32_16x16x128_f8f6f4 v[116:119], v[140:147], v[174:181], v[116:119]
	v_mfma_f32_16x16x128_f8f6f4 v[96:99], v[140:147], v[182:189], v[96:99]
	v_mfma_f32_16x16x128_f8f6f4 v[100:103], v[132:139], v[182:189], v[100:103]
	v_mfma_f32_16x16x128_f8f6f4 v[206:209], v[132:139], v[190:197], v[84:87]
	v_mfma_f32_16x16x128_f8f6f4 v[210:213], v[140:147], v[190:197], v[80:83]
	v_mfma_f32_16x16x128_f8f6f4 v[218:221], v[140:147], v[198:205], v[52:55]
	v_mfma_f32_16x16x128_f8f6f4 v[214:217], v[132:139], v[198:205], v[60:63]
	v_mfma_f32_16x16x128_f8f6f4 v[120:123], v[158:165], v[174:181], v[120:123]
	v_mfma_f32_16x16x128_f8f6f4 v[124:127], v[166:173], v[174:181], v[124:127]
	v_mfma_f32_16x16x128_f8f6f4 v[108:111], v[158:165], v[182:189], v[108:111]
	v_mfma_f32_16x16x128_f8f6f4 v[104:107], v[166:173], v[182:189], v[104:107]
	v_mfma_f32_16x16x128_f8f6f4 v[174:177], v[158:165], v[190:197], v[92:95]
	v_mfma_f32_16x16x128_f8f6f4 v[178:181], v[166:173], v[190:197], v[88:91]
	v_mfma_f32_16x16x128_f8f6f4 v[182:185], v[158:165], v[198:205], v[56:59]
	v_mfma_f32_16x16x128_f8f6f4 v[186:189], v[166:173], v[198:205], v[48:51]
	s_barrier
	s_nop 4
	ds_read_b128 v[48:51], v155 offset:16384
	ds_read_b128 v[52:55], v155 offset:17408
	ds_read_b128 v[56:59], v155 offset:18432
	ds_read_b128 v[60:63], v155 offset:19456
	ds_read_b128 v[80:83], v155 offset:20480
	ds_read_b128 v[84:87], v155 offset:21504
	ds_read_b128 v[88:91], v155 offset:22528
	ds_read_b128 v[92:95], v155 offset:23552
	s_add_i32 m0, s44, 0x10000
	s_nop 0
	global_load_lds_dwordx4 v150, s[30:31]
	s_nop 0
	s_add_i32 m0, s44, 0x12000
	s_nop 0
	global_load_lds_dwordx4 v152, s[30:31]
	s_add_u32 s26, s30, 0xe0000
	s_addc_u32 s27, s31, 0
	s_add_i32 m0, s44, 0x14000
	s_nop 0
	global_load_lds_dwordx4 v150, s[26:27]
	s_nop 0
	s_add_i32 m0, s44, 0x16000
	s_nop 0
	global_load_lds_dwordx4 v152, s[26:27]
	s_nop 0
	s_add_i32 m0, s44, 0
	s_nop 0
	global_load_lds_dwordx4 v149, s[36:37]
	s_nop 0
	s_add_i32 m0, s44, 0x2000
	s_nop 0
	global_load_lds_dwordx4 v151, s[36:37]
	s_waitcnt vmcnt(8)
	s_waitcnt lgkmcnt(0)
	s_barrier
	v_mfma_f32_16x16x128_f8f6f4 v[68:71], v[132:139], v[48:55], v[68:71]
	v_mfma_f32_16x16x128_f8f6f4 v[64:67], v[140:147], v[48:55], v[64:67]
	v_mfma_f32_16x16x128_f8f6f4 v[194:197], v[140:147], v[56:63], v[36:39]
	v_mfma_f32_16x16x128_f8f6f4 v[190:193], v[132:139], v[56:63], v[44:47]
	v_mfma_f32_16x16x128_f8f6f4 v[198:201], v[132:139], v[80:87], v[28:31]
	v_mfma_f32_16x16x128_f8f6f4 v[202:205], v[140:147], v[80:87], v[24:27]
	v_mfma_f32_16x16x128_f8f6f4 v[226:229], v[140:147], v[88:95], v[8:11]
	v_mfma_f32_16x16x128_f8f6f4 v[222:225], v[132:139], v[88:95], v[12:15]
	v_mfma_f32_16x16x128_f8f6f4 v[76:79], v[158:165], v[48:55], v[76:79]
	v_mfma_f32_16x16x128_f8f6f4 v[72:75], v[166:173], v[48:55], v[72:75]
	v_mfma_f32_16x16x128_f8f6f4 v[234:237], v[166:173], v[56:63], v[32:35]
	v_mfma_f32_16x16x128_f8f6f4 v[230:233], v[158:165], v[56:63], v[40:43]
	v_mfma_f32_16x16x128_f8f6f4 v[238:241], v[158:165], v[80:87], v[20:23]
	v_mfma_f32_16x16x128_f8f6f4 v[242:245], v[166:173], v[80:87], v[16:19]
	v_mfma_f32_16x16x128_f8f6f4 v[250:253], v[166:173], v[88:95], v[0:3]
	v_mfma_f32_16x16x128_f8f6f4 v[246:249], v[158:165], v[88:95], v[4:7]
	s_barrier
	s_nop 4
	ds_read_b128 v[0:3], v156
	ds_read_b128 v[4:7], v156 offset:1024
	ds_read_b128 v[16:19], v156 offset:2048
	ds_read_b128 v[20:23], v156 offset:3072
	ds_read_b128 v[132:135], v157
	ds_read_b128 v[136:139], v157 offset:1024
	ds_read_b128 v[140:143], v157 offset:2048
	ds_read_b128 v[144:147], v157 offset:3072
	ds_read_b128 v[8:11], v155 offset:32768
	ds_read_b128 v[12:15], v155 offset:33792
	ds_read_b128 v[24:27], v155 offset:34816
	ds_read_b128 v[28:31], v155 offset:35840
	ds_read_b128 v[32:35], v155 offset:36864
	ds_read_b128 v[36:39], v155 offset:37888
	ds_read_b128 v[40:43], v155 offset:38912
	ds_read_b128 v[44:47], v155 offset:39936
	s_add_u32 s26, s36, 0xe0000
	s_addc_u32 s27, s37, 0
	s_add_i32 m0, s44, 0x4000
	s_nop 0
	global_load_lds_dwordx4 v149, s[26:27]
	s_nop 0
	s_add_i32 m0, s44, 0x6000
	s_nop 0
	global_load_lds_dwordx4 v151, s[26:27]
	s_waitcnt vmcnt(8)
	s_waitcnt lgkmcnt(0)
	s_barrier
	v_mfma_f32_16x16x128_f8f6f4 v[112:115], v[0:7], v[8:15], v[112:115]
	v_mfma_f32_16x16x128_f8f6f4 v[116:119], v[16:23], v[8:15], v[116:119]
	v_mfma_f32_16x16x128_f8f6f4 v[96:99], v[16:23], v[24:31], v[96:99]
	v_mfma_f32_16x16x128_f8f6f4 v[100:103], v[0:7], v[24:31], v[100:103]
	v_mfma_f32_16x16x128_f8f6f4 v[84:87], v[0:7], v[32:39], v[206:209]
	v_mfma_f32_16x16x128_f8f6f4 v[80:83], v[16:23], v[32:39], v[210:213]
	v_mfma_f32_16x16x128_f8f6f4 v[52:55], v[16:23], v[40:47], v[218:221]
	v_mfma_f32_16x16x128_f8f6f4 v[60:63], v[0:7], v[40:47], v[214:217]
	v_mfma_f32_16x16x128_f8f6f4 v[120:123], v[132:139], v[8:15], v[120:123]
	v_mfma_f32_16x16x128_f8f6f4 v[124:127], v[140:147], v[8:15], v[124:127]
	v_mfma_f32_16x16x128_f8f6f4 v[104:107], v[140:147], v[24:31], v[104:107]
	v_mfma_f32_16x16x128_f8f6f4 v[108:111], v[132:139], v[24:31], v[108:111]
	v_mfma_f32_16x16x128_f8f6f4 v[92:95], v[132:139], v[32:39], v[174:177]
	v_mfma_f32_16x16x128_f8f6f4 v[88:91], v[140:147], v[32:39], v[178:181]
	v_mfma_f32_16x16x128_f8f6f4 v[48:51], v[140:147], v[40:47], v[186:189]
	v_mfma_f32_16x16x128_f8f6f4 v[56:59], v[132:139], v[40:47], v[182:185]
	s_barrier
	ds_read_b128 v[158:161], v155 offset:49152
	ds_read_b128 v[162:165], v155 offset:50176
	ds_read_b128 v[166:169], v155 offset:51200
	ds_read_b128 v[170:173], v155 offset:52224
	ds_read_b128 v[174:177], v155 offset:53248
	ds_read_b128 v[178:181], v155 offset:54272
	ds_read_b128 v[182:185], v155 offset:55296
	ds_read_b128 v[186:189], v155 offset:56320
	s_add_i32 m0, s44, 0x18000
	s_nop 0
	global_load_lds_dwordx4 v150, s[34:35]
	s_nop 0
	s_add_i32 m0, s44, 0x1a000
	s_nop 0
	global_load_lds_dwordx4 v152, s[34:35]
	s_add_u32 s26, s30, 0xe0080
	s_addc_u32 s27, s31, 0
	s_add_i32 m0, s44, 0x1c000
	s_nop 0
	global_load_lds_dwordx4 v150, s[26:27]
	s_nop 0
	s_add_i32 m0, s44, 0x1e000
	s_nop 0
	global_load_lds_dwordx4 v152, s[26:27]
	s_nop 0
	s_add_i32 m0, s44, 0x8000
	s_nop 0
	global_load_lds_dwordx4 v149, s[28:29]
	s_nop 0
	s_add_i32 m0, s44, 0xa000
	s_nop 0
	global_load_lds_dwordx4 v151, s[28:29]
	s_waitcnt vmcnt(8)
	s_waitcnt lgkmcnt(0)
	s_barrier
	v_mfma_f32_16x16x128_f8f6f4 v[68:71], v[0:7], v[158:165], v[68:71]
	v_mfma_f32_16x16x128_f8f6f4 v[64:67], v[16:23], v[158:165], v[64:67]
	v_mfma_f32_16x16x128_f8f6f4 v[36:39], v[16:23], v[166:173], v[194:197]
	v_mfma_f32_16x16x128_f8f6f4 v[44:47], v[0:7], v[166:173], v[190:193]
	v_mfma_f32_16x16x128_f8f6f4 v[28:31], v[0:7], v[174:181], v[198:201]
	v_mfma_f32_16x16x128_f8f6f4 v[24:27], v[16:23], v[174:181], v[202:205]
	v_mfma_f32_16x16x128_f8f6f4 v[8:11], v[16:23], v[182:189], v[226:229]
	v_mfma_f32_16x16x128_f8f6f4 v[12:15], v[0:7], v[182:189], v[222:225]
	v_mfma_f32_16x16x128_f8f6f4 v[76:79], v[132:139], v[158:165], v[76:79]
	v_mfma_f32_16x16x128_f8f6f4 v[72:75], v[140:147], v[158:165], v[72:75]
	v_mfma_f32_16x16x128_f8f6f4 v[32:35], v[140:147], v[166:173], v[234:237]
	v_mfma_f32_16x16x128_f8f6f4 v[40:43], v[132:139], v[166:173], v[230:233]
	v_mfma_f32_16x16x128_f8f6f4 v[20:23], v[132:139], v[174:181], v[238:241]
	v_mfma_f32_16x16x128_f8f6f4 v[16:19], v[140:147], v[174:181], v[242:245]
	v_mfma_f32_16x16x128_f8f6f4 v[0:3], v[140:147], v[182:189], v[250:253]
	v_mfma_f32_16x16x128_f8f6f4 v[4:7], v[132:139], v[182:189], v[246:249]
	s_barrier
	s_add_i32 s52, s52, 2
	s_add_u32 s23, s23, 0x100
	s_addc_u32 s51, s51, 0
	s_cmp_gt_u32 s52, 53
	s_mov_b64 s[26:27], s[24:25]
	s_cbranch_scc0 .LBB0_1488
	s_and_b64 vcc, exec, s[16:17]
	s_cbranch_vccz .LBB0_1491
	s_barrier
